# weight-conversion loads and stores in the B and D tails marked nt (streaming) so they do not displace the attention K/V working set in L2
# speedup vs baseline: 1.0183x; 1.0016x over previous
; #define LAS __attribute__((address_space(3)))
; __device__ __forceinline__ unsigned pk4_fp8(float x0, float x1, float x2, float x3) { int w = 0; w = __builtin_amdgcn_cvt_pk_fp8_f32(x0, x1, w, false); w = __builtin_amdgcn_cvt_pk_fp8_f32(x2, x3, w, true); return (unsigned)w; }
; __device__ __forceinline__ void transpose_item_fp8w(const float* W, int K, int N, unsigned char* WT, float q, LAS unsigned char* scr, int item, int lane) {
;     const int nblk = N / 128, kb = item / nblk, nb = item % nblk, k0 = 64 * kb, n0 = 128 * nb;
;     const int l5 = lane & 31, h = lane >> 5;
;     const float* src = W + (size_t)(k0 + 16 * h) * N + n0 + 4 * l5;
; #pragma unroll
;     for (int b = 0; b < 2; ++b) {
;         f32x4 x[16];
; #pragma unroll
;         for (int s_ = 0; s_ < 16; ++s_) x[s_] = *(const f32x4*)(src + (size_t)(32 * b + s_) * N);
; #pragma unroll
;         for (int i = 0; i < 4; ++i) {
;             u32x4 o;
;             o.x = pk4_fp8(x[0][i] * q, x[1][i] * q, x[2][i] * q, x[3][i] * q); o.y = pk4_fp8(x[4][i] * q, x[5][i] * q, x[6][i] * q, x[7][i] * q);
;             o.z = pk4_fp8(x[8][i] * q, x[9][i] * q, x[10][i] * q, x[11][i] * q); o.w = pk4_fp8(x[12][i] * q, x[13][i] * q, x[14][i] * q, x[15][i] * q);
;             *(LAS u32x4*)(scr + (l5 + 32 * i) * 80 + (2 * b + h) * 16) = o; }
.LBB0_331:
	s_cmpk_gt_i32 s5, 0x3df
	s_mov_b64 s[0:1], -1
	s_cbranch_scc0 .LBB0_359
	s_cmpk_gt_u32 s5, 0x46f
	s_cbranch_scc0 .LBB0_346
	s_cmpk_gt_u32 s5, 0x4ef
	s_cbranch_scc0 .LBB0_341
	s_cmpk_gt_u32 s5, 0x6ef
	s_cbranch_scc0 .LBB0_336
	s_add_i32 s2, s5, 0xfffff910
	v_readlane_b32 s8, v253, 32
	s_lshr_b32 s0, s2, 8
	v_readlane_b32 s9, v253, 33
	s_mov_b32 s13, s9
	s_add_i32 s12, s0, s21
	v_readlane_b32 s40, v253, 58
	s_lshl_b64 s[0:1], s[12:13], 23
	v_readlane_b32 s50, v254, 4
	v_readlane_b32 s51, v254, 5
	s_add_u32 s10, s50, s0
	s_addc_u32 s11, s51, s1
	s_lshl_b64 s[8:9], s[12:13], 21
	v_readlane_b32 s0, v246, 15
	s_add_u32 s1, s0, s8
	v_readlane_b32 s0, v246, 16
	s_addc_u32 s8, s0, s9
	s_lshl_b32 s0, s2, 6
	s_and_b32 s9, s0, 0x3c0
	v_add_u32_e32 v0, s9, v101
	s_lshl_b32 s0, s2, 3
	v_ashrrev_i32_e32 v1, 31, v0
	s_and_b32 s0, s0, 0x780
	v_lshlrev_b64 v[0:1], 13, v[0:1]
	v_lshl_add_u64 v[0:1], s[10:11], 0, v[0:1]
	s_lshl_b32 s12, s0, 2
	s_mov_b32 s3, s13
	v_readlane_b32 s41, v253, 59
	v_readlane_b32 s42, v253, 60
	v_readlane_b32 s43, v253, 61
	v_readlane_b32 s44, v253, 62
	v_readlane_b32 s45, v253, 63
	v_writelane_b32 v253, s2, 32
	v_lshl_add_u64 v[0:1], v[0:1], 0, s[12:13]
	v_lshl_add_u64 v[60:61], v[0:1], 0, v[152:153]
	v_writelane_b32 v253, s3, 33
	s_movk_i32 s2, 0x2000
	v_add_co_u32_e32 v4, vcc, s2, v60
	s_movk_i32 s2, 0x4000
	s_nop 0
	v_addc_co_u32_e32 v5, vcc, 0, v61, vcc
	v_add_co_u32_e32 v8, vcc, s2, v60
	s_movk_i32 s2, 0x6000
	s_nop 0
	v_addc_co_u32_e32 v9, vcc, 0, v61, vcc
	v_add_co_u32_e32 v12, vcc, s2, v60
	s_mov_b32 s2, 0x8000
	s_nop 0
	v_addc_co_u32_e32 v13, vcc, 0, v61, vcc
	v_add_co_u32_e32 v16, vcc, s2, v60
	s_mov_b32 s2, 0xa000
	s_nop 0
	v_addc_co_u32_e32 v17, vcc, 0, v61, vcc
	v_add_co_u32_e32 v20, vcc, s2, v60
	s_mov_b32 s2, 0xc000
	s_nop 0
	v_addc_co_u32_e32 v21, vcc, 0, v61, vcc
	v_add_co_u32_e32 v24, vcc, s2, v60
	s_mov_b32 s2, 0xe000
	s_nop 0
	v_addc_co_u32_e32 v25, vcc, 0, v61, vcc
	v_add_co_u32_e32 v28, vcc, s2, v60
	s_mov_b32 s2, 0x10000
	s_nop 0
	v_addc_co_u32_e32 v29, vcc, 0, v61, vcc
	v_add_co_u32_e32 v32, vcc, s2, v60
	s_mov_b32 s2, 0x12000
	s_nop 0
	v_addc_co_u32_e32 v33, vcc, 0, v61, vcc
	v_add_co_u32_e32 v36, vcc, s2, v60
	s_mov_b32 s2, 0x14000
	s_nop 0
	v_addc_co_u32_e32 v37, vcc, 0, v61, vcc
	v_add_co_u32_e32 v40, vcc, s2, v60
	s_mov_b32 s2, 0x16000
	s_nop 0
	v_addc_co_u32_e32 v41, vcc, 0, v61, vcc
	v_add_co_u32_e32 v44, vcc, s2, v60
	s_mov_b32 s2, 0x18000
	s_nop 0
	v_addc_co_u32_e32 v45, vcc, 0, v61, vcc
	v_add_co_u32_e32 v48, vcc, s2, v60
	global_load_dwordx4 v[0:3], v[60:61], off nt
	s_nop 0
	v_addc_co_u32_e32 v49, vcc, 0, v61, vcc
	global_load_dwordx4 v[4:7], v[4:5], off nt
	s_mov_b32 s2, 0x1a000
	global_load_dwordx4 v[12:15], v[12:13], off nt
	v_add_co_u32_e32 v52, vcc, s2, v60
	global_load_dwordx4 v[16:19], v[16:17], off nt
	s_nop 0
	v_addc_co_u32_e32 v53, vcc, 0, v61, vcc
	global_load_dwordx4 v[20:23], v[20:21], off nt
	s_mov_b32 s2, 0x1c000
	global_load_dwordx4 v[28:31], v[28:29], off nt
	v_add_co_u32_e32 v56, vcc, s2, v60
	global_load_dwordx4 v[32:35], v[32:33], off nt
	s_nop 0
	v_addc_co_u32_e32 v57, vcc, 0, v61, vcc
	global_load_dwordx4 v[36:39], v[36:37], off nt
	s_mov_b32 s2, 0x1e000
	global_load_dwordx4 v[44:47], v[44:45], off nt
	v_add_co_u32_e32 v62, vcc, s2, v60
	global_load_dwordx4 v[48:51], v[48:49], off nt
	s_nop 0
	v_addc_co_u32_e32 v63, vcc, 0, v61, vcc
	global_load_dwordx4 v[52:55], v[52:53], off nt
	v_mov_b32_e32 v120, v153
	global_load_dwordx4 v[8:11], v[8:9], off nt
	v_mov_b32_e32 v121, v153
	global_load_dwordx4 v[24:27], v[24:25], off nt
	v_mov_b32_e32 v122, v153
	global_load_dwordx4 v[40:43], v[40:41], off nt
	v_mov_b32_e32 v123, v153
	global_load_dwordx4 v[56:59], v[56:57], off nt
	s_mov_b32 s2, 0x40000
	global_load_dwordx4 v[116:119], v[62:63], off nt
	s_add_u32 s10, s1, s9
	s_addc_u32 s11, s8, 0
	v_readlane_b32 s46, v254, 0
	v_readlane_b32 s47, v254, 1
	v_readlane_b32 s48, v254, 2
	v_readlane_b32 s49, v254, 3
	v_readlane_b32 s52, v254, 6
	v_readlane_b32 s53, v254, 7
	v_readlane_b32 s54, v254, 8
	v_readlane_b32 s55, v254, 9
	s_waitcnt vmcnt(0)
	v_mul_f32_e32 v0, 0x43000000, v0
	s_waitcnt vmcnt(14)
	v_mul_f32_e32 v4, 0x43000000, v4
	v_cvt_pk_fp8_f32 v120, v0, v4
	s_waitcnt vmcnt(13)
	v_mul_f32_e32 v12, 0x43000000, v12
	s_waitcnt vmcnt(12)
	v_mul_f32_e32 v0, 0x43000000, v16
	s_waitcnt vmcnt(11)
	v_mul_f32_e32 v4, 0x43000000, v20
	v_cvt_pk_fp8_f32 v121, v0, v4
	s_waitcnt vmcnt(9)
	v_mul_f32_e32 v0, 0x43000000, v32
	s_waitcnt vmcnt(8)
	v_mul_f32_e32 v4, 0x43000000, v36
	v_cvt_pk_fp8_f32 v122, v0, v4
	s_waitcnt vmcnt(6)
	v_mul_f32_e32 v0, 0x43000000, v48
	s_waitcnt vmcnt(5)
	v_mul_f32_e32 v4, 0x43000000, v52
	v_cvt_pk_fp8_f32 v123, v0, v4
	s_waitcnt vmcnt(4)
	v_mul_f32_e32 v8, 0x43000000, v8
	v_cvt_pk_fp8_f32 v120, v8, v12 op_sel:[0,0,1]
	s_waitcnt vmcnt(3)
	v_mul_f32_e32 v8, 0x43000000, v24
	v_mul_f32_e32 v12, 0x43000000, v28
	v_cvt_pk_fp8_f32 v121, v8, v12 op_sel:[0,0,1]
	s_waitcnt vmcnt(2)
	v_mul_f32_e32 v8, 0x43000000, v40
	v_mul_f32_e32 v12, 0x43000000, v44
	v_cvt_pk_fp8_f32 v122, v8, v12 op_sel:[0,0,1]
	s_waitcnt vmcnt(1)
	v_mul_f32_e32 v8, 0x43000000, v56
	s_waitcnt vmcnt(0)
; #define LAS __attribute__((address_space(3)))
; __device__ __forceinline__ unsigned pk4_fp8(float x0, float x1, float x2, float x3) { int w = 0; w = __builtin_amdgcn_cvt_pk_fp8_f32(x0, x1, w, false); w = __builtin_amdgcn_cvt_pk_fp8_f32(x2, x3, w, true); return (unsigned)w; }
; __device__ __forceinline__ void transpose_item_fp8w(const float* W, int K, int N, unsigned char* WT, float q, LAS unsigned char* scr, int item, int lane) {
;     ...
;     for (int b = 0; b < 2; ++b) {
;         f32x4 x[16];
; #pragma unroll
;         for (int s_ = 0; s_ < 16; ++s_) x[s_] = *(const f32x4*)(src + (size_t)(32 * b + s_) * N);
; #pragma unroll
;         for (int i = 0; i < 4; ++i) {
;             u32x4 o;
;             o.x = pk4_fp8(x[0][i] * q, x[1][i] * q, x[2][i] * q, x[3][i] * q); o.y = pk4_fp8(x[4][i] * q, x[5][i] * q, x[6][i] * q, x[7][i] * q);
;             o.z = pk4_fp8(x[8][i] * q, x[9][i] * q, x[10][i] * q, x[11][i] * q); o.w = pk4_fp8(x[12][i] * q, x[13][i] * q, x[14][i] * q, x[15][i] * q);
;             *(LAS u32x4*)(scr + (l5 + 32 * i) * 80 + (2 * b + h) * 16) = o; }
	v_mul_f32_e32 v12, 0x43000000, v116
	v_cvt_pk_fp8_f32 v123, v8, v12 op_sel:[0,0,1]
	v_mul_f32_e32 v0, 0x43000000, v1
	v_mul_f32_e32 v1, 0x43000000, v5
	v_mul_f32_e32 v4, 0x43000000, v9
	ds_write_b128 v98, v[120:123]
	v_mov_b32_e32 v120, v153
	v_cvt_pk_fp8_f32 v120, v0, v1
	v_mul_f32_e32 v0, 0x43000000, v17
	v_mul_f32_e32 v1, 0x43000000, v21
	v_mov_b32_e32 v121, v153
	v_cvt_pk_fp8_f32 v121, v0, v1
	v_mul_f32_e32 v0, 0x43000000, v33
	v_mul_f32_e32 v1, 0x43000000, v37
	v_mov_b32_e32 v122, v153
	v_cvt_pk_fp8_f32 v122, v0, v1
	v_mul_f32_e32 v0, 0x43000000, v49
	v_mul_f32_e32 v1, 0x43000000, v53
	v_mov_b32_e32 v123, v153
	v_mul_f32_e32 v5, 0x43000000, v13
	v_cvt_pk_fp8_f32 v123, v0, v1
	v_cvt_pk_fp8_f32 v120, v4, v5 op_sel:[0,0,1]
	v_mul_f32_e32 v4, 0x43000000, v25
	v_mul_f32_e32 v5, 0x43000000, v29
	v_cvt_pk_fp8_f32 v121, v4, v5 op_sel:[0,0,1]
	v_mul_f32_e32 v4, 0x43000000, v41
	v_mul_f32_e32 v5, 0x43000000, v45
	v_cvt_pk_fp8_f32 v122, v4, v5 op_sel:[0,0,1]
	v_mul_f32_e32 v4, 0x43000000, v57
	v_mul_f32_e32 v5, 0x43000000, v117
	v_cvt_pk_fp8_f32 v123, v4, v5 op_sel:[0,0,1]
	v_mul_f32_e32 v0, 0x43000000, v2
	v_mul_f32_e32 v1, 0x43000000, v6
	v_mul_f32_e32 v2, 0x43000000, v10
	ds_write_b128 v98, v[120:123] offset:2560
	v_mov_b32_e32 v120, v153
	v_cvt_pk_fp8_f32 v120, v0, v1
	v_mul_f32_e32 v0, 0x43000000, v18
	v_mul_f32_e32 v1, 0x43000000, v22
	v_mov_b32_e32 v121, v153
	v_cvt_pk_fp8_f32 v121, v0, v1
	v_mul_f32_e32 v0, 0x43000000, v34
	v_mul_f32_e32 v1, 0x43000000, v38
	v_mov_b32_e32 v122, v153
	v_cvt_pk_fp8_f32 v122, v0, v1
	v_mul_f32_e32 v0, 0x43000000, v50
	v_mul_f32_e32 v1, 0x43000000, v54
	v_mov_b32_e32 v123, v153
	v_mul_f32_e32 v4, 0x43000000, v14
	v_cvt_pk_fp8_f32 v123, v0, v1
	v_cvt_pk_fp8_f32 v120, v2, v4 op_sel:[0,0,1]
	v_mul_f32_e32 v2, 0x43000000, v26
	v_mul_f32_e32 v4, 0x43000000, v30
	v_cvt_pk_fp8_f32 v121, v2, v4 op_sel:[0,0,1]
	v_mul_f32_e32 v2, 0x43000000, v42
	v_mul_f32_e32 v4, 0x43000000, v46
	v_cvt_pk_fp8_f32 v122, v2, v4 op_sel:[0,0,1]
	v_mul_f32_e32 v2, 0x43000000, v58
	v_mul_f32_e32 v4, 0x43000000, v118
	v_cvt_pk_fp8_f32 v123, v2, v4 op_sel:[0,0,1]
	v_mul_f32_e32 v1, 0x43000000, v3
	v_mul_f32_e32 v2, 0x43000000, v7
	v_mov_b32_e32 v0, v153
	v_cvt_pk_fp8_f32 v0, v1, v2
	v_mul_f32_e32 v3, 0x43000000, v11
	v_mul_f32_e32 v4, 0x43000000, v15
	v_mul_f32_e32 v2, 0x43000000, v19
	v_cvt_pk_fp8_f32 v0, v3, v4 op_sel:[0,0,1]
	v_mul_f32_e32 v3, 0x43000000, v23
	v_mov_b32_e32 v1, v153
	v_cvt_pk_fp8_f32 v1, v2, v3
	v_mul_f32_e32 v4, 0x43000000, v27
	v_mul_f32_e32 v5, 0x43000000, v31
	v_mul_f32_e32 v3, 0x43000000, v35
	v_cvt_pk_fp8_f32 v1, v4, v5 op_sel:[0,0,1]
	v_mul_f32_e32 v4, 0x43000000, v39
	v_mov_b32_e32 v2, v153
	v_cvt_pk_fp8_f32 v2, v3, v4
	v_mul_f32_e32 v5, 0x43000000, v43
	v_mul_f32_e32 v6, 0x43000000, v47
	v_mul_f32_e32 v4, 0x43000000, v51
	v_cvt_pk_fp8_f32 v2, v5, v6 op_sel:[0,0,1]
	v_mul_f32_e32 v5, 0x43000000, v55
	v_mov_b32_e32 v3, v153
	v_cvt_pk_fp8_f32 v3, v4, v5
	v_mul_f32_e32 v6, 0x43000000, v59
	v_mul_f32_e32 v7, 0x43000000, v119
	v_mov_b32_e32 v116, v153
	v_cvt_pk_fp8_f32 v3, v6, v7 op_sel:[0,0,1]
	v_mov_b32_e32 v117, v153
	v_mov_b32_e32 v118, v153
	v_mov_b32_e32 v119, v153
	ds_write_b128 v98, v[0:3] offset:7680
	v_add_co_u32_e32 v0, vcc, s2, v60
	s_mov_b32 s2, 0x42000
	s_nop 0
	v_addc_co_u32_e32 v1, vcc, 0, v61, vcc
	v_add_co_u32_e32 v4, vcc, s2, v60
	s_mov_b32 s2, 0x44000
	s_nop 0
	v_addc_co_u32_e32 v5, vcc, 0, v61, vcc
	v_add_co_u32_e32 v8, vcc, s2, v60
	s_mov_b32 s2, 0x46000
	s_nop 0
	v_addc_co_u32_e32 v9, vcc, 0, v61, vcc
	v_add_co_u32_e32 v12, vcc, s2, v60
	s_mov_b32 s2, 0x48000
	s_nop 0
	v_addc_co_u32_e32 v13, vcc, 0, v61, vcc
	global_load_dwordx4 v[8:11], v[8:9], off nt
	ds_write_b128 v98, v[120:123] offset:5120
	global_load_dwordx4 v[16:19], v[12:13], off nt
	v_add_co_u32_e32 v12, vcc, s2, v60
	s_mov_b32 s2, 0x4a000
	s_nop 0
	v_addc_co_u32_e32 v13, vcc, 0, v61, vcc
	v_add_co_u32_e32 v20, vcc, s2, v60
	s_mov_b32 s2, 0x4c000
	s_nop 0
	v_addc_co_u32_e32 v21, vcc, 0, v61, vcc
	global_load_dwordx4 v[12:15], v[12:13], off nt
	s_waitcnt vmcnt(0)
	v_mul_f32_e32 v8, 0x43000000, v8
	global_load_dwordx4 v[24:27], v[20:21], off nt
	v_add_co_u32_e32 v20, vcc, s2, v60
	s_mov_b32 s2, 0x4e000
	s_nop 0
	v_addc_co_u32_e32 v21, vcc, 0, v61, vcc
	global_load_dwordx4 v[28:31], v[20:21], off nt
	v_add_co_u32_e32 v20, vcc, s2, v60
	s_mov_b32 s2, 0x50000
	s_nop 0
	v_addc_co_u32_e32 v21, vcc, 0, v61, vcc
	global_load_dwordx4 v[40:43], v[20:21], off nt
	v_add_co_u32_e32 v20, vcc, s2, v60
	s_mov_b32 s2, 0x52000
	s_nop 0
	v_addc_co_u32_e32 v21, vcc, 0, v61, vcc
	v_add_co_u32_e32 v32, vcc, s2, v60
	s_mov_b32 s2, 0x54000
	s_nop 0
	v_addc_co_u32_e32 v33, vcc, 0, v61, vcc
	v_add_co_u32_e32 v36, vcc, s2, v60
	s_mov_b32 s2, 0x56000
	s_nop 0
	v_addc_co_u32_e32 v37, vcc, 0, v61, vcc
	v_add_co_u32_e32 v44, vcc, s2, v60
	s_mov_b32 s2, 0x58000
	s_nop 0
	v_addc_co_u32_e32 v45, vcc, 0, v61, vcc
	global_load_dwordx4 v[36:39], v[36:37], off nt
	s_waitcnt vmcnt(5)
	v_mul_f32_e32 v16, 0x43000000, v16
	global_load_dwordx4 v[48:51], v[44:45], off nt
	v_add_co_u32_e32 v44, vcc, s2, v60
	global_load_dwordx4 v[0:3], v[0:1], off nt
	s_nop 0
	v_addc_co_u32_e32 v45, vcc, 0, v61, vcc
	global_load_dwordx4 v[4:7], v[4:5], off nt
	s_mov_b32 s2, 0x5a000
	v_add_co_u32_e32 v52, vcc, s2, v60
	global_load_dwordx4 v[20:23], v[20:21], off nt
	s_nop 0
	v_addc_co_u32_e32 v53, vcc, 0, v61, vcc
	global_load_dwordx4 v[32:35], v[32:33], off nt
	s_mov_b32 s2, 0x5c000
	global_load_dwordx4 v[44:47], v[44:45], off nt
	v_add_co_u32_e32 v56, vcc, s2, v60
	global_load_dwordx4 v[52:55], v[52:53], off nt
	s_nop 0
	v_addc_co_u32_e32 v57, vcc, 0, v61, vcc
	s_mov_b32 s2, 0x5e000
	v_add_co_u32_e32 v60, vcc, s2, v60
	global_load_dwordx4 v[56:59], v[56:57], off nt
	s_nop 0
	v_addc_co_u32_e32 v61, vcc, 0, v61, vcc
	global_load_dwordx4 v[60:63], v[60:61], off nt
	s_waitcnt vmcnt(0)
; #define LAS __attribute__((address_space(3)))
; __device__ __forceinline__ unsigned pk4_fp8(float x0, float x1, float x2, float x3) { int w = 0; w = __builtin_amdgcn_cvt_pk_fp8_f32(x0, x1, w, false); w = __builtin_amdgcn_cvt_pk_fp8_f32(x2, x3, w, true); return (unsigned)w; }
; __device__ __forceinline__ void transpose_item_fp8w(const float* W, int K, int N, unsigned char* WT, float q, LAS unsigned char* scr, int item, int lane) {
;     ...
;         for (int i = 0; i < 4; ++i) {
;             u32x4 o;
;             o.x = pk4_fp8(x[0][i] * q, x[1][i] * q, x[2][i] * q, x[3][i] * q); o.y = pk4_fp8(x[4][i] * q, x[5][i] * q, x[6][i] * q, x[7][i] * q);
;             o.z = pk4_fp8(x[8][i] * q, x[9][i] * q, x[10][i] * q, x[11][i] * q); o.w = pk4_fp8(x[12][i] * q, x[13][i] * q, x[14][i] * q, x[15][i] * q);
;             *(LAS u32x4*)(scr + (l5 + 32 * i) * 80 + (2 * b + h) * 16) = o; }
;     }
;     asm volatile("s_waitcnt lgkmcnt(0)" ::: "memory");
; #pragma unroll
;     for (int qd = 0; qd < 8; ++qd) {
;         const int rho = 16 * qd + (lane >> 2), piece = lane & 3;
;         const u32x4 o = *(const LAS u32x4*)(scr + rho * 80 + piece * 16);
;         const int nl = 4 * (rho & 31) + (rho >> 5);
;         *(u32x4*)(WT + (size_t)(n0 + nl) * K + k0 + piece * 16) = o; }
;     asm volatile("s_waitcnt lgkmcnt(0)" ::: "memory");
	v_mul_f32_e32 v0, 0x43000000, v0
	s_waitcnt vmcnt(6)
	v_mul_f32_e32 v4, 0x43000000, v4
	v_cvt_pk_fp8_f32 v116, v0, v4
	v_mul_f32_e32 v0, 0x43000000, v12
	v_mul_f32_e32 v4, 0x43000000, v24
	v_cvt_pk_fp8_f32 v117, v0, v4
	s_waitcnt vmcnt(5)
	v_mul_f32_e32 v0, 0x43000000, v20
	v_cvt_pk_fp8_f32 v116, v8, v16 op_sel:[0,0,1]
	s_waitcnt vmcnt(4)
	v_mul_f32_e32 v4, 0x43000000, v32
	v_cvt_pk_fp8_f32 v118, v0, v4
	s_waitcnt vmcnt(3)
	v_mul_f32_e32 v0, 0x43000000, v44
	v_mul_f32_e32 v8, 0x43000000, v28
	v_mul_f32_e32 v12, 0x43000000, v40
	s_waitcnt vmcnt(2)
	v_mul_f32_e32 v4, 0x43000000, v52
	v_cvt_pk_fp8_f32 v119, v0, v4
	v_cvt_pk_fp8_f32 v117, v8, v12 op_sel:[0,0,1]
	v_mul_f32_e32 v8, 0x43000000, v36
	v_mul_f32_e32 v12, 0x43000000, v48
	v_cvt_pk_fp8_f32 v118, v8, v12 op_sel:[0,0,1]
	s_waitcnt vmcnt(1)
	v_mul_f32_e32 v8, 0x43000000, v56
	v_mul_f32_e32 v0, 0x43000000, v1
	v_mul_f32_e32 v1, 0x43000000, v5
	s_waitcnt vmcnt(0)
	v_mul_f32_e32 v12, 0x43000000, v60
	v_cvt_pk_fp8_f32 v119, v8, v12 op_sel:[0,0,1]
	v_mul_f32_e32 v4, 0x43000000, v9
	v_mul_f32_e32 v5, 0x43000000, v17
	ds_write_b128 v98, v[116:119] offset:32
	v_mov_b32_e32 v116, v153
	v_cvt_pk_fp8_f32 v116, v0, v1
	v_mul_f32_e32 v0, 0x43000000, v13
	v_mul_f32_e32 v1, 0x43000000, v25
	v_mov_b32_e32 v117, v153
	v_cvt_pk_fp8_f32 v117, v0, v1
	v_mul_f32_e32 v0, 0x43000000, v21
	v_mul_f32_e32 v1, 0x43000000, v33
	v_mov_b32_e32 v118, v153
	v_cvt_pk_fp8_f32 v118, v0, v1
	v_mul_f32_e32 v0, 0x43000000, v45
	v_mul_f32_e32 v1, 0x43000000, v53
	v_mov_b32_e32 v119, v153
	v_cvt_pk_fp8_f32 v119, v0, v1
	v_cvt_pk_fp8_f32 v116, v4, v5 op_sel:[0,0,1]
	v_mul_f32_e32 v4, 0x43000000, v29
	v_mul_f32_e32 v5, 0x43000000, v41
	v_cvt_pk_fp8_f32 v117, v4, v5 op_sel:[0,0,1]
	v_mul_f32_e32 v4, 0x43000000, v37
	v_mul_f32_e32 v5, 0x43000000, v49
	v_cvt_pk_fp8_f32 v118, v4, v5 op_sel:[0,0,1]
	v_mul_f32_e32 v4, 0x43000000, v57
	v_mul_f32_e32 v5, 0x43000000, v61
	v_cvt_pk_fp8_f32 v119, v4, v5 op_sel:[0,0,1]
	v_mul_f32_e32 v0, 0x43000000, v2
	v_mul_f32_e32 v1, 0x43000000, v6
	v_mul_f32_e32 v2, 0x43000000, v10
	ds_write_b128 v98, v[116:119] offset:2592
	v_mov_b32_e32 v116, v153
	v_cvt_pk_fp8_f32 v116, v0, v1
	v_mul_f32_e32 v0, 0x43000000, v14
	v_mul_f32_e32 v1, 0x43000000, v26
	v_mov_b32_e32 v117, v153
	v_cvt_pk_fp8_f32 v117, v0, v1
	v_mul_f32_e32 v0, 0x43000000, v22
	v_mul_f32_e32 v1, 0x43000000, v34
	v_mov_b32_e32 v118, v153
	v_cvt_pk_fp8_f32 v118, v0, v1
	v_mul_f32_e32 v0, 0x43000000, v46
	v_mul_f32_e32 v1, 0x43000000, v54
	v_mov_b32_e32 v119, v153
	v_mul_f32_e32 v4, 0x43000000, v18
	v_cvt_pk_fp8_f32 v119, v0, v1
	v_cvt_pk_fp8_f32 v116, v2, v4 op_sel:[0,0,1]
	v_mul_f32_e32 v2, 0x43000000, v30
	v_mul_f32_e32 v4, 0x43000000, v42
	v_cvt_pk_fp8_f32 v117, v2, v4 op_sel:[0,0,1]
	v_mul_f32_e32 v2, 0x43000000, v38
	v_mul_f32_e32 v4, 0x43000000, v50
	v_cvt_pk_fp8_f32 v118, v2, v4 op_sel:[0,0,1]
	v_mul_f32_e32 v2, 0x43000000, v58
	v_mul_f32_e32 v4, 0x43000000, v62
	v_cvt_pk_fp8_f32 v119, v2, v4 op_sel:[0,0,1]
	v_mul_f32_e32 v1, 0x43000000, v3
	v_mul_f32_e32 v2, 0x43000000, v7
	v_mov_b32_e32 v0, v153
	v_cvt_pk_fp8_f32 v0, v1, v2
	v_mul_f32_e32 v3, 0x43000000, v11
	v_mul_f32_e32 v4, 0x43000000, v19
	v_mul_f32_e32 v2, 0x43000000, v15
	v_cvt_pk_fp8_f32 v0, v3, v4 op_sel:[0,0,1]
	v_mul_f32_e32 v3, 0x43000000, v27
	v_mov_b32_e32 v1, v153
	v_cvt_pk_fp8_f32 v1, v2, v3
	v_mul_f32_e32 v4, 0x43000000, v31
	v_mul_f32_e32 v5, 0x43000000, v43
	v_mul_f32_e32 v3, 0x43000000, v23
	v_cvt_pk_fp8_f32 v1, v4, v5 op_sel:[0,0,1]
	v_mul_f32_e32 v4, 0x43000000, v35
	v_mov_b32_e32 v2, v153
	v_cvt_pk_fp8_f32 v2, v3, v4
	v_mul_f32_e32 v5, 0x43000000, v39
	v_mul_f32_e32 v6, 0x43000000, v51
	v_mul_f32_e32 v4, 0x43000000, v47
	v_cvt_pk_fp8_f32 v2, v5, v6 op_sel:[0,0,1]
	v_mul_f32_e32 v5, 0x43000000, v55
	v_mov_b32_e32 v3, v153
	v_cvt_pk_fp8_f32 v3, v4, v5
	v_mul_f32_e32 v6, 0x43000000, v59
	v_mul_f32_e32 v7, 0x43000000, v63
	ds_write_b128 v98, v[116:119] offset:5152
	v_cvt_pk_fp8_f32 v3, v6, v7 op_sel:[0,0,1]
	v_add_u32_e32 v6, s0, v102
	v_ashrrev_i32_e32 v7, 31, v6
	v_lshl_add_u64 v[4:5], s[10:11], 0, v[64:65]
	ds_write_b128 v98, v[0:3] offset:7712
	s_waitcnt lgkmcnt(0)
	ds_read_b128 v[0:3], v99
	v_lshlrev_b64 v[6:7], 10, v[6:7]
	v_lshl_add_u64 v[6:7], v[4:5], 0, v[6:7]
	s_waitcnt lgkmcnt(0)
	global_store_dwordx4 v[6:7], v[0:3], off nt
	ds_read_b128 v[0:3], v99 offset:1280
	v_add_u32_e32 v6, s0, v103
	v_ashrrev_i32_e32 v7, 31, v6
	v_lshlrev_b64 v[6:7], 10, v[6:7]
	v_lshl_add_u64 v[6:7], v[4:5], 0, v[6:7]
	s_waitcnt lgkmcnt(0)
	global_store_dwordx4 v[6:7], v[0:3], off nt
	ds_read_b128 v[0:3], v99 offset:2560
	v_add_u32_e32 v6, s0, v104
	v_ashrrev_i32_e32 v7, 31, v6
	v_lshlrev_b64 v[6:7], 10, v[6:7]
	v_lshl_add_u64 v[6:7], v[4:5], 0, v[6:7]
	s_waitcnt lgkmcnt(0)
	global_store_dwordx4 v[6:7], v[0:3], off nt
	ds_read_b128 v[0:3], v99 offset:3840
	v_add_u32_e32 v6, s0, v105
	v_ashrrev_i32_e32 v7, 31, v6
	v_lshlrev_b64 v[6:7], 10, v[6:7]
	v_lshl_add_u64 v[6:7], v[4:5], 0, v[6:7]
	s_waitcnt lgkmcnt(0)
	global_store_dwordx4 v[6:7], v[0:3], off nt
	ds_read_b128 v[0:3], v99 offset:5120
	v_add_u32_e32 v6, s0, v106
	v_ashrrev_i32_e32 v7, 31, v6
	v_lshlrev_b64 v[6:7], 10, v[6:7]
	v_lshl_add_u64 v[6:7], v[4:5], 0, v[6:7]
	s_waitcnt lgkmcnt(0)
	global_store_dwordx4 v[6:7], v[0:3], off nt
	ds_read_b128 v[0:3], v99 offset:6400
	v_add_u32_e32 v6, s0, v107
	v_ashrrev_i32_e32 v7, 31, v6
	v_lshlrev_b64 v[6:7], 10, v[6:7]
	v_lshl_add_u64 v[6:7], v[4:5], 0, v[6:7]
	s_waitcnt lgkmcnt(0)
	global_store_dwordx4 v[6:7], v[0:3], off nt
	ds_read_b128 v[0:3], v99 offset:7680
	v_add_u32_e32 v6, s0, v108
	v_ashrrev_i32_e32 v7, 31, v6
	v_lshlrev_b64 v[6:7], 10, v[6:7]
	v_lshl_add_u64 v[6:7], v[4:5], 0, v[6:7]
	s_waitcnt lgkmcnt(0)
	global_store_dwordx4 v[6:7], v[0:3], off nt
	ds_read_b128 v[0:3], v99 offset:8960
	v_add_u32_e32 v6, s0, v109
	v_ashrrev_i32_e32 v7, 31, v6
	v_lshlrev_b64 v[6:7], 10, v[6:7]
	v_lshl_add_u64 v[4:5], v[4:5], 0, v[6:7]
	s_waitcnt lgkmcnt(0)
	global_store_dwordx4 v[4:5], v[0:3], off nt
	s_waitcnt lgkmcnt(0)
	s_mov_b64 s[0:1], 0

; #define LAS __attribute__((address_space(3)))
; template <int QPERM>
; __device__ __forceinline__ void transpose_item(const float* W, int K, int N, bf16_t* WT, LAS float* scr, int item, int lane) {
;     const int nblk = N / 32, kb = item / nblk, nb = item % nblk, k0 = 64 * kb, n0 = 32 * nb;
; #pragma unroll 8
;     for (int i = 0; i < 32; ++i) { const int kk = 2 * i + (lane >> 5); scr[kk * 33 + (lane & 31)] = W[(size_t)(k0 + kk) * N + n0 + (lane & 31)]; }
;     asm volatile("s_waitcnt lgkmcnt(0)" ::: "memory");
.LBB0_338:
	s_lshl_b32 s11, s9, 1
	s_lshl_b32 s12, s8, 1
	v_add_u32_e32 v20, s11, v2
	v_add_u32_e32 v18, s12, v3
	v_ashrrev_i32_e32 v21, 31, v20
	v_ashrrev_i32_e32 v19, 31, v18
	v_lshlrev_b64 v[20:21], 12, v[20:21]
	v_lshlrev_b64 v[18:19], 12, v[18:19]
	v_lshl_add_u64 v[20:21], v[0:1], 0, v[20:21]
	v_lshl_add_u64 v[18:19], v[0:1], 0, v[18:19]
	global_load_dword v24, v[20:21], off nt
	global_load_dword v25, v[18:19], off nt
	v_add_u32_e32 v22, s12, v69
	v_add_u32_e32 v23, s11, v96
	v_mad_u64_u32 v[18:19], s[14:15], v23, s83, v[68:69]
	v_mad_u64_u32 v[20:21], s[14:15], v22, s83, v[68:69]
	v_add_u32_e32 v22, s12, v85
	v_add_u32_e32 v23, s11, v84
	s_add_i32 s9, s9, 16
	s_add_i32 s8, s8, 16
	s_add_i32 s10, s10, -16
	s_cmp_lg_u32 s10, 0
	s_waitcnt vmcnt(0)
	ds_write_b32 v18, v24
	s_waitcnt vmcnt(0)
	ds_write_b32 v20, v25
	v_add_u32_e32 v20, s11, v4
	v_add_u32_e32 v18, s12, v5
	v_ashrrev_i32_e32 v21, 31, v20
	v_ashrrev_i32_e32 v19, 31, v18
	v_lshlrev_b64 v[20:21], 12, v[20:21]
	v_lshlrev_b64 v[18:19], 12, v[18:19]
	v_lshl_add_u64 v[20:21], v[0:1], 0, v[20:21]
	v_lshl_add_u64 v[18:19], v[0:1], 0, v[18:19]
	global_load_dword v24, v[20:21], off nt
	global_load_dword v25, v[18:19], off nt
	v_mad_u64_u32 v[18:19], s[14:15], v23, s83, v[68:69]
	v_mad_u64_u32 v[20:21], s[14:15], v22, s83, v[68:69]
	v_add_u32_e32 v22, s12, v87
	v_add_u32_e32 v23, s11, v86
	s_waitcnt vmcnt(0)
	ds_write_b32 v18, v24
	s_waitcnt vmcnt(0)
	ds_write_b32 v20, v25
	v_add_u32_e32 v20, s11, v6
	v_add_u32_e32 v18, s12, v7
	v_ashrrev_i32_e32 v21, 31, v20
	v_ashrrev_i32_e32 v19, 31, v18
	v_lshlrev_b64 v[20:21], 12, v[20:21]
	v_lshlrev_b64 v[18:19], 12, v[18:19]
	v_lshl_add_u64 v[20:21], v[0:1], 0, v[20:21]
	v_lshl_add_u64 v[18:19], v[0:1], 0, v[18:19]
	global_load_dword v24, v[20:21], off nt
	global_load_dword v25, v[18:19], off nt
	v_mad_u64_u32 v[18:19], s[14:15], v23, s83, v[68:69]
	v_mad_u64_u32 v[20:21], s[14:15], v22, s83, v[68:69]
	v_add_u32_e32 v22, s12, v89
	v_add_u32_e32 v23, s11, v88
	s_waitcnt vmcnt(0)
	ds_write_b32 v18, v24
	s_waitcnt vmcnt(0)
	ds_write_b32 v20, v25
	v_add_u32_e32 v20, s11, v8
	v_add_u32_e32 v18, s12, v9
	v_ashrrev_i32_e32 v21, 31, v20
	v_ashrrev_i32_e32 v19, 31, v18
	v_lshlrev_b64 v[20:21], 12, v[20:21]
	v_lshlrev_b64 v[18:19], 12, v[18:19]
	v_lshl_add_u64 v[20:21], v[0:1], 0, v[20:21]
	v_lshl_add_u64 v[18:19], v[0:1], 0, v[18:19]
	global_load_dword v24, v[20:21], off nt
	global_load_dword v25, v[18:19], off nt
	v_mad_u64_u32 v[18:19], s[14:15], v23, s83, v[68:69]
	v_mad_u64_u32 v[20:21], s[14:15], v22, s83, v[68:69]
	v_add_u32_e32 v22, s12, v91
	v_add_u32_e32 v23, s11, v90
	s_waitcnt vmcnt(0)
	ds_write_b32 v18, v24
	s_waitcnt vmcnt(0)
	ds_write_b32 v20, v25
	v_add_u32_e32 v20, s11, v10
	v_add_u32_e32 v18, s12, v11
	v_ashrrev_i32_e32 v21, 31, v20
	v_ashrrev_i32_e32 v19, 31, v18
	v_lshlrev_b64 v[20:21], 12, v[20:21]
	v_lshlrev_b64 v[18:19], 12, v[18:19]
	v_lshl_add_u64 v[20:21], v[0:1], 0, v[20:21]
	v_lshl_add_u64 v[18:19], v[0:1], 0, v[18:19]
	global_load_dword v24, v[20:21], off nt
	global_load_dword v25, v[18:19], off nt
	v_mad_u64_u32 v[18:19], s[14:15], v23, s83, v[68:69]
	v_mad_u64_u32 v[20:21], s[14:15], v22, s83, v[68:69]
	v_add_u32_e32 v22, s12, v93
	v_add_u32_e32 v23, s11, v92
	s_waitcnt vmcnt(0)
	ds_write_b32 v18, v24
	s_waitcnt vmcnt(0)
	ds_write_b32 v20, v25
	v_add_u32_e32 v20, s11, v12
	v_add_u32_e32 v18, s12, v13
	v_ashrrev_i32_e32 v21, 31, v20
	v_ashrrev_i32_e32 v19, 31, v18
	v_lshlrev_b64 v[20:21], 12, v[20:21]
	v_lshlrev_b64 v[18:19], 12, v[18:19]
	v_lshl_add_u64 v[20:21], v[0:1], 0, v[20:21]
	v_lshl_add_u64 v[18:19], v[0:1], 0, v[18:19]
	global_load_dword v24, v[20:21], off nt
	global_load_dword v25, v[18:19], off nt
	v_mad_u64_u32 v[18:19], s[14:15], v23, s83, v[68:69]
	v_mad_u64_u32 v[20:21], s[14:15], v22, s83, v[68:69]
	v_add_u32_e32 v22, s12, v95
	v_add_u32_e32 v23, s11, v94
	s_waitcnt vmcnt(0)
	ds_write_b32 v18, v24
	s_waitcnt vmcnt(0)
	ds_write_b32 v20, v25
	v_add_u32_e32 v20, s11, v14
	v_add_u32_e32 v18, s12, v15
	v_ashrrev_i32_e32 v21, 31, v20
	v_ashrrev_i32_e32 v19, 31, v18
	v_lshlrev_b64 v[20:21], 12, v[20:21]
	v_lshlrev_b64 v[18:19], 12, v[18:19]
	v_lshl_add_u64 v[20:21], v[0:1], 0, v[20:21]
	v_lshl_add_u64 v[18:19], v[0:1], 0, v[18:19]
	global_load_dword v24, v[20:21], off nt
	global_load_dword v25, v[18:19], off nt
	v_mad_u64_u32 v[18:19], s[14:15], v23, s83, v[68:69]
	v_mad_u64_u32 v[20:21], s[14:15], v22, s83, v[68:69]
	v_add_u32_e32 v23, s11, v100
	v_add_u32_e32 v22, s12, v97
	s_waitcnt vmcnt(0)
	ds_write_b32 v18, v24
	s_waitcnt vmcnt(0)
	ds_write_b32 v20, v25
	v_add_u32_e32 v20, s11, v16
	v_add_u32_e32 v18, s12, v17
	v_ashrrev_i32_e32 v21, 31, v20
	v_ashrrev_i32_e32 v19, 31, v18
	v_lshlrev_b64 v[20:21], 12, v[20:21]
	v_lshlrev_b64 v[18:19], 12, v[18:19]
	v_lshl_add_u64 v[20:21], v[0:1], 0, v[20:21]
	v_lshl_add_u64 v[18:19], v[0:1], 0, v[18:19]
	global_load_dword v24, v[20:21], off nt
	global_load_dword v25, v[18:19], off nt
	v_mad_u64_u32 v[18:19], s[12:13], v23, s83, v[68:69]
	v_mad_u64_u32 v[20:21], s[12:13], v22, s83, v[68:69]
	s_waitcnt vmcnt(0)
	ds_write_b32 v18, v24
	s_waitcnt vmcnt(0)
	ds_write_b32 v20, v25
	s_cbranch_scc1 .LBB0_338
; #define LAS __attribute__((address_space(3)))
; __device__ __forceinline__ unsigned pk2(float lo, float hi) { unsigned r; asm("v_cvt_pk_bf16_f32 %0, %1, %2" : "=v"(r) : "v"(lo), "v"(hi)); return r; }
; template <int QPERM>
; __device__ __forceinline__ void transpose_item(const float* W, int K, int N, bf16_t* WT, LAS float* scr, int item, int lane) {
;     ...
;     const int c = lane & 7;
; #pragma unroll
;     for (int j = 0; j < 4; ++j) { const int n = (lane >> 3) + 8 * j; const LAS float* s = scr + (8 * c) * 33 + n;
;         u32x4 o; o.x = pk2(s[0 * 33], s[1 * 33]); o.y = pk2(s[2 * 33], s[3 * 33]); o.z = pk2(s[4 * 33], s[5 * 33]); o.w = pk2(s[6 * 33], s[7 * 33]);
;         int dn = n0 + n;
;         if (QPERM == 1) { const int h = dn / 192, d = dn % 192; if (d >= 128) { const int jj = d - 128, a = jj >> 5, p = (jj >> 4) & 1, f = jj & 15; dn = h * 192 + 128 + 2 * (a * 16 + f) + p; } }
;         if (QPERM == 2) { const int h = dn >> 8, j = dn & 255; dn = (j < 128) ? h * 128 + j : 512 + h * 128 + (j - 128); }
;         *(u32x4*)(WT + (size_t)dn * K + k0 + 8 * c) = o; }
;     asm volatile("s_waitcnt lgkmcnt(0)" ::: "memory");
	s_waitcnt lgkmcnt(0)
	ds_read2_b32 v[6:7], v111 offset0:33 offset1:41
	ds_read2_b32 v[8:9], v111 offset1:8
	s_lshl_b32 s2, s1, 1
	s_mov_b32 s1, s3
	ds_read2_b32 v[10:11], v111 offset0:66 offset1:74
	ds_read2_b32 v[12:13], v111 offset0:99 offset1:107
	ds_read2_b32 v[14:15], v111 offset0:132 offset1:140
	ds_read2_b32 v[16:17], v111 offset0:165 offset1:173
	ds_read2_b32 v[18:19], v111 offset0:198 offset1:206
	ds_read2_b32 v[20:21], v111 offset0:231 offset1:239
	v_writelane_b32 v253, s0, 32
	v_lshl_add_u64 v[4:5], v[70:71], 0, s[2:3]
	s_waitcnt lgkmcnt(6)
	v_cvt_pk_bf16_f32 v0, v8, v6
	s_waitcnt lgkmcnt(4)
	v_cvt_pk_bf16_f32 v1, v10, v12
	s_waitcnt lgkmcnt(2)
	v_cvt_pk_bf16_f32 v2, v14, v16
	s_waitcnt lgkmcnt(0)
	v_cvt_pk_bf16_f32 v3, v18, v20
	v_add_u32_e32 v22, s0, v110
	v_ashrrev_i32_e32 v23, 31, v22
	v_lshlrev_b64 v[22:23], 11, v[22:23]
	v_lshl_add_u64 v[22:23], v[4:5], 0, v[22:23]
	v_add_u32_e32 v6, s0, v112
	global_store_dwordx4 v[22:23], v[0:3], off nt
	v_add_u32_e32 v22, s0, v113
	v_ashrrev_i32_e32 v23, 31, v22
	v_cvt_pk_bf16_f32 v0, v9, v7
	v_ashrrev_i32_e32 v7, 31, v6
	v_lshlrev_b64 v[6:7], 11, v[6:7]
	v_lshl_add_u64 v[6:7], v[4:5], 0, v[6:7]
	v_cvt_pk_bf16_f32 v1, v11, v13
	v_cvt_pk_bf16_f32 v2, v15, v17
	v_cvt_pk_bf16_f32 v3, v19, v21
	global_store_dwordx4 v[6:7], v[0:3], off nt
	ds_read2_b32 v[6:7], v111 offset0:16 offset1:24
	ds_read2_b32 v[8:9], v111 offset0:49 offset1:57
	ds_read2_b32 v[10:11], v111 offset0:82 offset1:90
	ds_read2_b32 v[12:13], v111 offset0:115 offset1:123
	ds_read2_b32 v[14:15], v111 offset0:148 offset1:156
	ds_read2_b32 v[16:17], v111 offset0:181 offset1:189
	ds_read2_b32 v[18:19], v111 offset0:214 offset1:222
	ds_read2_b32 v[20:21], v111 offset0:247 offset1:255
	v_lshlrev_b64 v[22:23], 11, v[22:23]
	s_waitcnt lgkmcnt(6)
	v_cvt_pk_bf16_f32 v0, v6, v8
	v_lshl_add_u64 v[22:23], v[4:5], 0, v[22:23]
	v_add_u32_e32 v6, s0, v114
	s_waitcnt lgkmcnt(4)
	v_cvt_pk_bf16_f32 v1, v10, v12
	s_waitcnt lgkmcnt(2)
	v_cvt_pk_bf16_f32 v2, v14, v16
	s_waitcnt lgkmcnt(0)
	v_cvt_pk_bf16_f32 v3, v18, v20
	global_store_dwordx4 v[22:23], v[0:3], off nt
	v_writelane_b32 v253, s1, 33
	s_nop 0
	v_cvt_pk_bf16_f32 v0, v7, v9
	v_ashrrev_i32_e32 v7, 31, v6
	v_lshlrev_b64 v[6:7], 11, v[6:7]
	v_lshl_add_u64 v[4:5], v[4:5], 0, v[6:7]
	v_cvt_pk_bf16_f32 v1, v11, v13
	v_cvt_pk_bf16_f32 v2, v15, v17
	v_cvt_pk_bf16_f32 v3, v19, v21
	global_store_dwordx4 v[4:5], v[0:3], off nt
	s_waitcnt lgkmcnt(0)

; #define LAS __attribute__((address_space(3)))
; template <int QPERM>
; __device__ __forceinline__ void transpose_item(const float* W, int K, int N, bf16_t* WT, LAS float* scr, int item, int lane) {
;     const int nblk = N / 32, kb = item / nblk, nb = item % nblk, k0 = 64 * kb, n0 = 32 * nb;
; #pragma unroll 8
;     for (int i = 0; i < 32; ++i) { const int kk = 2 * i + (lane >> 5); scr[kk * 33 + (lane & 31)] = W[(size_t)(k0 + kk) * N + n0 + (lane & 31)]; }
;     asm volatile("s_waitcnt lgkmcnt(0)" ::: "memory");
.LBB0_343:
	s_lshl_b32 s11, s9, 1
	s_lshl_b32 s12, s8, 1
	v_add_u32_e32 v20, s11, v2
	v_add_u32_e32 v18, s12, v3
	v_ashrrev_i32_e32 v21, 31, v20
	v_ashrrev_i32_e32 v19, 31, v18
	v_lshlrev_b64 v[20:21], 12, v[20:21]
	v_lshlrev_b64 v[18:19], 12, v[18:19]
	v_lshl_add_u64 v[20:21], v[0:1], 0, v[20:21]
	v_lshl_add_u64 v[18:19], v[0:1], 0, v[18:19]
	global_load_dword v24, v[20:21], off nt
	global_load_dword v25, v[18:19], off nt
	v_add_u32_e32 v22, s12, v69
	v_add_u32_e32 v23, s11, v96
	v_mad_u64_u32 v[18:19], s[14:15], v23, s83, v[68:69]
	v_mad_u64_u32 v[20:21], s[14:15], v22, s83, v[68:69]
	v_add_u32_e32 v22, s12, v85
	v_add_u32_e32 v23, s11, v84
	s_add_i32 s9, s9, 16
	s_add_i32 s8, s8, 16
	s_add_i32 s10, s10, -16
	s_cmp_lg_u32 s10, 0
	s_waitcnt vmcnt(0)
	ds_write_b32 v18, v24
	s_waitcnt vmcnt(0)
	ds_write_b32 v20, v25
	v_add_u32_e32 v20, s11, v4
	v_add_u32_e32 v18, s12, v5
	v_ashrrev_i32_e32 v21, 31, v20
	v_ashrrev_i32_e32 v19, 31, v18
	v_lshlrev_b64 v[20:21], 12, v[20:21]
	v_lshlrev_b64 v[18:19], 12, v[18:19]
	v_lshl_add_u64 v[20:21], v[0:1], 0, v[20:21]
	v_lshl_add_u64 v[18:19], v[0:1], 0, v[18:19]
	global_load_dword v24, v[20:21], off nt
	global_load_dword v25, v[18:19], off nt
	v_mad_u64_u32 v[18:19], s[14:15], v23, s83, v[68:69]
	v_mad_u64_u32 v[20:21], s[14:15], v22, s83, v[68:69]
	v_add_u32_e32 v22, s12, v87
	v_add_u32_e32 v23, s11, v86
	s_waitcnt vmcnt(0)
	ds_write_b32 v18, v24
	s_waitcnt vmcnt(0)
	ds_write_b32 v20, v25
	v_add_u32_e32 v20, s11, v6
	v_add_u32_e32 v18, s12, v7
	v_ashrrev_i32_e32 v21, 31, v20
	v_ashrrev_i32_e32 v19, 31, v18
	v_lshlrev_b64 v[20:21], 12, v[20:21]
	v_lshlrev_b64 v[18:19], 12, v[18:19]
	v_lshl_add_u64 v[20:21], v[0:1], 0, v[20:21]
	v_lshl_add_u64 v[18:19], v[0:1], 0, v[18:19]
	global_load_dword v24, v[20:21], off nt
	global_load_dword v25, v[18:19], off nt
	v_mad_u64_u32 v[18:19], s[14:15], v23, s83, v[68:69]
	v_mad_u64_u32 v[20:21], s[14:15], v22, s83, v[68:69]
	v_add_u32_e32 v22, s12, v89
	v_add_u32_e32 v23, s11, v88
	s_waitcnt vmcnt(0)
	ds_write_b32 v18, v24
	s_waitcnt vmcnt(0)
	ds_write_b32 v20, v25
	v_add_u32_e32 v20, s11, v8
	v_add_u32_e32 v18, s12, v9
	v_ashrrev_i32_e32 v21, 31, v20
	v_ashrrev_i32_e32 v19, 31, v18
	v_lshlrev_b64 v[20:21], 12, v[20:21]
	v_lshlrev_b64 v[18:19], 12, v[18:19]
	v_lshl_add_u64 v[20:21], v[0:1], 0, v[20:21]
	v_lshl_add_u64 v[18:19], v[0:1], 0, v[18:19]
	global_load_dword v24, v[20:21], off nt
	global_load_dword v25, v[18:19], off nt
	v_mad_u64_u32 v[18:19], s[14:15], v23, s83, v[68:69]
	v_mad_u64_u32 v[20:21], s[14:15], v22, s83, v[68:69]
	v_add_u32_e32 v22, s12, v91
	v_add_u32_e32 v23, s11, v90
	s_waitcnt vmcnt(0)
	ds_write_b32 v18, v24
	s_waitcnt vmcnt(0)
	ds_write_b32 v20, v25
	v_add_u32_e32 v20, s11, v10
	v_add_u32_e32 v18, s12, v11
	v_ashrrev_i32_e32 v21, 31, v20
	v_ashrrev_i32_e32 v19, 31, v18
	v_lshlrev_b64 v[20:21], 12, v[20:21]
	v_lshlrev_b64 v[18:19], 12, v[18:19]
	v_lshl_add_u64 v[20:21], v[0:1], 0, v[20:21]
	v_lshl_add_u64 v[18:19], v[0:1], 0, v[18:19]
	global_load_dword v24, v[20:21], off nt
	global_load_dword v25, v[18:19], off nt
	v_mad_u64_u32 v[18:19], s[14:15], v23, s83, v[68:69]
	v_mad_u64_u32 v[20:21], s[14:15], v22, s83, v[68:69]
	v_add_u32_e32 v22, s12, v93
	v_add_u32_e32 v23, s11, v92
	s_waitcnt vmcnt(0)
	ds_write_b32 v18, v24
	s_waitcnt vmcnt(0)
	ds_write_b32 v20, v25
	v_add_u32_e32 v20, s11, v12
	v_add_u32_e32 v18, s12, v13
	v_ashrrev_i32_e32 v21, 31, v20
	v_ashrrev_i32_e32 v19, 31, v18
	v_lshlrev_b64 v[20:21], 12, v[20:21]
	v_lshlrev_b64 v[18:19], 12, v[18:19]
	v_lshl_add_u64 v[20:21], v[0:1], 0, v[20:21]
	v_lshl_add_u64 v[18:19], v[0:1], 0, v[18:19]
	global_load_dword v24, v[20:21], off nt
	global_load_dword v25, v[18:19], off nt
	v_mad_u64_u32 v[18:19], s[14:15], v23, s83, v[68:69]
	v_mad_u64_u32 v[20:21], s[14:15], v22, s83, v[68:69]
	v_add_u32_e32 v22, s12, v95
	v_add_u32_e32 v23, s11, v94
	s_waitcnt vmcnt(0)
	ds_write_b32 v18, v24
	s_waitcnt vmcnt(0)
	ds_write_b32 v20, v25
	v_add_u32_e32 v20, s11, v14
	v_add_u32_e32 v18, s12, v15
	v_ashrrev_i32_e32 v21, 31, v20
	v_ashrrev_i32_e32 v19, 31, v18
	v_lshlrev_b64 v[20:21], 12, v[20:21]
	v_lshlrev_b64 v[18:19], 12, v[18:19]
	v_lshl_add_u64 v[20:21], v[0:1], 0, v[20:21]
	v_lshl_add_u64 v[18:19], v[0:1], 0, v[18:19]
	global_load_dword v24, v[20:21], off nt
	global_load_dword v25, v[18:19], off nt
	v_mad_u64_u32 v[18:19], s[14:15], v23, s83, v[68:69]
	v_mad_u64_u32 v[20:21], s[14:15], v22, s83, v[68:69]
	v_add_u32_e32 v23, s11, v100
	v_add_u32_e32 v22, s12, v97
	s_waitcnt vmcnt(0)
	ds_write_b32 v18, v24
	s_waitcnt vmcnt(0)
	ds_write_b32 v20, v25
	v_add_u32_e32 v20, s11, v16
	v_add_u32_e32 v18, s12, v17
	v_ashrrev_i32_e32 v21, 31, v20
	v_ashrrev_i32_e32 v19, 31, v18
	v_lshlrev_b64 v[20:21], 12, v[20:21]
	v_lshlrev_b64 v[18:19], 12, v[18:19]
	v_lshl_add_u64 v[20:21], v[0:1], 0, v[20:21]
	v_lshl_add_u64 v[18:19], v[0:1], 0, v[18:19]
	global_load_dword v24, v[20:21], off nt
	global_load_dword v25, v[18:19], off nt
	v_mad_u64_u32 v[18:19], s[12:13], v23, s83, v[68:69]
	v_mad_u64_u32 v[20:21], s[12:13], v22, s83, v[68:69]
	s_waitcnt vmcnt(0)
	ds_write_b32 v18, v24
	s_waitcnt vmcnt(0)
	ds_write_b32 v20, v25
	s_cbranch_scc1 .LBB0_343
; #define LAS __attribute__((address_space(3)))
; __device__ __forceinline__ unsigned pk2(float lo, float hi) { unsigned r; asm("v_cvt_pk_bf16_f32 %0, %1, %2" : "=v"(r) : "v"(lo), "v"(hi)); return r; }
; template <int QPERM>
; __device__ __forceinline__ void transpose_item(const float* W, int K, int N, bf16_t* WT, LAS float* scr, int item, int lane) {
;     ...
;     const int c = lane & 7;
; #pragma unroll
;     for (int j = 0; j < 4; ++j) { const int n = (lane >> 3) + 8 * j; const LAS float* s = scr + (8 * c) * 33 + n;
;         u32x4 o; o.x = pk2(s[0 * 33], s[1 * 33]); o.y = pk2(s[2 * 33], s[3 * 33]); o.z = pk2(s[4 * 33], s[5 * 33]); o.w = pk2(s[6 * 33], s[7 * 33]);
;         int dn = n0 + n;
;         if (QPERM == 1) { const int h = dn / 192, d = dn % 192; if (d >= 128) { const int jj = d - 128, a = jj >> 5, p = (jj >> 4) & 1, f = jj & 15; dn = h * 192 + 128 + 2 * (a * 16 + f) + p; } }
;         if (QPERM == 2) { const int h = dn >> 8, j = dn & 255; dn = (j < 128) ? h * 128 + j : 512 + h * 128 + (j - 128); }
;         *(u32x4*)(WT + (size_t)dn * K + k0 + 8 * c) = o; }
;     asm volatile("s_waitcnt lgkmcnt(0)" ::: "memory");
	s_waitcnt lgkmcnt(0)
	ds_read2_b32 v[6:7], v111 offset0:33 offset1:41
	ds_read2_b32 v[8:9], v111 offset1:8
	ds_read2_b32 v[10:11], v111 offset0:66 offset1:74
	ds_read2_b32 v[12:13], v111 offset0:99 offset1:107
	s_lshl_b32 s2, s1, 1
	s_mov_b32 s1, s3
	v_writelane_b32 v253, s0, 32
	s_waitcnt lgkmcnt(2)
	v_cvt_pk_bf16_f32 v0, v8, v6
	v_lshl_add_u64 v[4:5], v[74:75], 0, s[2:3]
	s_movk_i32 s2, 0x180
	v_add_u32_e32 v6, s0, v110
	v_and_b32_e32 v8, 0xff, v6
	v_ashrrev_i32_e32 v6, 1, v6
	v_writelane_b32 v253, s1, 33
	s_movk_i32 s1, 0x80
	v_and_b32_e32 v6, 0xffffff80, v6
	s_waitcnt lgkmcnt(0)
	v_cvt_pk_bf16_f32 v1, v10, v12
	ds_read2_b32 v[14:15], v111 offset0:132 offset1:140
	ds_read2_b32 v[16:17], v111 offset0:165 offset1:173
	ds_read2_b32 v[18:19], v111 offset0:198 offset1:206
	ds_read2_b32 v[20:21], v111 offset0:231 offset1:239
	v_cmp_gt_u32_e32 vcc, s1, v8
	v_or_b32_e32 v10, v6, v8
	v_add3_u32 v6, v8, v6, s2
	v_cndmask_b32_e32 v22, v6, v10, vcc
	v_ashrrev_i32_e32 v23, 31, v22
	v_lshlrev_b64 v[22:23], 9, v[22:23]
	v_lshl_add_u64 v[22:23], v[4:5], 0, v[22:23]
	v_add_u32_e32 v6, s0, v112
	s_waitcnt lgkmcnt(2)
	v_cvt_pk_bf16_f32 v2, v14, v16
	s_waitcnt lgkmcnt(0)
	v_cvt_pk_bf16_f32 v3, v18, v20
	global_store_dwordx4 v[22:23], v[0:3], off nt
	s_nop 1
	v_cvt_pk_bf16_f32 v0, v9, v7
	v_and_b32_e32 v7, 0xff, v6
	v_ashrrev_i32_e32 v6, 1, v6
	v_and_b32_e32 v6, 0xffffff80, v6
	v_cmp_gt_u32_e32 vcc, s1, v7
	v_or_b32_e32 v8, v6, v7
	v_add3_u32 v6, v7, v6, s2
	v_cndmask_b32_e32 v6, v6, v8, vcc
	v_ashrrev_i32_e32 v7, 31, v6
	v_lshlrev_b64 v[6:7], 9, v[6:7]
	v_lshl_add_u64 v[6:7], v[4:5], 0, v[6:7]
	v_cvt_pk_bf16_f32 v1, v11, v13
	v_cvt_pk_bf16_f32 v2, v15, v17
	v_cvt_pk_bf16_f32 v3, v19, v21
	global_store_dwordx4 v[6:7], v[0:3], off nt
	ds_read2_b32 v[6:7], v111 offset0:16 offset1:24
	ds_read2_b32 v[8:9], v111 offset0:49 offset1:57
	ds_read2_b32 v[10:11], v111 offset0:82 offset1:90
	ds_read2_b32 v[12:13], v111 offset0:115 offset1:123
	s_waitcnt lgkmcnt(2)
	v_cvt_pk_bf16_f32 v0, v6, v8
	v_add_u32_e32 v6, s0, v113
	v_and_b32_e32 v8, 0xff, v6
	v_ashrrev_i32_e32 v6, 1, v6
	v_and_b32_e32 v6, 0xffffff80, v6
	s_waitcnt lgkmcnt(0)
	v_cvt_pk_bf16_f32 v1, v10, v12
	ds_read2_b32 v[14:15], v111 offset0:148 offset1:156
	ds_read2_b32 v[16:17], v111 offset0:181 offset1:189
	ds_read2_b32 v[18:19], v111 offset0:214 offset1:222
	ds_read2_b32 v[20:21], v111 offset0:247 offset1:255
	v_cmp_gt_u32_e32 vcc, s1, v8
	v_or_b32_e32 v10, v6, v8
	v_add3_u32 v6, v8, v6, s2
	v_cndmask_b32_e32 v22, v6, v10, vcc
	v_ashrrev_i32_e32 v23, 31, v22
	v_lshlrev_b64 v[22:23], 9, v[22:23]
	v_lshl_add_u64 v[22:23], v[4:5], 0, v[22:23]
	v_add_u32_e32 v6, s0, v114
	s_waitcnt lgkmcnt(2)
	v_cvt_pk_bf16_f32 v2, v14, v16
	s_waitcnt lgkmcnt(0)
	v_cvt_pk_bf16_f32 v3, v18, v20
	global_store_dwordx4 v[22:23], v[0:3], off nt
	s_nop 1
	v_cvt_pk_bf16_f32 v0, v7, v9
	v_and_b32_e32 v7, 0xff, v6
	v_ashrrev_i32_e32 v6, 1, v6
	v_and_b32_e32 v6, 0xffffff80, v6
	v_cmp_gt_u32_e32 vcc, s1, v7
	v_or_b32_e32 v8, v6, v7
	v_add3_u32 v6, v7, v6, s2
	v_cndmask_b32_e32 v6, v6, v8, vcc
	v_ashrrev_i32_e32 v7, 31, v6
	v_lshlrev_b64 v[6:7], 9, v[6:7]
	v_lshl_add_u64 v[4:5], v[4:5], 0, v[6:7]
	v_cvt_pk_bf16_f32 v1, v11, v13
	v_cvt_pk_bf16_f32 v2, v15, v17
	v_cvt_pk_bf16_f32 v3, v19, v21
	global_store_dwordx4 v[4:5], v[0:3], off nt
	s_waitcnt lgkmcnt(0)

; #define LAS __attribute__((address_space(3)))
; template <int QPERM>
; __device__ __forceinline__ void transpose_item(const float* W, int K, int N, bf16_t* WT, LAS float* scr, int item, int lane) {
;     const int nblk = N / 32, kb = item / nblk, nb = item % nblk, k0 = 64 * kb, n0 = 32 * nb;
; #pragma unroll 8
;     for (int i = 0; i < 32; ++i) { const int kk = 2 * i + (lane >> 5); scr[kk * 33 + (lane & 31)] = W[(size_t)(k0 + kk) * N + n0 + (lane & 31)]; }
;     asm volatile("s_waitcnt lgkmcnt(0)" ::: "memory");
.LBB0_348:
	s_lshl_b32 s11, s10, 1
	s_lshl_b32 s12, s1, 1
	v_add_u32_e32 v18, s11, v2
	v_add_u32_e32 v20, s12, v3
	v_mad_i64_i32 v[18:19], s[14:15], v18, s2, v[0:1]
	v_mad_i64_i32 v[20:21], s[14:15], v20, s2, v[0:1]
	global_load_dword v24, v[18:19], off nt
	global_load_dword v25, v[20:21], off nt
	v_add_u32_e32 v23, s11, v96
	v_add_u32_e32 v22, s12, v69
	v_mad_u64_u32 v[18:19], s[14:15], v23, s83, v[68:69]
	v_mad_u64_u32 v[20:21], s[14:15], v22, s83, v[68:69]
	v_add_u32_e32 v23, s11, v84
	v_add_u32_e32 v22, s12, v85
	s_add_i32 s10, s10, 16
	s_add_i32 s1, s1, 16
	s_add_i32 s0, s0, -16
	s_cmp_lg_u32 s0, 0
	s_waitcnt vmcnt(0)
	ds_write_b32 v18, v24
	s_waitcnt vmcnt(0)
	ds_write_b32 v20, v25
	v_add_u32_e32 v18, s11, v4
	v_add_u32_e32 v20, s12, v5
	v_mad_i64_i32 v[18:19], s[14:15], v18, s2, v[0:1]
	v_mad_i64_i32 v[20:21], s[14:15], v20, s2, v[0:1]
	global_load_dword v24, v[18:19], off nt
	global_load_dword v25, v[20:21], off nt
	v_mad_u64_u32 v[18:19], s[14:15], v23, s83, v[68:69]
	v_mad_u64_u32 v[20:21], s[14:15], v22, s83, v[68:69]
	v_add_u32_e32 v23, s11, v86
	v_add_u32_e32 v22, s12, v87
	s_waitcnt vmcnt(0)
	ds_write_b32 v18, v24
	s_waitcnt vmcnt(0)
	ds_write_b32 v20, v25
	v_add_u32_e32 v18, s11, v6
	v_add_u32_e32 v20, s12, v7
	v_mad_i64_i32 v[18:19], s[14:15], v18, s2, v[0:1]
	v_mad_i64_i32 v[20:21], s[14:15], v20, s2, v[0:1]
	global_load_dword v24, v[18:19], off nt
	global_load_dword v25, v[20:21], off nt
	v_mad_u64_u32 v[18:19], s[14:15], v23, s83, v[68:69]
	v_mad_u64_u32 v[20:21], s[14:15], v22, s83, v[68:69]
	v_add_u32_e32 v23, s11, v88
	v_add_u32_e32 v22, s12, v89
	s_waitcnt vmcnt(0)
	ds_write_b32 v18, v24
	s_waitcnt vmcnt(0)
	ds_write_b32 v20, v25
	v_add_u32_e32 v18, s11, v8
	v_add_u32_e32 v20, s12, v9
	v_mad_i64_i32 v[18:19], s[14:15], v18, s2, v[0:1]
	v_mad_i64_i32 v[20:21], s[14:15], v20, s2, v[0:1]
	global_load_dword v24, v[18:19], off nt
	global_load_dword v25, v[20:21], off nt
	v_mad_u64_u32 v[18:19], s[14:15], v23, s83, v[68:69]
	v_mad_u64_u32 v[20:21], s[14:15], v22, s83, v[68:69]
	v_add_u32_e32 v23, s11, v90
	v_add_u32_e32 v22, s12, v91
	s_waitcnt vmcnt(0)
	ds_write_b32 v18, v24
	s_waitcnt vmcnt(0)
	ds_write_b32 v20, v25
	v_add_u32_e32 v18, s11, v10
	v_add_u32_e32 v20, s12, v11
	v_mad_i64_i32 v[18:19], s[14:15], v18, s2, v[0:1]
	v_mad_i64_i32 v[20:21], s[14:15], v20, s2, v[0:1]
	global_load_dword v24, v[18:19], off nt
	global_load_dword v25, v[20:21], off nt
	v_mad_u64_u32 v[18:19], s[14:15], v23, s83, v[68:69]
	v_mad_u64_u32 v[20:21], s[14:15], v22, s83, v[68:69]
	v_add_u32_e32 v23, s11, v92
	v_add_u32_e32 v22, s12, v93
	s_waitcnt vmcnt(0)
	ds_write_b32 v18, v24
	s_waitcnt vmcnt(0)
	ds_write_b32 v20, v25
	v_add_u32_e32 v18, s11, v12
	v_add_u32_e32 v20, s12, v13
	v_mad_i64_i32 v[18:19], s[14:15], v18, s2, v[0:1]
	v_mad_i64_i32 v[20:21], s[14:15], v20, s2, v[0:1]
	global_load_dword v24, v[18:19], off nt
	global_load_dword v25, v[20:21], off nt
	v_mad_u64_u32 v[18:19], s[14:15], v23, s83, v[68:69]
	v_mad_u64_u32 v[20:21], s[14:15], v22, s83, v[68:69]
	v_add_u32_e32 v23, s11, v94
	v_add_u32_e32 v22, s12, v95
	s_waitcnt vmcnt(0)
	ds_write_b32 v18, v24
	s_waitcnt vmcnt(0)
	ds_write_b32 v20, v25
	v_add_u32_e32 v18, s11, v14
	v_add_u32_e32 v20, s12, v15
	v_mad_i64_i32 v[18:19], s[14:15], v18, s2, v[0:1]
	v_mad_i64_i32 v[20:21], s[14:15], v20, s2, v[0:1]
	global_load_dword v24, v[18:19], off nt
	global_load_dword v25, v[20:21], off nt
	v_mad_u64_u32 v[18:19], s[14:15], v23, s83, v[68:69]
	v_mad_u64_u32 v[20:21], s[14:15], v22, s83, v[68:69]
	v_add_u32_e32 v22, s12, v97
	v_add_u32_e32 v23, s11, v100
	s_waitcnt vmcnt(0)
	ds_write_b32 v18, v24
	s_waitcnt vmcnt(0)
	ds_write_b32 v20, v25
	v_add_u32_e32 v18, s11, v16
	v_add_u32_e32 v20, s12, v17
	v_mad_i64_i32 v[18:19], s[12:13], v18, s2, v[0:1]
	v_mad_i64_i32 v[20:21], s[12:13], v20, s2, v[0:1]
	global_load_dword v24, v[18:19], off nt
	global_load_dword v25, v[20:21], off nt
	v_mad_u64_u32 v[18:19], s[12:13], v23, s83, v[68:69]
	v_mad_u64_u32 v[20:21], s[12:13], v22, s83, v[68:69]
	s_waitcnt vmcnt(0)
	ds_write_b32 v18, v24
	s_waitcnt vmcnt(0)
	ds_write_b32 v20, v25
	s_cbranch_scc1 .LBB0_348
; #define LAS __attribute__((address_space(3)))
; __device__ __forceinline__ unsigned pk2(float lo, float hi) { unsigned r; asm("v_cvt_pk_bf16_f32 %0, %1, %2" : "=v"(r) : "v"(lo), "v"(hi)); return r; }
; template <int QPERM>
; __device__ __forceinline__ void transpose_item(const float* W, int K, int N, bf16_t* WT, LAS float* scr, int item, int lane) {
;     ...
;     const int c = lane & 7;
; #pragma unroll
;     for (int j = 0; j < 4; ++j) { const int n = (lane >> 3) + 8 * j; const LAS float* s = scr + (8 * c) * 33 + n;
;         u32x4 o; o.x = pk2(s[0 * 33], s[1 * 33]); o.y = pk2(s[2 * 33], s[3 * 33]); o.z = pk2(s[4 * 33], s[5 * 33]); o.w = pk2(s[6 * 33], s[7 * 33]);
;         int dn = n0 + n;
;         if (QPERM == 1) { const int h = dn / 192, d = dn % 192; if (d >= 128) { const int jj = d - 128, a = jj >> 5, p = (jj >> 4) & 1, f = jj & 15; dn = h * 192 + 128 + 2 * (a * 16 + f) + p; } }
;         if (QPERM == 2) { const int h = dn >> 8, j = dn & 255; dn = (j < 128) ? h * 128 + j : 512 + h * 128 + (j - 128); }
;         *(u32x4*)(WT + (size_t)dn * K + k0 + 8 * c) = o; }
	s_waitcnt lgkmcnt(0)
	ds_read2_b32 v[0:1], v111 offset1:33
	ds_read2_b32 v[2:3], v111 offset0:66 offset1:99
	s_waitcnt lgkmcnt(1)
	v_cvt_pk_bf16_f32 v0, v0, v1
	s_waitcnt lgkmcnt(0)
	v_cvt_pk_bf16_f32 v1, v2, v3
	ds_read2_b32 v[2:3], v111 offset0:132 offset1:165
	ds_read2_b32 v[4:5], v111 offset0:198 offset1:231
	v_add_u32_e32 v6, s8, v110
	s_mov_b32 s0, 0x2aaaaaab
	s_waitcnt lgkmcnt(1)
	v_cvt_pk_bf16_f32 v2, v2, v3
	s_waitcnt lgkmcnt(0)
	v_cvt_pk_bf16_f32 v3, v4, v5
	v_mul_hi_i32 v4, v6, s0
	v_lshrrev_b32_e32 v5, 31, v4
	v_lshrrev_b32_e32 v4, 5, v4
	v_add_u32_e32 v4, v4, v5
	s_movk_i32 s0, 0xc0
	v_mul_lo_u32 v4, v4, s0
	v_sub_u32_e32 v4, v6, v4
	s_movk_i32 s0, 0x7f
	v_cmp_lt_i32_e32 vcc, s0, v4
	s_and_saveexec_b64 s[0:1], vcc
	v_bfe_u32 v5, v4, 4, 1
	v_lshlrev_b32_e32 v7, 1, v4
	v_and_b32_e32 v8, 0x7fffffe0, v4
	v_sub_u32_e32 v4, v6, v4
	v_and_b32_e32 v7, 30, v7
	v_add_u32_e32 v4, v4, v8
	v_add3_u32 v6, v4, v7, v5
	s_or_b64 exec, exec, s[0:1]
	s_mov_b32 s1, s3
	s_lshl_b32 s2, s9, 1
	v_writelane_b32 v253, s0, 32
	v_lshl_add_u64 v[4:5], v[78:79], 0, s[2:3]
	s_mov_b32 s2, 0x2aaaaaab
	v_writelane_b32 v253, s1, 33
	s_movk_i32 s0, 0x300
	v_mad_i64_i32 v[6:7], s[0:1], v6, s0, v[4:5]
	global_store_dwordx4 v[6:7], v[0:3], off nt
	ds_read2_b32 v[0:1], v111 offset0:8 offset1:41
	ds_read2_b32 v[2:3], v111 offset0:74 offset1:107
	s_waitcnt lgkmcnt(1)
	v_cvt_pk_bf16_f32 v0, v0, v1
	s_waitcnt lgkmcnt(0)
	v_cvt_pk_bf16_f32 v1, v2, v3
	ds_read2_b32 v[2:3], v111 offset0:140 offset1:173
	ds_read2_b32 v[6:7], v111 offset0:206 offset1:239
	s_waitcnt lgkmcnt(1)
	v_cvt_pk_bf16_f32 v2, v2, v3
	s_waitcnt lgkmcnt(0)
	v_cvt_pk_bf16_f32 v3, v6, v7
	v_add_u32_e32 v6, s8, v112
	v_mul_hi_i32 v7, v6, s2
	v_lshrrev_b32_e32 v8, 31, v7
	v_lshrrev_b32_e32 v7, 5, v7
	v_add_u32_e32 v7, v7, v8
	s_movk_i32 s0, 0xc0
	v_mul_lo_u32 v7, v7, s0
	v_sub_u32_e32 v7, v6, v7
	s_movk_i32 s0, 0x7f
	v_cmp_lt_i32_e32 vcc, s0, v7
	s_and_saveexec_b64 s[0:1], vcc
	v_lshlrev_b32_e32 v9, 1, v7
	v_and_b32_e32 v10, 0x7fffffe0, v7
	v_sub_u32_e32 v6, v6, v7
	v_bfe_u32 v8, v7, 4, 1
	v_and_b32_e32 v9, 30, v9
	v_add_u32_e32 v6, v6, v10
	v_add3_u32 v6, v6, v9, v8
	s_or_b64 exec, exec, s[0:1]
	s_movk_i32 s0, 0x300
	v_mad_i64_i32 v[6:7], s[0:1], v6, s0, v[4:5]
	global_store_dwordx4 v[6:7], v[0:3], off nt
	ds_read2_b32 v[0:1], v111 offset0:16 offset1:49
	ds_read2_b32 v[2:3], v111 offset0:82 offset1:115
	s_waitcnt lgkmcnt(1)
	v_cvt_pk_bf16_f32 v0, v0, v1
	s_waitcnt lgkmcnt(0)
	v_cvt_pk_bf16_f32 v1, v2, v3
	ds_read2_b32 v[2:3], v111 offset0:148 offset1:181
	ds_read2_b32 v[6:7], v111 offset0:214 offset1:247
	s_waitcnt lgkmcnt(1)
	v_cvt_pk_bf16_f32 v2, v2, v3
	s_waitcnt lgkmcnt(0)
	v_cvt_pk_bf16_f32 v3, v6, v7
	v_add_u32_e32 v6, s8, v113
	v_mul_hi_i32 v7, v6, s2
	v_lshrrev_b32_e32 v8, 31, v7
	v_lshrrev_b32_e32 v7, 5, v7
	v_add_u32_e32 v7, v7, v8
	s_movk_i32 s0, 0xc0
	v_mul_lo_u32 v7, v7, s0
	v_sub_u32_e32 v7, v6, v7
	s_movk_i32 s0, 0x7f
	v_cmp_lt_i32_e32 vcc, s0, v7
	s_and_saveexec_b64 s[0:1], vcc
	v_lshlrev_b32_e32 v9, 1, v7
	v_and_b32_e32 v10, 0x7fffffe0, v7
	v_sub_u32_e32 v6, v6, v7
	v_bfe_u32 v8, v7, 4, 1
	v_and_b32_e32 v9, 30, v9
	v_add_u32_e32 v6, v6, v10
	v_add3_u32 v6, v6, v9, v8
	s_or_b64 exec, exec, s[0:1]
	s_movk_i32 s0, 0x300
	v_mad_i64_i32 v[6:7], s[0:1], v6, s0, v[4:5]
	global_store_dwordx4 v[6:7], v[0:3], off nt
	ds_read2_b32 v[0:1], v111 offset0:24 offset1:57
	ds_read2_b32 v[2:3], v111 offset0:90 offset1:123
	s_waitcnt lgkmcnt(1)
	v_cvt_pk_bf16_f32 v0, v0, v1
	s_waitcnt lgkmcnt(0)
	v_cvt_pk_bf16_f32 v1, v2, v3
	ds_read2_b32 v[2:3], v111 offset0:156 offset1:189
	ds_read2_b32 v[6:7], v111 offset0:222 offset1:255
	s_waitcnt lgkmcnt(1)
	v_cvt_pk_bf16_f32 v2, v2, v3
	s_waitcnt lgkmcnt(0)
	v_cvt_pk_bf16_f32 v3, v6, v7
	v_add_u32_e32 v6, s8, v114
	v_mul_hi_i32 v7, v6, s2
	v_lshrrev_b32_e32 v8, 31, v7
	v_lshrrev_b32_e32 v7, 5, v7
	v_add_u32_e32 v7, v7, v8
	s_movk_i32 s0, 0xc0
	v_mul_lo_u32 v7, v7, s0
	v_sub_u32_e32 v7, v6, v7
	s_movk_i32 s0, 0x7f
	v_cmp_lt_i32_e32 vcc, s0, v7
	s_and_saveexec_b64 s[0:1], vcc
	v_lshlrev_b32_e32 v9, 1, v7
	v_and_b32_e32 v10, 0x7fffffe0, v7
	v_sub_u32_e32 v6, v6, v7
	v_bfe_u32 v8, v7, 4, 1
	v_and_b32_e32 v9, 30, v9
	v_add_u32_e32 v6, v6, v10
	v_add3_u32 v6, v6, v9, v8
	s_or_b64 exec, exec, s[0:1]
	s_movk_i32 s0, 0x300
	v_mad_i64_i32 v[4:5], s[0:1], v6, s0, v[4:5]
	global_store_dwordx4 v[4:5], v[0:3], off nt
	s_waitcnt lgkmcnt(0)

; #define LAS __attribute__((address_space(3)))
; __device__ __forceinline__ void transpose_item_fp8(const float* W, int K, int N, unsigned char* WT, float q, LAS float* scr, int item, int lane) {
;     const int nblk = N / 32, kb = item / nblk, nb = item % nblk, k0 = 64 * kb, n0 = 32 * nb;
; #pragma unroll 8
;     for (int i = 0; i < 32; ++i) { const int kk = 2 * i + (lane >> 5); scr[kk * 33 + (lane & 31)] = W[(size_t)(k0 + kk) * N + n0 + (lane & 31)]; }
.LBB0_361:
	s_lshl_b32 s11, s1, 1
	s_lshl_b32 s12, s0, 1
	v_add_u32_e32 v18, s11, v2
	v_add_u32_e32 v20, s12, v3
	v_mad_i64_i32 v[18:19], s[14:15], v18, s82, v[0:1]
	v_mad_i64_i32 v[20:21], s[14:15], v20, s82, v[0:1]
	global_load_dword v24, v[18:19], off nt
	global_load_dword v25, v[20:21], off nt
	v_add_u32_e32 v23, s11, v96
	v_add_u32_e32 v22, s12, v69
	v_mad_u64_u32 v[18:19], s[14:15], v23, s83, v[68:69]
	v_mad_u64_u32 v[20:21], s[14:15], v22, s83, v[68:69]
	v_add_u32_e32 v23, s11, v84
	v_add_u32_e32 v22, s12, v85
	s_add_i32 s1, s1, 16
	s_add_i32 s0, s0, 16
	s_add_i32 s9, s9, -16
	s_cmp_lg_u32 s9, 0
	s_waitcnt vmcnt(0)
	ds_write_b32 v18, v24
	s_waitcnt vmcnt(0)
	ds_write_b32 v20, v25
	v_add_u32_e32 v18, s11, v4
	v_add_u32_e32 v20, s12, v5
	v_mad_i64_i32 v[18:19], s[14:15], v18, s82, v[0:1]
	v_mad_i64_i32 v[20:21], s[14:15], v20, s82, v[0:1]
	global_load_dword v24, v[18:19], off nt
	global_load_dword v25, v[20:21], off nt
	v_mad_u64_u32 v[18:19], s[14:15], v23, s83, v[68:69]
	v_mad_u64_u32 v[20:21], s[14:15], v22, s83, v[68:69]
	v_add_u32_e32 v23, s11, v86
	v_add_u32_e32 v22, s12, v87
	s_waitcnt vmcnt(0)
	ds_write_b32 v18, v24
	s_waitcnt vmcnt(0)
	ds_write_b32 v20, v25
	v_add_u32_e32 v18, s11, v6
	v_add_u32_e32 v20, s12, v7
	v_mad_i64_i32 v[18:19], s[14:15], v18, s82, v[0:1]
	v_mad_i64_i32 v[20:21], s[14:15], v20, s82, v[0:1]
	global_load_dword v24, v[18:19], off nt
	global_load_dword v25, v[20:21], off nt
	v_mad_u64_u32 v[18:19], s[14:15], v23, s83, v[68:69]
	v_mad_u64_u32 v[20:21], s[14:15], v22, s83, v[68:69]
	v_add_u32_e32 v23, s11, v88
	v_add_u32_e32 v22, s12, v89
	s_waitcnt vmcnt(0)
	ds_write_b32 v18, v24
	s_waitcnt vmcnt(0)
	ds_write_b32 v20, v25
	v_add_u32_e32 v18, s11, v8
	v_add_u32_e32 v20, s12, v9
	v_mad_i64_i32 v[18:19], s[14:15], v18, s82, v[0:1]
	v_mad_i64_i32 v[20:21], s[14:15], v20, s82, v[0:1]
	global_load_dword v24, v[18:19], off nt
	global_load_dword v25, v[20:21], off nt
	v_mad_u64_u32 v[18:19], s[14:15], v23, s83, v[68:69]
	v_mad_u64_u32 v[20:21], s[14:15], v22, s83, v[68:69]
	v_add_u32_e32 v23, s11, v90
	v_add_u32_e32 v22, s12, v91
	s_waitcnt vmcnt(0)
	ds_write_b32 v18, v24
	s_waitcnt vmcnt(0)
	ds_write_b32 v20, v25
	v_add_u32_e32 v18, s11, v10
	v_add_u32_e32 v20, s12, v11
	v_mad_i64_i32 v[18:19], s[14:15], v18, s82, v[0:1]
	v_mad_i64_i32 v[20:21], s[14:15], v20, s82, v[0:1]
	global_load_dword v24, v[18:19], off nt
	global_load_dword v25, v[20:21], off nt
	v_mad_u64_u32 v[18:19], s[14:15], v23, s83, v[68:69]
	v_mad_u64_u32 v[20:21], s[14:15], v22, s83, v[68:69]
	v_add_u32_e32 v23, s11, v92
	v_add_u32_e32 v22, s12, v93
	s_waitcnt vmcnt(0)
	ds_write_b32 v18, v24
	s_waitcnt vmcnt(0)
	ds_write_b32 v20, v25
	v_add_u32_e32 v18, s11, v12
	v_add_u32_e32 v20, s12, v13
	v_mad_i64_i32 v[18:19], s[14:15], v18, s82, v[0:1]
	v_mad_i64_i32 v[20:21], s[14:15], v20, s82, v[0:1]
	global_load_dword v24, v[18:19], off nt
	global_load_dword v25, v[20:21], off nt
	v_mad_u64_u32 v[18:19], s[14:15], v23, s83, v[68:69]
	v_mad_u64_u32 v[20:21], s[14:15], v22, s83, v[68:69]
	v_add_u32_e32 v23, s11, v94
	v_add_u32_e32 v22, s12, v95
	s_waitcnt vmcnt(0)
	ds_write_b32 v18, v24
	s_waitcnt vmcnt(0)
	ds_write_b32 v20, v25
	v_add_u32_e32 v18, s11, v14
	v_add_u32_e32 v20, s12, v15
	v_mad_i64_i32 v[18:19], s[14:15], v18, s82, v[0:1]
	v_mad_i64_i32 v[20:21], s[14:15], v20, s82, v[0:1]
	global_load_dword v24, v[18:19], off nt
	global_load_dword v25, v[20:21], off nt
	v_mad_u64_u32 v[18:19], s[14:15], v23, s83, v[68:69]
	v_mad_u64_u32 v[20:21], s[14:15], v22, s83, v[68:69]
	v_add_u32_e32 v22, s12, v97
	v_add_u32_e32 v23, s11, v100
	s_waitcnt vmcnt(0)
	ds_write_b32 v18, v24
	s_waitcnt vmcnt(0)
	ds_write_b32 v20, v25
	v_add_u32_e32 v18, s11, v16
	v_add_u32_e32 v20, s12, v17
	v_mad_i64_i32 v[18:19], s[12:13], v18, s82, v[0:1]
	v_mad_i64_i32 v[20:21], s[12:13], v20, s82, v[0:1]
	global_load_dword v24, v[18:19], off nt
	global_load_dword v25, v[20:21], off nt
	v_mad_u64_u32 v[18:19], s[12:13], v23, s83, v[68:69]
	v_mad_u64_u32 v[20:21], s[12:13], v22, s83, v[68:69]
	s_waitcnt vmcnt(0)
	ds_write_b32 v18, v24
	s_waitcnt vmcnt(0)
	ds_write_b32 v20, v25
	s_cbranch_scc1 .LBB0_361
; #define LAS __attribute__((address_space(3)))
; __device__ __forceinline__ unsigned pk4_fp8(float x0, float x1, float x2, float x3) { int w = 0; w = __builtin_amdgcn_cvt_pk_fp8_f32(x0, x1, w, false); w = __builtin_amdgcn_cvt_pk_fp8_f32(x2, x3, w, true); return (unsigned)w; }
; __device__ __forceinline__ void transpose_item_fp8(const float* W, int K, int N, unsigned char* WT, float q, LAS float* scr, int item, int lane) {
;     ...
;     asm volatile("s_waitcnt lgkmcnt(0)" ::: "memory");
;     const int c = lane & 7;
; #pragma unroll
;     for (int j = 0; j < 4; ++j) { const int n = (lane >> 3) + 8 * j; const LAS float* s = scr + (8 * c) * 33 + n;
;         u32x2 o; o.x = pk4_fp8(s[0 * 33] * q, s[1 * 33] * q, s[2 * 33] * q, s[3 * 33] * q); o.y = pk4_fp8(s[4 * 33] * q, s[5 * 33] * q, s[6 * 33] * q, s[7 * 33] * q);
;         *(u32x2*)(WT + (size_t)(n0 + n) * K + k0 + 8 * c) = o; }
;     asm volatile("s_waitcnt lgkmcnt(0)" ::: "memory");
	s_waitcnt lgkmcnt(0)
	ds_read2_b32 v[2:3], v111 offset1:8
	ds_read2_b32 v[4:5], v111 offset0:33 offset1:41
	ds_read2_b32 v[12:13], v111 offset0:132 offset1:140
	ds_read2_b32 v[14:15], v111 offset0:165 offset1:173
	ds_read2_b32 v[6:7], v111 offset0:66 offset1:74
	ds_read2_b32 v[8:9], v111 offset0:99 offset1:107
	s_waitcnt lgkmcnt(5)
	v_mul_f32_e32 v2, 0x43000000, v2
	s_waitcnt lgkmcnt(4)
	v_mul_f32_e32 v4, 0x43000000, v4
	v_mov_b32_e32 v10, v153
	ds_read2_b32 v[16:17], v111 offset0:198 offset1:206
	ds_read2_b32 v[18:19], v111 offset0:231 offset1:239
	v_cvt_pk_fp8_f32 v10, v2, v4
	s_waitcnt lgkmcnt(5)
	v_mul_f32_e32 v2, 0x43000000, v12
	s_waitcnt lgkmcnt(4)
	v_mul_f32_e32 v4, 0x43000000, v14
	v_mov_b32_e32 v11, v153
	v_cvt_pk_fp8_f32 v11, v2, v4
	v_mul_f32_e32 v3, 0x43000000, v3
	v_mul_f32_e32 v4, 0x43000000, v5
	v_mov_b32_e32 v2, v153
	v_cvt_pk_fp8_f32 v2, v3, v4
	s_waitcnt lgkmcnt(3)
	v_mul_f32_e32 v6, 0x43000000, v6
	s_waitcnt lgkmcnt(2)
	v_mul_f32_e32 v8, 0x43000000, v8
	v_cvt_pk_fp8_f32 v10, v6, v8 op_sel:[0,0,1]
	s_waitcnt lgkmcnt(1)
	v_mul_f32_e32 v6, 0x43000000, v16
	s_waitcnt lgkmcnt(0)
	v_mul_f32_e32 v8, 0x43000000, v18
	v_cvt_pk_fp8_f32 v11, v6, v8 op_sel:[0,0,1]
	v_mul_f32_e32 v5, 0x43000000, v7
	v_mul_f32_e32 v6, 0x43000000, v9
	v_cvt_pk_fp8_f32 v2, v5, v6 op_sel:[0,0,1]
	v_mul_f32_e32 v4, 0x43000000, v13
	v_mul_f32_e32 v5, 0x43000000, v15
	v_mov_b32_e32 v3, v153
	v_cvt_pk_fp8_f32 v3, v4, v5
	v_mul_f32_e32 v6, 0x43000000, v17
	v_mul_f32_e32 v7, 0x43000000, v19
	v_add_u32_e32 v4, s8, v112
	v_cvt_pk_fp8_f32 v3, v6, v7 op_sel:[0,0,1]
	s_ashr_i32 s11, s10, 31
	v_ashrrev_i32_e32 v5, 31, v4
	v_lshl_add_u64 v[0:1], v[82:83], 0, s[10:11]
	v_lshlrev_b64 v[4:5], 10, v[4:5]
	v_lshl_add_u64 v[4:5], v[0:1], 0, v[4:5]
	global_store_dwordx2 v[4:5], v[2:3], off nt
	ds_read2_b32 v[2:3], v111 offset0:16 offset1:24
	ds_read2_b32 v[4:5], v111 offset0:49 offset1:57
	v_add_u32_e32 v20, s8, v110
	ds_read2_b32 v[12:13], v111 offset0:148 offset1:156
	ds_read2_b32 v[14:15], v111 offset0:181 offset1:189
	v_ashrrev_i32_e32 v21, 31, v20
	v_lshlrev_b64 v[20:21], 10, v[20:21]
	v_lshl_add_u64 v[20:21], v[0:1], 0, v[20:21]
	ds_read2_b32 v[6:7], v111 offset0:82 offset1:90
	ds_read2_b32 v[8:9], v111 offset0:115 offset1:123
	global_store_dwordx2 v[20:21], v[10:11], off nt
	s_waitcnt lgkmcnt(5)
	v_mul_f32_e32 v2, 0x43000000, v2
	s_waitcnt lgkmcnt(4)
	v_mul_f32_e32 v4, 0x43000000, v4
	v_mov_b32_e32 v10, v153
	ds_read2_b32 v[16:17], v111 offset0:214 offset1:222
	ds_read2_b32 v[18:19], v111 offset0:247 offset1:255
	v_cvt_pk_fp8_f32 v10, v2, v4
	s_waitcnt lgkmcnt(5)
	v_mul_f32_e32 v2, 0x43000000, v12
	s_waitcnt lgkmcnt(4)
	v_mul_f32_e32 v4, 0x43000000, v14
	v_mov_b32_e32 v11, v153
	v_cvt_pk_fp8_f32 v11, v2, v4
	v_mul_f32_e32 v3, 0x43000000, v3
	v_mul_f32_e32 v4, 0x43000000, v5
	v_mov_b32_e32 v2, v153
	v_cvt_pk_fp8_f32 v2, v3, v4
	s_waitcnt lgkmcnt(3)
	v_mul_f32_e32 v6, 0x43000000, v6
	s_waitcnt lgkmcnt(2)
	v_mul_f32_e32 v8, 0x43000000, v8
	v_cvt_pk_fp8_f32 v10, v6, v8 op_sel:[0,0,1]
	s_waitcnt lgkmcnt(1)
	v_mul_f32_e32 v6, 0x43000000, v16
	s_waitcnt lgkmcnt(0)
	v_mul_f32_e32 v8, 0x43000000, v18
	v_cvt_pk_fp8_f32 v11, v6, v8 op_sel:[0,0,1]
	v_mul_f32_e32 v5, 0x43000000, v7
	v_mul_f32_e32 v6, 0x43000000, v9
	v_cvt_pk_fp8_f32 v2, v5, v6 op_sel:[0,0,1]
	v_mul_f32_e32 v4, 0x43000000, v13
	v_mul_f32_e32 v5, 0x43000000, v15
	v_mov_b32_e32 v3, v153
	v_cvt_pk_fp8_f32 v3, v4, v5
	v_mul_f32_e32 v6, 0x43000000, v17
	v_mul_f32_e32 v7, 0x43000000, v19
	v_add_u32_e32 v20, s8, v113
	v_cvt_pk_fp8_f32 v3, v6, v7 op_sel:[0,0,1]
	v_add_u32_e32 v4, s8, v114
	v_ashrrev_i32_e32 v21, 31, v20
	v_ashrrev_i32_e32 v5, 31, v4
	v_lshlrev_b64 v[20:21], 10, v[20:21]
	v_lshlrev_b64 v[4:5], 10, v[4:5]
	v_lshl_add_u64 v[20:21], v[0:1], 0, v[20:21]
	v_lshl_add_u64 v[0:1], v[0:1], 0, v[4:5]
	global_store_dwordx2 v[20:21], v[10:11], off nt
	global_store_dwordx2 v[0:1], v[2:3], off nt
	s_waitcnt lgkmcnt(0)
	s_branch .LBB0_330

; #define LAS __attribute__((address_space(3)))
; __device__ __forceinline__ unsigned pk4_fp8(float x0, float x1, float x2, float x3) { int w = 0; w = __builtin_amdgcn_cvt_pk_fp8_f32(x0, x1, w, false); w = __builtin_amdgcn_cvt_pk_fp8_f32(x2, x3, w, true); return (unsigned)w; }
; __device__ __forceinline__ void transpose_item_fp8w(const float* W, int K, int N, unsigned char* WT, float q, LAS unsigned char* scr, int item, int lane) {
;     const int nblk = N / 128, kb = item / nblk, nb = item % nblk, k0 = 64 * kb, n0 = 128 * nb;
;     const int l5 = lane & 31, h = lane >> 5;
;     const float* src = W + (size_t)(k0 + 16 * h) * N + n0 + 4 * l5;
; #pragma unroll
;     for (int b = 0; b < 2; ++b) {
;         f32x4 x[16];
; #pragma unroll
;         for (int s_ = 0; s_ < 16; ++s_) x[s_] = *(const f32x4*)(src + (size_t)(32 * b + s_) * N);
; #pragma unroll
;         for (int i = 0; i < 4; ++i) {
;             u32x4 o;
;             o.x = pk4_fp8(x[0][i] * q, x[1][i] * q, x[2][i] * q, x[3][i] * q); o.y = pk4_fp8(x[4][i] * q, x[5][i] * q, x[6][i] * q, x[7][i] * q);
;             o.z = pk4_fp8(x[8][i] * q, x[9][i] * q, x[10][i] * q, x[11][i] * q); o.w = pk4_fp8(x[12][i] * q, x[13][i] * q, x[14][i] * q, x[15][i] * q);
;             *(LAS u32x4*)(scr + (l5 + 32 * i) * 80 + (2 * b + h) * 16) = o; }
.LBB0_662:
	s_cmpk_gt_i32 s5, 0x3df
	s_mov_b64 s[0:1], -1
	s_cbranch_scc0 .LBB0_694
	s_cmpk_gt_u32 s5, 0x46f
	s_cbranch_scc0 .LBB0_681
	s_cmpk_gt_u32 s5, 0x4ef
	s_cbranch_scc0 .LBB0_676
	s_cmpk_gt_u32 s5, 0x6ef
	s_cbranch_scc0 .LBB0_671
	s_cmpk_gt_u32 s5, 0x26ef
	v_lshlrev_b32_e32 v152, 2, v64
	v_add_u32_e32 v118, v102, v103
	s_cbranch_scc0 .LBB0_668
	s_add_i32 s4, s5, 0xffffd910
	v_readlane_b32 s2, v253, 32
	s_lshr_b32 s0, s4, 7
	v_readlane_b32 s3, v253, 33
	s_mov_b32 s11, s3
	s_add_i32 s10, s0, s56
	v_readlane_b32 s40, v253, 58
	s_lshl_b64 s[2:3], s[10:11], 20
	s_lshl_b64 s[0:1], s[10:11], 22
	v_readlane_b32 s54, v254, 8
	v_readlane_b32 s55, v254, 9
	s_add_u32 s8, s54, s0
	s_addc_u32 s9, s55, s1
	v_readlane_b32 s0, v246, 17
	s_add_u32 s1, s0, s2
	v_readlane_b32 s0, v246, 18
	s_addc_u32 s6, s0, s3
	s_lshl_b32 s0, s4, 6
	s_and_b32 s7, s0, 0x3c0
	v_add_u32_e32 v0, s7, v99
	s_lshl_b32 s0, s4, 3
	v_ashrrev_i32_e32 v1, 31, v0
	s_and_b32 s0, s0, 0x380
	v_lshlrev_b64 v[0:1], 12, v[0:1]
	v_lshl_add_u64 v[0:1], s[8:9], 0, v[0:1]
	s_lshl_b32 s10, s0, 2
	s_mov_b32 s3, s11
	v_readlane_b32 s41, v253, 59
	v_readlane_b32 s42, v253, 60
	v_readlane_b32 s43, v253, 61
	v_readlane_b32 s44, v253, 62
	v_readlane_b32 s45, v253, 63
	v_writelane_b32 v253, s2, 32
	v_lshl_add_u64 v[0:1], v[0:1], 0, s[10:11]
	v_lshl_add_u64 v[100:101], v[0:1], 0, v[152:153]
	v_writelane_b32 v253, s3, 33
	s_movk_i32 s2, 0x2000
	v_add_co_u32_e32 v8, vcc, s2, v100
	s_movk_i32 s2, 0x4000
	s_nop 0
	v_addc_co_u32_e32 v9, vcc, 0, v101, vcc
	v_add_co_u32_e32 v12, vcc, s2, v100
	s_movk_i32 s2, 0x6000
	s_nop 0
	v_addc_co_u32_e32 v13, vcc, 0, v101, vcc
	v_add_co_u32_e32 v24, vcc, s2, v100
	s_mov_b32 s2, 0x8000
	s_nop 0
	v_addc_co_u32_e32 v25, vcc, 0, v101, vcc
	v_add_co_u32_e32 v28, vcc, s2, v100
	s_mov_b32 s2, 0xa000
	s_nop 0
	v_addc_co_u32_e32 v29, vcc, 0, v101, vcc
	v_add_co_u32_e32 v40, vcc, s2, v100
	s_mov_b32 s2, 0xc000
	s_nop 0
	v_addc_co_u32_e32 v41, vcc, 0, v101, vcc
	global_load_dwordx4 v[0:3], v[100:101], off nt
	v_add_co_u32_e32 v44, vcc, s2, v100
	global_load_dwordx4 v[4:7], v[8:9], off offset:-4096 nt
	s_nop 0
	global_load_dwordx4 v[8:11], v[8:9], off nt
	s_nop 0
	global_load_dwordx4 v[16:19], v[12:13], off offset:-4096 nt
	s_nop 0
	global_load_dwordx4 v[12:15], v[12:13], off nt
	v_addc_co_u32_e32 v45, vcc, 0, v101, vcc
	s_mov_b32 s2, 0xe000
	global_load_dwordx4 v[20:23], v[24:25], off offset:-4096 nt
	s_nop 0
	global_load_dwordx4 v[24:27], v[24:25], off nt
	s_nop 0
	global_load_dwordx4 v[32:35], v[28:29], off offset:-4096 nt
	s_nop 0
	global_load_dwordx4 v[28:31], v[28:29], off nt
	v_add_co_u32_e32 v56, vcc, s2, v100
	global_load_dwordx4 v[36:39], v[40:41], off offset:-4096 nt
	s_nop 0
	global_load_dwordx4 v[40:43], v[40:41], off nt
	s_nop 0
	global_load_dwordx4 v[48:51], v[44:45], off offset:-4096 nt
	s_nop 0
	global_load_dwordx4 v[44:47], v[44:45], off nt
	v_addc_co_u32_e32 v57, vcc, 0, v101, vcc
	global_load_dwordx4 v[52:55], v[56:57], off offset:-4096 nt
	s_nop 0
	global_load_dwordx4 v[56:59], v[56:57], off nt
	s_mov_b32 s2, 0xf000
	v_add_co_u32_e32 v60, vcc, s2, v100
	v_mov_b32_e32 v120, v153
	s_nop 0
	v_addc_co_u32_e32 v61, vcc, 0, v101, vcc
	global_load_dwordx4 v[60:63], v[60:61], off nt
	v_mov_b32_e32 v121, v153
	v_mov_b32_e32 v122, v153
	v_mov_b32_e32 v123, v153
	s_mov_b32 s2, 0x21000
	v_readlane_b32 s46, v254, 0
	v_readlane_b32 s47, v254, 1
	v_readlane_b32 s48, v254, 2
	v_readlane_b32 s49, v254, 3
	v_readlane_b32 s50, v254, 4
	v_readlane_b32 s51, v254, 5
	v_readlane_b32 s52, v254, 6
	v_readlane_b32 s53, v254, 7
	s_waitcnt vmcnt(0)
	v_mul_f32_e32 v0, 0x43800000, v0
	v_mul_f32_e32 v4, 0x43800000, v4
	v_cvt_pk_fp8_f32 v120, v0, v4
	v_mul_f32_e32 v0, 0x43800000, v12
	v_mul_f32_e32 v8, 0x43800000, v8
	v_mul_f32_e32 v16, 0x43800000, v16
	v_mul_f32_e32 v4, 0x43800000, v20
	v_cvt_pk_fp8_f32 v121, v0, v4
	v_mul_f32_e32 v0, 0x43800000, v28
	v_cvt_pk_fp8_f32 v120, v8, v16 op_sel:[0,0,1]
	v_mul_f32_e32 v4, 0x43800000, v36
	v_cvt_pk_fp8_f32 v122, v0, v4
	v_mul_f32_e32 v0, 0x43800000, v44
	v_mul_f32_e32 v8, 0x43800000, v24
	v_mul_f32_e32 v4, 0x43800000, v52
	v_cvt_pk_fp8_f32 v123, v0, v4
	v_mul_f32_e32 v12, 0x43800000, v32
	v_cvt_pk_fp8_f32 v121, v8, v12 op_sel:[0,0,1]
	v_mul_f32_e32 v8, 0x43800000, v40
	v_mul_f32_e32 v12, 0x43800000, v48
	v_cvt_pk_fp8_f32 v122, v8, v12 op_sel:[0,0,1]
	v_mul_f32_e32 v8, 0x43800000, v56
	v_mul_f32_e32 v12, 0x43800000, v60
	v_cvt_pk_fp8_f32 v123, v8, v12 op_sel:[0,0,1]
	v_mul_f32_e32 v0, 0x43800000, v1
	v_mul_f32_e32 v1, 0x43800000, v5
	v_mul_f32_e32 v4, 0x43800000, v9
	ds_write_b128 v117, v[120:123]
	v_mov_b32_e32 v120, v153
	v_cvt_pk_fp8_f32 v120, v0, v1
	v_mul_f32_e32 v0, 0x43800000, v13
	v_mul_f32_e32 v1, 0x43800000, v21
	v_mov_b32_e32 v121, v153
	v_cvt_pk_fp8_f32 v121, v0, v1
	v_mul_f32_e32 v0, 0x43800000, v29
	v_mul_f32_e32 v1, 0x43800000, v37
	v_mov_b32_e32 v122, v153
	v_cvt_pk_fp8_f32 v122, v0, v1
	v_mul_f32_e32 v0, 0x43800000, v45
	v_mul_f32_e32 v1, 0x43800000, v53
	v_mov_b32_e32 v123, v153
	v_mul_f32_e32 v5, 0x43800000, v17
	v_cvt_pk_fp8_f32 v123, v0, v1
	v_cvt_pk_fp8_f32 v120, v4, v5 op_sel:[0,0,1]
	v_mul_f32_e32 v4, 0x43800000, v25
	v_mul_f32_e32 v5, 0x43800000, v33
	v_cvt_pk_fp8_f32 v121, v4, v5 op_sel:[0,0,1]
	v_mul_f32_e32 v4, 0x43800000, v41
	v_mul_f32_e32 v5, 0x43800000, v49
	v_cvt_pk_fp8_f32 v122, v4, v5 op_sel:[0,0,1]
	v_mul_f32_e32 v4, 0x43800000, v57
	v_mul_f32_e32 v5, 0x43800000, v61
	v_cvt_pk_fp8_f32 v123, v4, v5 op_sel:[0,0,1]
	v_mul_f32_e32 v0, 0x43800000, v2
	v_mul_f32_e32 v1, 0x43800000, v6
	v_mul_f32_e32 v2, 0x43800000, v10
	ds_write_b128 v117, v[120:123] offset:2560
	v_mov_b32_e32 v120, v153
	v_cvt_pk_fp8_f32 v120, v0, v1
; #define LAS __attribute__((address_space(3)))
; __device__ __forceinline__ unsigned pk4_fp8(float x0, float x1, float x2, float x3) { int w = 0; w = __builtin_amdgcn_cvt_pk_fp8_f32(x0, x1, w, false); w = __builtin_amdgcn_cvt_pk_fp8_f32(x2, x3, w, true); return (unsigned)w; }
; __device__ __forceinline__ void transpose_item_fp8w(const float* W, int K, int N, unsigned char* WT, float q, LAS unsigned char* scr, int item, int lane) {
;     ...
;     for (int b = 0; b < 2; ++b) {
;         f32x4 x[16];
; #pragma unroll
;         for (int s_ = 0; s_ < 16; ++s_) x[s_] = *(const f32x4*)(src + (size_t)(32 * b + s_) * N);
; #pragma unroll
;         for (int i = 0; i < 4; ++i) {
;             u32x4 o;
;             o.x = pk4_fp8(x[0][i] * q, x[1][i] * q, x[2][i] * q, x[3][i] * q); o.y = pk4_fp8(x[4][i] * q, x[5][i] * q, x[6][i] * q, x[7][i] * q);
;             o.z = pk4_fp8(x[8][i] * q, x[9][i] * q, x[10][i] * q, x[11][i] * q); o.w = pk4_fp8(x[12][i] * q, x[13][i] * q, x[14][i] * q, x[15][i] * q);
;             *(LAS u32x4*)(scr + (l5 + 32 * i) * 80 + (2 * b + h) * 16) = o; }
	v_mul_f32_e32 v0, 0x43800000, v14
	v_mul_f32_e32 v1, 0x43800000, v22
	v_mov_b32_e32 v121, v153
	v_cvt_pk_fp8_f32 v121, v0, v1
	v_mul_f32_e32 v0, 0x43800000, v30
	v_mul_f32_e32 v1, 0x43800000, v38
	v_mov_b32_e32 v122, v153
	v_cvt_pk_fp8_f32 v122, v0, v1
	v_mul_f32_e32 v0, 0x43800000, v46
	v_mul_f32_e32 v1, 0x43800000, v54
	v_mov_b32_e32 v123, v153
	v_mul_f32_e32 v4, 0x43800000, v18
	v_cvt_pk_fp8_f32 v123, v0, v1
	v_cvt_pk_fp8_f32 v120, v2, v4 op_sel:[0,0,1]
	v_mul_f32_e32 v2, 0x43800000, v26
	v_mul_f32_e32 v4, 0x43800000, v34
	v_cvt_pk_fp8_f32 v121, v2, v4 op_sel:[0,0,1]
	v_mul_f32_e32 v2, 0x43800000, v42
	v_mul_f32_e32 v4, 0x43800000, v50
	v_cvt_pk_fp8_f32 v122, v2, v4 op_sel:[0,0,1]
	v_mul_f32_e32 v2, 0x43800000, v58
	v_mul_f32_e32 v4, 0x43800000, v62
	v_cvt_pk_fp8_f32 v123, v2, v4 op_sel:[0,0,1]
	v_mul_f32_e32 v1, 0x43800000, v3
	v_mul_f32_e32 v2, 0x43800000, v7
	v_mov_b32_e32 v0, v153
	v_cvt_pk_fp8_f32 v0, v1, v2
	v_mul_f32_e32 v3, 0x43800000, v11
	v_mul_f32_e32 v4, 0x43800000, v19
	v_mul_f32_e32 v2, 0x43800000, v15
	v_cvt_pk_fp8_f32 v0, v3, v4 op_sel:[0,0,1]
	v_mul_f32_e32 v3, 0x43800000, v23
	v_mov_b32_e32 v1, v153
	v_cvt_pk_fp8_f32 v1, v2, v3
	v_mul_f32_e32 v4, 0x43800000, v27
	v_mul_f32_e32 v5, 0x43800000, v35
	v_mul_f32_e32 v3, 0x43800000, v31
	v_cvt_pk_fp8_f32 v1, v4, v5 op_sel:[0,0,1]
	v_mul_f32_e32 v4, 0x43800000, v39
	v_mov_b32_e32 v2, v153
	v_cvt_pk_fp8_f32 v2, v3, v4
	v_mul_f32_e32 v5, 0x43800000, v43
	v_mul_f32_e32 v6, 0x43800000, v51
	v_mul_f32_e32 v4, 0x43800000, v47
	v_cvt_pk_fp8_f32 v2, v5, v6 op_sel:[0,0,1]
	v_mul_f32_e32 v5, 0x43800000, v55
	v_mov_b32_e32 v3, v153
	v_cvt_pk_fp8_f32 v3, v4, v5
	v_mul_f32_e32 v6, 0x43800000, v59
	v_mul_f32_e32 v7, 0x43800000, v63
	ds_write_b128 v117, v[120:123] offset:5120
	v_cvt_pk_fp8_f32 v3, v6, v7 op_sel:[0,0,1]
	v_mov_b32_e32 v120, v153
	v_mov_b32_e32 v122, v153
	v_mov_b32_e32 v121, v153
	ds_write_b128 v117, v[0:3] offset:7680
	v_add_co_u32_e32 v0, vcc, s2, v100
	s_mov_b32 s2, 0x23000
	s_nop 0
	v_addc_co_u32_e32 v1, vcc, 0, v101, vcc
	global_load_dwordx4 v[32:35], v[0:1], off offset:-4096 nt
	global_load_dwordx4 v[36:39], v[0:1], off nt
	v_add_co_u32_e32 v0, vcc, s2, v100
	s_mov_b32 s2, 0x25000
	s_nop 0
	v_addc_co_u32_e32 v1, vcc, 0, v101, vcc
	global_load_dwordx4 v[48:51], v[0:1], off offset:-4096 nt
	global_load_dwordx4 v[52:55], v[0:1], off nt
	v_add_co_u32_e32 v0, vcc, s2, v100
	s_mov_b32 s2, 0x27000
	s_nop 0
	v_addc_co_u32_e32 v1, vcc, 0, v101, vcc
	global_load_dwordx4 v[40:43], v[0:1], off offset:-4096 nt
	global_load_dwordx4 v[44:47], v[0:1], off nt
	v_add_co_u32_e32 v0, vcc, s2, v100
	s_mov_b32 s2, 0x29000
	s_nop 0
	v_addc_co_u32_e32 v1, vcc, 0, v101, vcc
	v_add_co_u32_e32 v4, vcc, s2, v100
	s_mov_b32 s2, 0x2b000
	s_nop 0
	v_addc_co_u32_e32 v5, vcc, 0, v101, vcc
	v_add_co_u32_e32 v8, vcc, s2, v100
	s_mov_b32 s2, 0x2d000
	s_nop 0
	v_addc_co_u32_e32 v9, vcc, 0, v101, vcc
	v_add_co_u32_e32 v12, vcc, s2, v100
	global_load_dwordx4 v[56:59], v[0:1], off offset:-4096 nt
	global_load_dwordx4 v[60:63], v[0:1], off nt
	s_nop 0
	global_load_dwordx4 v[0:3], v[4:5], off offset:-4096 nt
	s_nop 0
	global_load_dwordx4 v[4:7], v[4:5], off nt
	v_addc_co_u32_e32 v13, vcc, 0, v101, vcc
	global_load_dwordx4 v[16:19], v[8:9], off offset:-4096 nt
	global_load_dwordx4 v[20:23], v[8:9], off nt
	s_nop 0
	global_load_dwordx4 v[8:11], v[12:13], off offset:-4096 nt
	s_nop 0
	global_load_dwordx4 v[12:15], v[12:13], off nt
	s_mov_b32 s2, 0x2f000
	v_add_co_u32_e32 v28, vcc, s2, v100
	v_mov_b32_e32 v123, v153
	s_nop 0
	v_addc_co_u32_e32 v29, vcc, 0, v101, vcc
	global_load_dwordx4 v[24:27], v[28:29], off offset:-4096 nt
	s_nop 0
	global_load_dwordx4 v[28:31], v[28:29], off nt
	s_add_u32 s2, s1, s7
	s_addc_u32 s3, s6, 0
	s_waitcnt vmcnt(0)
	v_mul_f32_e32 v32, 0x43800000, v32
	s_waitcnt vmcnt(14)
	v_mul_f32_e32 v36, 0x43800000, v36
	v_cvt_pk_fp8_f32 v120, v32, v36
	s_waitcnt vmcnt(13)
	v_mul_f32_e32 v48, 0x43800000, v48
	s_waitcnt vmcnt(12)
	v_mul_f32_e32 v52, 0x43800000, v52
	v_cvt_pk_fp8_f32 v120, v48, v52 op_sel:[0,0,1]
	s_waitcnt vmcnt(11)
	v_mul_f32_e32 v32, 0x43800000, v40
	s_waitcnt vmcnt(10)
	v_mul_f32_e32 v36, 0x43800000, v44
	v_cvt_pk_fp8_f32 v121, v32, v36
	s_waitcnt vmcnt(9)
	v_mul_f32_e32 v40, 0x43800000, v56
	s_waitcnt vmcnt(7)
	v_mul_f32_e32 v0, 0x43800000, v0
	s_waitcnt vmcnt(6)
	v_mul_f32_e32 v4, 0x43800000, v4
	v_cvt_pk_fp8_f32 v122, v0, v4
	v_mul_f32_e32 v44, 0x43800000, v60
	s_waitcnt vmcnt(3)
	v_mul_f32_e32 v0, 0x43800000, v8
	s_waitcnt vmcnt(2)
	v_mul_f32_e32 v4, 0x43800000, v12
	v_cvt_pk_fp8_f32 v123, v0, v4
	v_mul_f32_e32 v16, 0x43800000, v16
	v_mul_f32_e32 v20, 0x43800000, v20
	v_cvt_pk_fp8_f32 v121, v40, v44 op_sel:[0,0,1]
	v_cvt_pk_fp8_f32 v122, v16, v20 op_sel:[0,0,1]
	s_waitcnt vmcnt(1)
	v_mul_f32_e32 v8, 0x43800000, v24
	s_waitcnt vmcnt(0)
; #define LAS __attribute__((address_space(3)))
; __device__ __forceinline__ unsigned pk4_fp8(float x0, float x1, float x2, float x3) { int w = 0; w = __builtin_amdgcn_cvt_pk_fp8_f32(x0, x1, w, false); w = __builtin_amdgcn_cvt_pk_fp8_f32(x2, x3, w, true); return (unsigned)w; }
; __device__ __forceinline__ void transpose_item_fp8w(const float* W, int K, int N, unsigned char* WT, float q, LAS unsigned char* scr, int item, int lane) {
;     ...
; #pragma unroll
;         for (int i = 0; i < 4; ++i) {
;             u32x4 o;
;             o.x = pk4_fp8(x[0][i] * q, x[1][i] * q, x[2][i] * q, x[3][i] * q); o.y = pk4_fp8(x[4][i] * q, x[5][i] * q, x[6][i] * q, x[7][i] * q);
;             o.z = pk4_fp8(x[8][i] * q, x[9][i] * q, x[10][i] * q, x[11][i] * q); o.w = pk4_fp8(x[12][i] * q, x[13][i] * q, x[14][i] * q, x[15][i] * q);
;             *(LAS u32x4*)(scr + (l5 + 32 * i) * 80 + (2 * b + h) * 16) = o; }
;     }
;     asm volatile("s_waitcnt lgkmcnt(0)" ::: "memory");
; #pragma unroll
;     for (int qd = 0; qd < 8; ++qd) {
;         const int rho = 16 * qd + (lane >> 2), piece = lane & 3;
;         const u32x4 o = *(const LAS u32x4*)(scr + rho * 80 + piece * 16);
;         const int nl = 4 * (rho & 31) + (rho >> 5);
;         *(u32x4*)(WT + (size_t)(n0 + nl) * K + k0 + piece * 16) = o; }
;     asm volatile("s_waitcnt lgkmcnt(0)" ::: "memory");
	v_mul_f32_e32 v12, 0x43800000, v28
	v_cvt_pk_fp8_f32 v123, v8, v12 op_sel:[0,0,1]
	v_mul_f32_e32 v0, 0x43800000, v33
	v_mul_f32_e32 v4, 0x43800000, v37
	v_mul_f32_e32 v8, 0x43800000, v49
	ds_write_b128 v117, v[120:123] offset:32
	v_mov_b32_e32 v120, v153
	v_cvt_pk_fp8_f32 v120, v0, v4
	v_mul_f32_e32 v0, 0x43800000, v41
	v_mul_f32_e32 v4, 0x43800000, v45
	v_mov_b32_e32 v121, v153
	v_cvt_pk_fp8_f32 v121, v0, v4
	v_mul_f32_e32 v0, 0x43800000, v1
	v_mul_f32_e32 v1, 0x43800000, v5
	v_mov_b32_e32 v122, v153
	v_cvt_pk_fp8_f32 v122, v0, v1
	v_mul_f32_e32 v0, 0x43800000, v9
	v_mul_f32_e32 v1, 0x43800000, v13
	v_mov_b32_e32 v123, v153
	v_cvt_pk_fp8_f32 v123, v0, v1
	v_mul_f32_e32 v12, 0x43800000, v53
	v_mul_f32_e32 v4, 0x43800000, v17
	v_mul_f32_e32 v5, 0x43800000, v21
	v_cvt_pk_fp8_f32 v120, v8, v12 op_sel:[0,0,1]
	v_mul_f32_e32 v8, 0x43800000, v57
	v_mul_f32_e32 v12, 0x43800000, v61
	v_cvt_pk_fp8_f32 v122, v4, v5 op_sel:[0,0,1]
	v_mul_f32_e32 v4, 0x43800000, v25
	v_mul_f32_e32 v5, 0x43800000, v29
	v_cvt_pk_fp8_f32 v121, v8, v12 op_sel:[0,0,1]
	v_cvt_pk_fp8_f32 v123, v4, v5 op_sel:[0,0,1]
	v_mul_f32_e32 v0, 0x43800000, v34
	v_mul_f32_e32 v1, 0x43800000, v38
	v_mul_f32_e32 v4, 0x43800000, v50
	ds_write_b128 v117, v[120:123] offset:2592
	v_mov_b32_e32 v120, v153
	v_cvt_pk_fp8_f32 v120, v0, v1
	v_mul_f32_e32 v0, 0x43800000, v42
	v_mul_f32_e32 v1, 0x43800000, v46
	v_mov_b32_e32 v121, v153
	v_cvt_pk_fp8_f32 v121, v0, v1
	v_mul_f32_e32 v0, 0x43800000, v2
	v_mul_f32_e32 v1, 0x43800000, v6
	v_mov_b32_e32 v122, v153
	v_cvt_pk_fp8_f32 v122, v0, v1
	v_mul_f32_e32 v0, 0x43800000, v10
	v_mul_f32_e32 v1, 0x43800000, v14
	v_mov_b32_e32 v123, v153
	v_mul_f32_e32 v5, 0x43800000, v54
	v_cvt_pk_fp8_f32 v123, v0, v1
	v_cvt_pk_fp8_f32 v120, v4, v5 op_sel:[0,0,1]
	v_mul_f32_e32 v4, 0x43800000, v58
	v_mul_f32_e32 v5, 0x43800000, v62
	v_cvt_pk_fp8_f32 v121, v4, v5 op_sel:[0,0,1]
	v_mul_f32_e32 v2, 0x43800000, v18
	v_mul_f32_e32 v4, 0x43800000, v22
	v_cvt_pk_fp8_f32 v122, v2, v4 op_sel:[0,0,1]
	v_mul_f32_e32 v2, 0x43800000, v26
	v_mul_f32_e32 v4, 0x43800000, v30
	v_cvt_pk_fp8_f32 v123, v2, v4 op_sel:[0,0,1]
	v_mul_f32_e32 v1, 0x43800000, v35
	v_mul_f32_e32 v2, 0x43800000, v39
	v_mov_b32_e32 v0, v153
	v_cvt_pk_fp8_f32 v0, v1, v2
	v_mul_f32_e32 v4, 0x43800000, v51
	v_mul_f32_e32 v5, 0x43800000, v55
	v_mul_f32_e32 v2, 0x43800000, v43
	v_cvt_pk_fp8_f32 v0, v4, v5 op_sel:[0,0,1]
	v_mul_f32_e32 v4, 0x43800000, v47
	v_mov_b32_e32 v1, v153
	v_cvt_pk_fp8_f32 v1, v2, v4
	v_mul_f32_e32 v3, 0x43800000, v3
	v_mul_f32_e32 v4, 0x43800000, v7
	v_mov_b32_e32 v2, v153
	v_cvt_pk_fp8_f32 v2, v3, v4
	v_mul_f32_e32 v5, 0x43800000, v59
	v_mul_f32_e32 v6, 0x43800000, v63
	v_cvt_pk_fp8_f32 v1, v5, v6 op_sel:[0,0,1]
	v_mul_f32_e32 v5, 0x43800000, v19
	v_mul_f32_e32 v6, 0x43800000, v23
	v_cvt_pk_fp8_f32 v2, v5, v6 op_sel:[0,0,1]
	v_mul_f32_e32 v4, 0x43800000, v11
	v_mul_f32_e32 v5, 0x43800000, v15
	v_mov_b32_e32 v3, v153
	v_cvt_pk_fp8_f32 v3, v4, v5
	v_mul_f32_e32 v6, 0x43800000, v27
	v_mul_f32_e32 v7, 0x43800000, v31
	ds_write_b128 v117, v[120:123] offset:5152
	v_cvt_pk_fp8_f32 v3, v6, v7 op_sel:[0,0,1]
	v_add_u32_e32 v6, s0, v104
	v_ashrrev_i32_e32 v7, 31, v6
	v_lshl_add_u64 v[4:5], s[2:3], 0, v[66:67]
	ds_write_b128 v117, v[0:3] offset:7712
	s_waitcnt lgkmcnt(0)
	ds_read_b128 v[0:3], v118
	v_lshlrev_b64 v[6:7], 10, v[6:7]
	v_lshl_add_u64 v[6:7], v[4:5], 0, v[6:7]
	s_waitcnt lgkmcnt(0)
	global_store_dwordx4 v[6:7], v[0:3], off nt
	ds_read_b128 v[0:3], v118 offset:1280
	v_add_u32_e32 v6, s0, v105
	v_ashrrev_i32_e32 v7, 31, v6
	v_lshlrev_b64 v[6:7], 10, v[6:7]
	v_lshl_add_u64 v[6:7], v[4:5], 0, v[6:7]
	s_waitcnt lgkmcnt(0)
	global_store_dwordx4 v[6:7], v[0:3], off nt
	ds_read_b128 v[0:3], v118 offset:2560
	v_add_u32_e32 v6, s0, v106
	v_ashrrev_i32_e32 v7, 31, v6
	v_lshlrev_b64 v[6:7], 10, v[6:7]
	v_lshl_add_u64 v[6:7], v[4:5], 0, v[6:7]
	s_waitcnt lgkmcnt(0)
	global_store_dwordx4 v[6:7], v[0:3], off nt
	ds_read_b128 v[0:3], v118 offset:3840
	v_add_u32_e32 v6, s0, v107
	v_ashrrev_i32_e32 v7, 31, v6
	v_lshlrev_b64 v[6:7], 10, v[6:7]
	v_lshl_add_u64 v[6:7], v[4:5], 0, v[6:7]
	s_waitcnt lgkmcnt(0)
	global_store_dwordx4 v[6:7], v[0:3], off nt
	ds_read_b128 v[0:3], v118 offset:5120
	v_add_u32_e32 v6, s0, v108
	v_ashrrev_i32_e32 v7, 31, v6
	v_lshlrev_b64 v[6:7], 10, v[6:7]
	v_lshl_add_u64 v[6:7], v[4:5], 0, v[6:7]
	s_waitcnt lgkmcnt(0)
	global_store_dwordx4 v[6:7], v[0:3], off nt
	ds_read_b128 v[0:3], v118 offset:6400
	v_add_u32_e32 v6, s0, v109
	v_ashrrev_i32_e32 v7, 31, v6
	v_lshlrev_b64 v[6:7], 10, v[6:7]
	v_lshl_add_u64 v[6:7], v[4:5], 0, v[6:7]
	s_waitcnt lgkmcnt(0)
	global_store_dwordx4 v[6:7], v[0:3], off nt
	ds_read_b128 v[0:3], v118 offset:7680
	v_add_u32_e32 v6, s0, v110
	v_ashrrev_i32_e32 v7, 31, v6
	v_lshlrev_b64 v[6:7], 10, v[6:7]
	v_lshl_add_u64 v[6:7], v[4:5], 0, v[6:7]
	s_waitcnt lgkmcnt(0)
	global_store_dwordx4 v[6:7], v[0:3], off nt
	ds_read_b128 v[0:3], v118 offset:8960
	v_add_u32_e32 v6, s0, v111
	v_ashrrev_i32_e32 v7, 31, v6
	v_lshlrev_b64 v[6:7], 10, v[6:7]
	v_lshl_add_u64 v[4:5], v[4:5], 0, v[6:7]
	s_waitcnt lgkmcnt(0)
	global_store_dwordx4 v[4:5], v[0:3], off nt
	s_waitcnt lgkmcnt(0)
	s_mov_b64 s[0:1], 0
; #define LAS __attribute__((address_space(3)))
; __device__ __forceinline__ unsigned pk4_fp8(float x0, float x1, float x2, float x3) { int w = 0; w = __builtin_amdgcn_cvt_pk_fp8_f32(x0, x1, w, false); w = __builtin_amdgcn_cvt_pk_fp8_f32(x2, x3, w, true); return (unsigned)w; }
; __device__ __forceinline__ void transpose_item_fp8w(const float* W, int K, int N, unsigned char* WT, float q, LAS unsigned char* scr, int item, int lane) {
;     const int nblk = N / 128, kb = item / nblk, nb = item % nblk, k0 = 64 * kb, n0 = 128 * nb;
;     const int l5 = lane & 31, h = lane >> 5;
;     const float* src = W + (size_t)(k0 + 16 * h) * N + n0 + 4 * l5;
; #pragma unroll
;     for (int b = 0; b < 2; ++b) {
;         f32x4 x[16];
; #pragma unroll
;         for (int s_ = 0; s_ < 16; ++s_) x[s_] = *(const f32x4*)(src + (size_t)(32 * b + s_) * N);
; #pragma unroll
;         for (int i = 0; i < 4; ++i) {
;             u32x4 o;
;             o.x = pk4_fp8(x[0][i] * q, x[1][i] * q, x[2][i] * q, x[3][i] * q); o.y = pk4_fp8(x[4][i] * q, x[5][i] * q, x[6][i] * q, x[7][i] * q);
;             o.z = pk4_fp8(x[8][i] * q, x[9][i] * q, x[10][i] * q, x[11][i] * q); o.w = pk4_fp8(x[12][i] * q, x[13][i] * q, x[14][i] * q, x[15][i] * q);
;             *(LAS u32x4*)(scr + (l5 + 32 * i) * 80 + (2 * b + h) * 16) = o; }
.LBB0_668:
	s_andn2_b64 vcc, exec, s[0:1]
	s_cbranch_vccnz .LBB0_670
	s_add_i32 s4, s5, 0xfffff910
	v_readlane_b32 s2, v253, 32
	s_lshr_b32 s0, s4, 8
	v_readlane_b32 s3, v253, 33
	s_mov_b32 s9, s3
	s_add_i32 s8, s0, s56
	v_readlane_b32 s40, v253, 58
	s_lshl_b64 s[0:1], s[8:9], 23
	v_readlane_b32 s50, v254, 4
	v_readlane_b32 s51, v254, 5
	s_add_u32 s2, s50, s0
	s_addc_u32 s3, s51, s1
	s_lshl_b64 s[6:7], s[8:9], 21
	v_readlane_b32 s0, v246, 15
	s_add_u32 s1, s0, s6
	v_readlane_b32 s0, v246, 16
	s_addc_u32 s6, s0, s7
	s_lshl_b32 s0, s4, 6
	s_and_b32 s7, s0, 0x3c0
	v_add_u32_e32 v0, s7, v99
	s_lshl_b32 s0, s4, 3
	v_ashrrev_i32_e32 v1, 31, v0
	s_and_b32 s0, s0, 0x780
	v_lshlrev_b64 v[0:1], 13, v[0:1]
	v_lshl_add_u64 v[0:1], s[2:3], 0, v[0:1]
	s_lshl_b32 s8, s0, 2
	s_mov_b32 s3, s9
	v_readlane_b32 s41, v253, 59
	v_readlane_b32 s42, v253, 60
	v_readlane_b32 s43, v253, 61
	v_readlane_b32 s44, v253, 62
	v_readlane_b32 s45, v253, 63
	v_writelane_b32 v253, s2, 32
	v_lshl_add_u64 v[0:1], v[0:1], 0, s[8:9]
	v_lshl_add_u64 v[60:61], v[0:1], 0, v[152:153]
	v_writelane_b32 v253, s3, 33
	s_movk_i32 s2, 0x2000
	v_add_co_u32_e32 v4, vcc, s2, v60
	s_movk_i32 s2, 0x4000
	s_nop 0
	v_addc_co_u32_e32 v5, vcc, 0, v61, vcc
	v_add_co_u32_e32 v8, vcc, s2, v60
	s_movk_i32 s2, 0x6000
	s_nop 0
	v_addc_co_u32_e32 v9, vcc, 0, v61, vcc
	v_add_co_u32_e32 v12, vcc, s2, v60
	s_mov_b32 s2, 0x8000
	s_nop 0
	v_addc_co_u32_e32 v13, vcc, 0, v61, vcc
	v_add_co_u32_e32 v16, vcc, s2, v60
	s_mov_b32 s2, 0xa000
	s_nop 0
	v_addc_co_u32_e32 v17, vcc, 0, v61, vcc
	v_add_co_u32_e32 v20, vcc, s2, v60
	s_mov_b32 s2, 0xc000
	s_nop 0
	v_addc_co_u32_e32 v21, vcc, 0, v61, vcc
	v_add_co_u32_e32 v24, vcc, s2, v60
	s_mov_b32 s2, 0xe000
	s_nop 0
	v_addc_co_u32_e32 v25, vcc, 0, v61, vcc
	v_add_co_u32_e32 v28, vcc, s2, v60
	s_mov_b32 s2, 0x10000
	s_nop 0
	v_addc_co_u32_e32 v29, vcc, 0, v61, vcc
	v_add_co_u32_e32 v32, vcc, s2, v60
	s_mov_b32 s2, 0x12000
	s_nop 0
	v_addc_co_u32_e32 v33, vcc, 0, v61, vcc
	v_add_co_u32_e32 v36, vcc, s2, v60
	s_mov_b32 s2, 0x14000
	s_nop 0
	v_addc_co_u32_e32 v37, vcc, 0, v61, vcc
	v_add_co_u32_e32 v40, vcc, s2, v60
	s_mov_b32 s2, 0x16000
	s_nop 0
	v_addc_co_u32_e32 v41, vcc, 0, v61, vcc
	v_add_co_u32_e32 v44, vcc, s2, v60
	s_mov_b32 s2, 0x18000
	s_nop 0
	v_addc_co_u32_e32 v45, vcc, 0, v61, vcc
	v_add_co_u32_e32 v48, vcc, s2, v60
	global_load_dwordx4 v[0:3], v[60:61], off nt
	s_nop 0
	v_addc_co_u32_e32 v49, vcc, 0, v61, vcc
	global_load_dwordx4 v[4:7], v[4:5], off nt
	s_mov_b32 s2, 0x1a000
	global_load_dwordx4 v[12:15], v[12:13], off nt
	v_add_co_u32_e32 v52, vcc, s2, v60
	global_load_dwordx4 v[16:19], v[16:17], off nt
	s_nop 0
	v_addc_co_u32_e32 v53, vcc, 0, v61, vcc
	global_load_dwordx4 v[20:23], v[20:21], off nt
	s_mov_b32 s2, 0x1c000
	global_load_dwordx4 v[28:31], v[28:29], off nt
	v_add_co_u32_e32 v56, vcc, s2, v60
	global_load_dwordx4 v[32:35], v[32:33], off nt
	s_nop 0
	v_addc_co_u32_e32 v57, vcc, 0, v61, vcc
	global_load_dwordx4 v[36:39], v[36:37], off nt
	s_mov_b32 s2, 0x1e000
	global_load_dwordx4 v[44:47], v[44:45], off nt
	v_add_co_u32_e32 v62, vcc, s2, v60
	global_load_dwordx4 v[48:51], v[48:49], off nt
	s_nop 0
	v_addc_co_u32_e32 v63, vcc, 0, v61, vcc
	global_load_dwordx4 v[52:55], v[52:53], off nt
	v_mov_b32_e32 v124, v153
	global_load_dwordx4 v[8:11], v[8:9], off nt
	v_mov_b32_e32 v125, v153
	global_load_dwordx4 v[24:27], v[24:25], off nt
	v_mov_b32_e32 v126, v153
	global_load_dwordx4 v[40:43], v[40:41], off nt
	v_mov_b32_e32 v127, v153
	global_load_dwordx4 v[56:59], v[56:57], off nt
	s_mov_b32 s2, 0x40000
	global_load_dwordx4 v[120:123], v[62:63], off nt
	v_readlane_b32 s46, v254, 0
	v_readlane_b32 s47, v254, 1
	v_readlane_b32 s48, v254, 2
	v_readlane_b32 s49, v254, 3
	v_readlane_b32 s52, v254, 6
	v_readlane_b32 s53, v254, 7
	v_readlane_b32 s54, v254, 8
	v_readlane_b32 s55, v254, 9
	s_waitcnt vmcnt(0)
	v_mul_f32_e32 v0, 0x43000000, v0
	v_mul_f32_e32 v4, 0x43000000, v4
	v_cvt_pk_fp8_f32 v124, v0, v4
	v_mul_f32_e32 v12, 0x43000000, v12
	v_mul_f32_e32 v0, 0x43000000, v16
	v_mul_f32_e32 v4, 0x43000000, v20
	v_cvt_pk_fp8_f32 v125, v0, v4
	v_mul_f32_e32 v0, 0x43000000, v32
	v_mul_f32_e32 v4, 0x43000000, v36
	v_cvt_pk_fp8_f32 v126, v0, v4
	v_mul_f32_e32 v0, 0x43000000, v48
	v_mul_f32_e32 v4, 0x43000000, v52
	v_cvt_pk_fp8_f32 v127, v0, v4
	v_mul_f32_e32 v8, 0x43000000, v8
	v_cvt_pk_fp8_f32 v124, v8, v12 op_sel:[0,0,1]
	v_mul_f32_e32 v8, 0x43000000, v24
	v_mul_f32_e32 v12, 0x43000000, v28
	v_cvt_pk_fp8_f32 v125, v8, v12 op_sel:[0,0,1]
	v_mul_f32_e32 v8, 0x43000000, v40
	v_mul_f32_e32 v12, 0x43000000, v44
	v_cvt_pk_fp8_f32 v126, v8, v12 op_sel:[0,0,1]
	v_mul_f32_e32 v8, 0x43000000, v56
	v_mul_f32_e32 v12, 0x43000000, v120
	v_cvt_pk_fp8_f32 v127, v8, v12 op_sel:[0,0,1]
	v_mul_f32_e32 v0, 0x43000000, v1
	v_mul_f32_e32 v1, 0x43000000, v5
	v_mul_f32_e32 v4, 0x43000000, v9
	ds_write_b128 v117, v[124:127]
	v_mov_b32_e32 v124, v153
	v_cvt_pk_fp8_f32 v124, v0, v1
	v_mul_f32_e32 v0, 0x43000000, v17
	v_mul_f32_e32 v1, 0x43000000, v21
	v_mov_b32_e32 v125, v153
	v_cvt_pk_fp8_f32 v125, v0, v1
	v_mul_f32_e32 v0, 0x43000000, v33
	v_mul_f32_e32 v1, 0x43000000, v37
	v_mov_b32_e32 v126, v153
	v_cvt_pk_fp8_f32 v126, v0, v1
	v_mul_f32_e32 v0, 0x43000000, v49
	v_mul_f32_e32 v1, 0x43000000, v53
	v_mov_b32_e32 v127, v153
	v_mul_f32_e32 v5, 0x43000000, v13
	v_cvt_pk_fp8_f32 v127, v0, v1
	v_cvt_pk_fp8_f32 v124, v4, v5 op_sel:[0,0,1]
	v_mul_f32_e32 v4, 0x43000000, v25
	v_mul_f32_e32 v5, 0x43000000, v29
	v_cvt_pk_fp8_f32 v125, v4, v5 op_sel:[0,0,1]
	v_mul_f32_e32 v4, 0x43000000, v41
	v_mul_f32_e32 v5, 0x43000000, v45
	v_cvt_pk_fp8_f32 v126, v4, v5 op_sel:[0,0,1]
	v_mul_f32_e32 v4, 0x43000000, v57
; #define LAS __attribute__((address_space(3)))
; __device__ __forceinline__ unsigned pk4_fp8(float x0, float x1, float x2, float x3) { int w = 0; w = __builtin_amdgcn_cvt_pk_fp8_f32(x0, x1, w, false); w = __builtin_amdgcn_cvt_pk_fp8_f32(x2, x3, w, true); return (unsigned)w; }
; __device__ __forceinline__ void transpose_item_fp8w(const float* W, int K, int N, unsigned char* WT, float q, LAS unsigned char* scr, int item, int lane) {
;     ...
;     for (int b = 0; b < 2; ++b) {
;         f32x4 x[16];
; #pragma unroll
;         for (int s_ = 0; s_ < 16; ++s_) x[s_] = *(const f32x4*)(src + (size_t)(32 * b + s_) * N);
; #pragma unroll
;         for (int i = 0; i < 4; ++i) {
;             u32x4 o;
;             o.x = pk4_fp8(x[0][i] * q, x[1][i] * q, x[2][i] * q, x[3][i] * q); o.y = pk4_fp8(x[4][i] * q, x[5][i] * q, x[6][i] * q, x[7][i] * q);
;             o.z = pk4_fp8(x[8][i] * q, x[9][i] * q, x[10][i] * q, x[11][i] * q); o.w = pk4_fp8(x[12][i] * q, x[13][i] * q, x[14][i] * q, x[15][i] * q);
;             *(LAS u32x4*)(scr + (l5 + 32 * i) * 80 + (2 * b + h) * 16) = o; }
	v_mul_f32_e32 v5, 0x43000000, v121
	v_cvt_pk_fp8_f32 v127, v4, v5 op_sel:[0,0,1]
	v_mul_f32_e32 v0, 0x43000000, v2
	v_mul_f32_e32 v1, 0x43000000, v6
	v_mul_f32_e32 v2, 0x43000000, v10
	ds_write_b128 v117, v[124:127] offset:2560
	v_mov_b32_e32 v124, v153
	v_cvt_pk_fp8_f32 v124, v0, v1
	v_mul_f32_e32 v0, 0x43000000, v18
	v_mul_f32_e32 v1, 0x43000000, v22
	v_mov_b32_e32 v125, v153
	v_cvt_pk_fp8_f32 v125, v0, v1
	v_mul_f32_e32 v0, 0x43000000, v34
	v_mul_f32_e32 v1, 0x43000000, v38
	v_mov_b32_e32 v126, v153
	v_cvt_pk_fp8_f32 v126, v0, v1
	v_mul_f32_e32 v0, 0x43000000, v50
	v_mul_f32_e32 v1, 0x43000000, v54
	v_mov_b32_e32 v127, v153
	v_mul_f32_e32 v4, 0x43000000, v14
	v_cvt_pk_fp8_f32 v127, v0, v1
	v_cvt_pk_fp8_f32 v124, v2, v4 op_sel:[0,0,1]
	v_mul_f32_e32 v2, 0x43000000, v26
	v_mul_f32_e32 v4, 0x43000000, v30
	v_cvt_pk_fp8_f32 v125, v2, v4 op_sel:[0,0,1]
	v_mul_f32_e32 v2, 0x43000000, v42
	v_mul_f32_e32 v4, 0x43000000, v46
	v_cvt_pk_fp8_f32 v126, v2, v4 op_sel:[0,0,1]
	v_mul_f32_e32 v2, 0x43000000, v58
	v_mul_f32_e32 v4, 0x43000000, v122
	v_cvt_pk_fp8_f32 v127, v2, v4 op_sel:[0,0,1]
	v_mul_f32_e32 v1, 0x43000000, v3
	v_mul_f32_e32 v2, 0x43000000, v7
	v_mov_b32_e32 v0, v153
	v_cvt_pk_fp8_f32 v0, v1, v2
	v_mul_f32_e32 v3, 0x43000000, v11
	v_mul_f32_e32 v4, 0x43000000, v15
	v_mul_f32_e32 v2, 0x43000000, v19
	v_cvt_pk_fp8_f32 v0, v3, v4 op_sel:[0,0,1]
	v_mul_f32_e32 v3, 0x43000000, v23
	v_mov_b32_e32 v1, v153
	v_cvt_pk_fp8_f32 v1, v2, v3
	v_mul_f32_e32 v4, 0x43000000, v27
	v_mul_f32_e32 v5, 0x43000000, v31
	v_mul_f32_e32 v3, 0x43000000, v35
	v_cvt_pk_fp8_f32 v1, v4, v5 op_sel:[0,0,1]
	v_mul_f32_e32 v4, 0x43000000, v39
	v_mov_b32_e32 v2, v153
	v_cvt_pk_fp8_f32 v2, v3, v4
	v_mul_f32_e32 v5, 0x43000000, v43
	v_mul_f32_e32 v6, 0x43000000, v47
	v_mul_f32_e32 v4, 0x43000000, v51
	v_cvt_pk_fp8_f32 v2, v5, v6 op_sel:[0,0,1]
	v_mul_f32_e32 v5, 0x43000000, v55
	v_mov_b32_e32 v3, v153
	v_cvt_pk_fp8_f32 v3, v4, v5
	v_mul_f32_e32 v6, 0x43000000, v59
	v_mul_f32_e32 v7, 0x43000000, v123
	v_mov_b32_e32 v120, v153
	v_cvt_pk_fp8_f32 v3, v6, v7 op_sel:[0,0,1]
	v_mov_b32_e32 v121, v153
	v_mov_b32_e32 v122, v153
	v_mov_b32_e32 v123, v153
	ds_write_b128 v117, v[0:3] offset:7680
	v_add_co_u32_e32 v0, vcc, s2, v60
	s_mov_b32 s2, 0x42000
	s_nop 0
	v_addc_co_u32_e32 v1, vcc, 0, v61, vcc
	v_add_co_u32_e32 v4, vcc, s2, v60
	s_mov_b32 s2, 0x44000
	s_nop 0
	v_addc_co_u32_e32 v5, vcc, 0, v61, vcc
	v_add_co_u32_e32 v8, vcc, s2, v60
	s_mov_b32 s2, 0x46000
	s_nop 0
	v_addc_co_u32_e32 v9, vcc, 0, v61, vcc
	v_add_co_u32_e32 v12, vcc, s2, v60
	s_mov_b32 s2, 0x48000
	s_nop 0
	v_addc_co_u32_e32 v13, vcc, 0, v61, vcc
	global_load_dwordx4 v[8:11], v[8:9], off nt
	ds_write_b128 v117, v[124:127] offset:5120
	global_load_dwordx4 v[16:19], v[12:13], off nt
	v_add_co_u32_e32 v12, vcc, s2, v60
	s_mov_b32 s2, 0x4a000
	s_nop 0
	v_addc_co_u32_e32 v13, vcc, 0, v61, vcc
	v_add_co_u32_e32 v20, vcc, s2, v60
	s_mov_b32 s2, 0x4c000
	s_nop 0
	v_addc_co_u32_e32 v21, vcc, 0, v61, vcc
	global_load_dwordx4 v[12:15], v[12:13], off nt
	s_waitcnt vmcnt(0)
	v_mul_f32_e32 v8, 0x43000000, v8
	global_load_dwordx4 v[24:27], v[20:21], off nt
	v_add_co_u32_e32 v20, vcc, s2, v60
	s_mov_b32 s2, 0x4e000
	s_nop 0
	v_addc_co_u32_e32 v21, vcc, 0, v61, vcc
	global_load_dwordx4 v[28:31], v[20:21], off nt
	v_add_co_u32_e32 v20, vcc, s2, v60
	s_mov_b32 s2, 0x50000
	s_nop 0
	v_addc_co_u32_e32 v21, vcc, 0, v61, vcc
	global_load_dwordx4 v[40:43], v[20:21], off nt
	v_add_co_u32_e32 v20, vcc, s2, v60
	s_mov_b32 s2, 0x52000
	s_nop 0
	v_addc_co_u32_e32 v21, vcc, 0, v61, vcc
	v_add_co_u32_e32 v32, vcc, s2, v60
	s_mov_b32 s2, 0x54000
	s_nop 0
	v_addc_co_u32_e32 v33, vcc, 0, v61, vcc
	v_add_co_u32_e32 v36, vcc, s2, v60
	s_mov_b32 s2, 0x56000
	s_nop 0
	v_addc_co_u32_e32 v37, vcc, 0, v61, vcc
	v_add_co_u32_e32 v44, vcc, s2, v60
	s_mov_b32 s2, 0x58000
	s_nop 0
	v_addc_co_u32_e32 v45, vcc, 0, v61, vcc
	global_load_dwordx4 v[36:39], v[36:37], off nt
	s_waitcnt vmcnt(5)
	v_mul_f32_e32 v16, 0x43000000, v16
	global_load_dwordx4 v[48:51], v[44:45], off nt
	v_add_co_u32_e32 v44, vcc, s2, v60
	global_load_dwordx4 v[0:3], v[0:1], off nt
	s_nop 0
	v_addc_co_u32_e32 v45, vcc, 0, v61, vcc
	global_load_dwordx4 v[4:7], v[4:5], off nt
	s_mov_b32 s2, 0x5a000
	v_add_co_u32_e32 v52, vcc, s2, v60
	global_load_dwordx4 v[20:23], v[20:21], off nt
	s_nop 0
	v_addc_co_u32_e32 v53, vcc, 0, v61, vcc
	global_load_dwordx4 v[32:35], v[32:33], off nt
	s_mov_b32 s2, 0x5c000
	global_load_dwordx4 v[44:47], v[44:45], off nt
	v_add_co_u32_e32 v56, vcc, s2, v60
	global_load_dwordx4 v[52:55], v[52:53], off nt
	s_nop 0
	v_addc_co_u32_e32 v57, vcc, 0, v61, vcc
	s_mov_b32 s2, 0x5e000
	v_add_co_u32_e32 v60, vcc, s2, v60
	global_load_dwordx4 v[56:59], v[56:57], off nt
	s_nop 0
	v_addc_co_u32_e32 v61, vcc, 0, v61, vcc
	global_load_dwordx4 v[60:63], v[60:61], off nt
	s_add_u32 s2, s1, s7
	s_addc_u32 s3, s6, 0
	s_waitcnt vmcnt(0)
	v_mul_f32_e32 v0, 0x43000000, v0
	s_waitcnt vmcnt(6)
	v_mul_f32_e32 v4, 0x43000000, v4
	v_cvt_pk_fp8_f32 v120, v0, v4
	v_mul_f32_e32 v0, 0x43000000, v12
	v_mul_f32_e32 v4, 0x43000000, v24
	v_cvt_pk_fp8_f32 v121, v0, v4
	s_waitcnt vmcnt(5)
	v_mul_f32_e32 v0, 0x43000000, v20
	v_cvt_pk_fp8_f32 v120, v8, v16 op_sel:[0,0,1]
	s_waitcnt vmcnt(4)
	v_mul_f32_e32 v4, 0x43000000, v32
	v_cvt_pk_fp8_f32 v122, v0, v4
	s_waitcnt vmcnt(3)
	v_mul_f32_e32 v0, 0x43000000, v44
	v_mul_f32_e32 v8, 0x43000000, v28
	v_mul_f32_e32 v12, 0x43000000, v40
	s_waitcnt vmcnt(2)
; #define LAS __attribute__((address_space(3)))
; __device__ __forceinline__ unsigned pk4_fp8(float x0, float x1, float x2, float x3) { int w = 0; w = __builtin_amdgcn_cvt_pk_fp8_f32(x0, x1, w, false); w = __builtin_amdgcn_cvt_pk_fp8_f32(x2, x3, w, true); return (unsigned)w; }
; __device__ __forceinline__ void transpose_item_fp8w(const float* W, int K, int N, unsigned char* WT, float q, LAS unsigned char* scr, int item, int lane) {
;     ...
; #pragma unroll
;         for (int i = 0; i < 4; ++i) {
;             u32x4 o;
;             o.x = pk4_fp8(x[0][i] * q, x[1][i] * q, x[2][i] * q, x[3][i] * q); o.y = pk4_fp8(x[4][i] * q, x[5][i] * q, x[6][i] * q, x[7][i] * q);
;             o.z = pk4_fp8(x[8][i] * q, x[9][i] * q, x[10][i] * q, x[11][i] * q); o.w = pk4_fp8(x[12][i] * q, x[13][i] * q, x[14][i] * q, x[15][i] * q);
;             *(LAS u32x4*)(scr + (l5 + 32 * i) * 80 + (2 * b + h) * 16) = o; }
;     }
;     asm volatile("s_waitcnt lgkmcnt(0)" ::: "memory");
; #pragma unroll
;     for (int qd = 0; qd < 8; ++qd) {
;         const int rho = 16 * qd + (lane >> 2), piece = lane & 3;
;         const u32x4 o = *(const LAS u32x4*)(scr + rho * 80 + piece * 16);
;         const int nl = 4 * (rho & 31) + (rho >> 5);
;         *(u32x4*)(WT + (size_t)(n0 + nl) * K + k0 + piece * 16) = o; }
	v_mul_f32_e32 v4, 0x43000000, v52
	v_cvt_pk_fp8_f32 v123, v0, v4
	v_cvt_pk_fp8_f32 v121, v8, v12 op_sel:[0,0,1]
	v_mul_f32_e32 v8, 0x43000000, v36
	v_mul_f32_e32 v12, 0x43000000, v48
	v_cvt_pk_fp8_f32 v122, v8, v12 op_sel:[0,0,1]
	s_waitcnt vmcnt(1)
	v_mul_f32_e32 v8, 0x43000000, v56
	v_mul_f32_e32 v0, 0x43000000, v1
	v_mul_f32_e32 v1, 0x43000000, v5
	s_waitcnt vmcnt(0)
	v_mul_f32_e32 v12, 0x43000000, v60
	v_cvt_pk_fp8_f32 v123, v8, v12 op_sel:[0,0,1]
	v_mul_f32_e32 v4, 0x43000000, v9
	v_mul_f32_e32 v5, 0x43000000, v17
	ds_write_b128 v117, v[120:123] offset:32
	v_mov_b32_e32 v120, v153
	v_cvt_pk_fp8_f32 v120, v0, v1
	v_mul_f32_e32 v0, 0x43000000, v13
	v_mul_f32_e32 v1, 0x43000000, v25
	v_mov_b32_e32 v121, v153
	v_cvt_pk_fp8_f32 v121, v0, v1
	v_mul_f32_e32 v0, 0x43000000, v21
	v_mul_f32_e32 v1, 0x43000000, v33
	v_mov_b32_e32 v122, v153
	v_cvt_pk_fp8_f32 v122, v0, v1
	v_mul_f32_e32 v0, 0x43000000, v45
	v_mul_f32_e32 v1, 0x43000000, v53
	v_mov_b32_e32 v123, v153
	v_cvt_pk_fp8_f32 v123, v0, v1
	v_cvt_pk_fp8_f32 v120, v4, v5 op_sel:[0,0,1]
	v_mul_f32_e32 v4, 0x43000000, v29
	v_mul_f32_e32 v5, 0x43000000, v41
	v_cvt_pk_fp8_f32 v121, v4, v5 op_sel:[0,0,1]
	v_mul_f32_e32 v4, 0x43000000, v37
	v_mul_f32_e32 v5, 0x43000000, v49
	v_cvt_pk_fp8_f32 v122, v4, v5 op_sel:[0,0,1]
	v_mul_f32_e32 v4, 0x43000000, v57
	v_mul_f32_e32 v5, 0x43000000, v61
	v_cvt_pk_fp8_f32 v123, v4, v5 op_sel:[0,0,1]
	v_mul_f32_e32 v0, 0x43000000, v2
	v_mul_f32_e32 v1, 0x43000000, v6
	v_mul_f32_e32 v2, 0x43000000, v10
	ds_write_b128 v117, v[120:123] offset:2592
	v_mov_b32_e32 v120, v153
	v_cvt_pk_fp8_f32 v120, v0, v1
	v_mul_f32_e32 v0, 0x43000000, v14
	v_mul_f32_e32 v1, 0x43000000, v26
	v_mov_b32_e32 v121, v153
	v_cvt_pk_fp8_f32 v121, v0, v1
	v_mul_f32_e32 v0, 0x43000000, v22
	v_mul_f32_e32 v1, 0x43000000, v34
	v_mov_b32_e32 v122, v153
	v_cvt_pk_fp8_f32 v122, v0, v1
	v_mul_f32_e32 v0, 0x43000000, v46
	v_mul_f32_e32 v1, 0x43000000, v54
	v_mov_b32_e32 v123, v153
	v_mul_f32_e32 v4, 0x43000000, v18
	v_cvt_pk_fp8_f32 v123, v0, v1
	v_cvt_pk_fp8_f32 v120, v2, v4 op_sel:[0,0,1]
	v_mul_f32_e32 v2, 0x43000000, v30
	v_mul_f32_e32 v4, 0x43000000, v42
	v_cvt_pk_fp8_f32 v121, v2, v4 op_sel:[0,0,1]
	v_mul_f32_e32 v2, 0x43000000, v38
	v_mul_f32_e32 v4, 0x43000000, v50
	v_cvt_pk_fp8_f32 v122, v2, v4 op_sel:[0,0,1]
	v_mul_f32_e32 v2, 0x43000000, v58
	v_mul_f32_e32 v4, 0x43000000, v62
	v_cvt_pk_fp8_f32 v123, v2, v4 op_sel:[0,0,1]
	v_mul_f32_e32 v1, 0x43000000, v3
	v_mul_f32_e32 v2, 0x43000000, v7
	v_mov_b32_e32 v0, v153
	v_cvt_pk_fp8_f32 v0, v1, v2
	v_mul_f32_e32 v3, 0x43000000, v11
	v_mul_f32_e32 v4, 0x43000000, v19
	v_mul_f32_e32 v2, 0x43000000, v15
	v_cvt_pk_fp8_f32 v0, v3, v4 op_sel:[0,0,1]
	v_mul_f32_e32 v3, 0x43000000, v27
	v_mov_b32_e32 v1, v153
	v_cvt_pk_fp8_f32 v1, v2, v3
	v_mul_f32_e32 v4, 0x43000000, v31
	v_mul_f32_e32 v5, 0x43000000, v43
	v_mul_f32_e32 v3, 0x43000000, v23
	v_cvt_pk_fp8_f32 v1, v4, v5 op_sel:[0,0,1]
	v_mul_f32_e32 v4, 0x43000000, v35
	v_mov_b32_e32 v2, v153
	v_cvt_pk_fp8_f32 v2, v3, v4
	v_mul_f32_e32 v5, 0x43000000, v39
	v_mul_f32_e32 v6, 0x43000000, v51
	v_mul_f32_e32 v4, 0x43000000, v47
	v_cvt_pk_fp8_f32 v2, v5, v6 op_sel:[0,0,1]
	v_mul_f32_e32 v5, 0x43000000, v55
	v_mov_b32_e32 v3, v153
	v_cvt_pk_fp8_f32 v3, v4, v5
	v_mul_f32_e32 v6, 0x43000000, v59
	v_mul_f32_e32 v7, 0x43000000, v63
	ds_write_b128 v117, v[120:123] offset:5152
	v_cvt_pk_fp8_f32 v3, v6, v7 op_sel:[0,0,1]
	v_add_u32_e32 v6, s0, v104
	v_ashrrev_i32_e32 v7, 31, v6
	v_lshl_add_u64 v[4:5], s[2:3], 0, v[66:67]
	ds_write_b128 v117, v[0:3] offset:7712
	s_waitcnt lgkmcnt(0)
	ds_read_b128 v[0:3], v118
	v_lshlrev_b64 v[6:7], 10, v[6:7]
	v_lshl_add_u64 v[6:7], v[4:5], 0, v[6:7]
	s_waitcnt lgkmcnt(0)
	global_store_dwordx4 v[6:7], v[0:3], off nt
	ds_read_b128 v[0:3], v118 offset:1280
	v_add_u32_e32 v6, s0, v105
	v_ashrrev_i32_e32 v7, 31, v6
	v_lshlrev_b64 v[6:7], 10, v[6:7]
	v_lshl_add_u64 v[6:7], v[4:5], 0, v[6:7]
	s_waitcnt lgkmcnt(0)
	global_store_dwordx4 v[6:7], v[0:3], off nt
	ds_read_b128 v[0:3], v118 offset:2560
	v_add_u32_e32 v6, s0, v106
	v_ashrrev_i32_e32 v7, 31, v6
	v_lshlrev_b64 v[6:7], 10, v[6:7]
	v_lshl_add_u64 v[6:7], v[4:5], 0, v[6:7]
	s_waitcnt lgkmcnt(0)
	global_store_dwordx4 v[6:7], v[0:3], off nt
	ds_read_b128 v[0:3], v118 offset:3840
	v_add_u32_e32 v6, s0, v107
	v_ashrrev_i32_e32 v7, 31, v6
	v_lshlrev_b64 v[6:7], 10, v[6:7]
	v_lshl_add_u64 v[6:7], v[4:5], 0, v[6:7]
	s_waitcnt lgkmcnt(0)
	global_store_dwordx4 v[6:7], v[0:3], off nt
	ds_read_b128 v[0:3], v118 offset:5120
	v_add_u32_e32 v6, s0, v108
	v_ashrrev_i32_e32 v7, 31, v6
	v_lshlrev_b64 v[6:7], 10, v[6:7]
	v_lshl_add_u64 v[6:7], v[4:5], 0, v[6:7]
	s_waitcnt lgkmcnt(0)
	global_store_dwordx4 v[6:7], v[0:3], off nt
	ds_read_b128 v[0:3], v118 offset:6400
	v_add_u32_e32 v6, s0, v109
	v_ashrrev_i32_e32 v7, 31, v6
	v_lshlrev_b64 v[6:7], 10, v[6:7]
	v_lshl_add_u64 v[6:7], v[4:5], 0, v[6:7]
	s_waitcnt lgkmcnt(0)
	global_store_dwordx4 v[6:7], v[0:3], off nt
	ds_read_b128 v[0:3], v118 offset:7680
	v_add_u32_e32 v6, s0, v110
	v_ashrrev_i32_e32 v7, 31, v6
	v_lshlrev_b64 v[6:7], 10, v[6:7]
	v_lshl_add_u64 v[6:7], v[4:5], 0, v[6:7]
	s_waitcnt lgkmcnt(0)
	global_store_dwordx4 v[6:7], v[0:3], off nt
	ds_read_b128 v[0:3], v118 offset:8960
	v_add_u32_e32 v6, s0, v111
	v_ashrrev_i32_e32 v7, 31, v6
	v_lshlrev_b64 v[6:7], 10, v[6:7]
	v_lshl_add_u64 v[4:5], v[4:5], 0, v[6:7]
	s_waitcnt lgkmcnt(0)
	global_store_dwordx4 v[4:5], v[0:3], off nt
	s_waitcnt lgkmcnt(0)

; #define LAS __attribute__((address_space(3)))
; template <int QPERM>
; __device__ __forceinline__ void transpose_item(const float* W, int K, int N, bf16_t* WT, LAS float* scr, int item, int lane) {
;     const int nblk = N / 32, kb = item / nblk, nb = item % nblk, k0 = 64 * kb, n0 = 32 * nb;
; #pragma unroll 8
;     for (int i = 0; i < 32; ++i) { const int kk = 2 * i + (lane >> 5); scr[kk * 33 + (lane & 31)] = W[(size_t)(k0 + kk) * N + n0 + (lane & 31)]; }
.LBB0_673:
	s_lshl_b32 s9, s7, 1
	s_lshl_b32 s10, s6, 1
	v_add_u32_e32 v20, s9, v2
	v_add_u32_e32 v18, s10, v3
	v_ashrrev_i32_e32 v21, 31, v20
	v_ashrrev_i32_e32 v19, 31, v18
	v_lshlrev_b64 v[20:21], 12, v[20:21]
	v_lshlrev_b64 v[18:19], 12, v[18:19]
	v_lshl_add_u64 v[20:21], v[0:1], 0, v[20:21]
	v_lshl_add_u64 v[18:19], v[0:1], 0, v[18:19]
	global_load_dword v24, v[20:21], off nt
	global_load_dword v25, v[18:19], off nt
	v_add_u32_e32 v22, s10, v65
	v_add_u32_e32 v23, s9, v128
	v_mad_u64_u32 v[18:19], s[2:3], v23, s83, v[70:71]
	v_mad_u64_u32 v[20:21], s[2:3], v22, s83, v[70:71]
	v_add_u32_e32 v22, s10, v71
	v_add_u32_e32 v23, s9, v86
	s_add_i32 s7, s7, 16
	s_add_i32 s6, s6, 16
	s_add_i32 s8, s8, -16
	s_cmp_lg_u32 s8, 0
	s_waitcnt vmcnt(0)
	ds_write_b32 v18, v24
	ds_write_b32 v20, v25
	v_add_u32_e32 v20, s9, v4
	v_add_u32_e32 v18, s10, v5
	v_ashrrev_i32_e32 v21, 31, v20
	v_ashrrev_i32_e32 v19, 31, v18
	v_lshlrev_b64 v[20:21], 12, v[20:21]
	v_lshlrev_b64 v[18:19], 12, v[18:19]
	v_lshl_add_u64 v[20:21], v[0:1], 0, v[20:21]
	v_lshl_add_u64 v[18:19], v[0:1], 0, v[18:19]
	global_load_dword v24, v[20:21], off nt
	global_load_dword v25, v[18:19], off nt
	v_mad_u64_u32 v[18:19], s[2:3], v23, s83, v[70:71]
	v_mad_u64_u32 v[20:21], s[2:3], v22, s83, v[70:71]
	v_add_u32_e32 v22, s10, v87
	v_add_u32_e32 v23, s9, v88
	s_waitcnt vmcnt(0)
	ds_write_b32 v18, v24
	s_waitcnt vmcnt(0)
	ds_write_b32 v20, v25
	v_add_u32_e32 v20, s9, v6
	v_add_u32_e32 v18, s10, v7
	v_ashrrev_i32_e32 v21, 31, v20
	v_ashrrev_i32_e32 v19, 31, v18
	v_lshlrev_b64 v[20:21], 12, v[20:21]
	v_lshlrev_b64 v[18:19], 12, v[18:19]
	v_lshl_add_u64 v[20:21], v[0:1], 0, v[20:21]
	v_lshl_add_u64 v[18:19], v[0:1], 0, v[18:19]
	global_load_dword v24, v[20:21], off nt
	global_load_dword v25, v[18:19], off nt
	v_mad_u64_u32 v[18:19], s[2:3], v23, s83, v[70:71]
	v_mad_u64_u32 v[20:21], s[2:3], v22, s83, v[70:71]
	v_add_u32_e32 v22, s10, v89
	v_add_u32_e32 v23, s9, v90
	s_waitcnt vmcnt(0)
	ds_write_b32 v18, v24
	s_waitcnt vmcnt(0)
	ds_write_b32 v20, v25
	v_add_u32_e32 v20, s9, v8
	v_add_u32_e32 v18, s10, v9
	v_ashrrev_i32_e32 v21, 31, v20
	v_ashrrev_i32_e32 v19, 31, v18
	v_lshlrev_b64 v[20:21], 12, v[20:21]
	v_lshlrev_b64 v[18:19], 12, v[18:19]
	v_lshl_add_u64 v[20:21], v[0:1], 0, v[20:21]
	v_lshl_add_u64 v[18:19], v[0:1], 0, v[18:19]
	global_load_dword v24, v[20:21], off nt
	global_load_dword v25, v[18:19], off nt
	v_mad_u64_u32 v[18:19], s[2:3], v23, s83, v[70:71]
	v_mad_u64_u32 v[20:21], s[2:3], v22, s83, v[70:71]
	v_add_u32_e32 v22, s10, v91
	v_add_u32_e32 v23, s9, v92
	s_waitcnt vmcnt(0)
	ds_write_b32 v18, v24
	s_waitcnt vmcnt(0)
	ds_write_b32 v20, v25
	v_add_u32_e32 v20, s9, v10
	v_add_u32_e32 v18, s10, v11
	v_ashrrev_i32_e32 v21, 31, v20
	v_ashrrev_i32_e32 v19, 31, v18
	v_lshlrev_b64 v[20:21], 12, v[20:21]
	v_lshlrev_b64 v[18:19], 12, v[18:19]
	v_lshl_add_u64 v[20:21], v[0:1], 0, v[20:21]
	v_lshl_add_u64 v[18:19], v[0:1], 0, v[18:19]
	global_load_dword v24, v[20:21], off nt
	global_load_dword v25, v[18:19], off nt
	v_mad_u64_u32 v[18:19], s[2:3], v23, s83, v[70:71]
	v_mad_u64_u32 v[20:21], s[2:3], v22, s83, v[70:71]
	v_add_u32_e32 v22, s10, v93
	v_add_u32_e32 v23, s9, v94
	s_waitcnt vmcnt(0)
	ds_write_b32 v18, v24
	s_waitcnt vmcnt(0)
	ds_write_b32 v20, v25
	v_add_u32_e32 v20, s9, v12
	v_add_u32_e32 v18, s10, v13
	v_ashrrev_i32_e32 v21, 31, v20
	v_ashrrev_i32_e32 v19, 31, v18
	v_lshlrev_b64 v[20:21], 12, v[20:21]
	v_lshlrev_b64 v[18:19], 12, v[18:19]
	v_lshl_add_u64 v[20:21], v[0:1], 0, v[20:21]
	v_lshl_add_u64 v[18:19], v[0:1], 0, v[18:19]
	global_load_dword v24, v[20:21], off nt
	global_load_dword v25, v[18:19], off nt
	v_mad_u64_u32 v[18:19], s[2:3], v23, s83, v[70:71]
	v_mad_u64_u32 v[20:21], s[2:3], v22, s83, v[70:71]
	v_add_u32_e32 v22, s10, v95
	v_add_u32_e32 v23, s9, v96
	s_waitcnt vmcnt(0)
	ds_write_b32 v18, v24
	s_waitcnt vmcnt(0)
	ds_write_b32 v20, v25
	v_add_u32_e32 v20, s9, v14
	v_add_u32_e32 v18, s10, v15
	v_ashrrev_i32_e32 v21, 31, v20
	v_ashrrev_i32_e32 v19, 31, v18
	v_lshlrev_b64 v[20:21], 12, v[20:21]
	v_lshlrev_b64 v[18:19], 12, v[18:19]
	v_lshl_add_u64 v[20:21], v[0:1], 0, v[20:21]
	v_lshl_add_u64 v[18:19], v[0:1], 0, v[18:19]
	global_load_dword v24, v[20:21], off nt
	global_load_dword v25, v[18:19], off nt
	v_mad_u64_u32 v[18:19], s[2:3], v23, s83, v[70:71]
	v_mad_u64_u32 v[20:21], s[2:3], v22, s83, v[70:71]
	v_add_u32_e32 v23, s9, v98
	v_add_u32_e32 v22, s10, v97
	s_waitcnt vmcnt(0)
	ds_write_b32 v18, v24
	s_waitcnt vmcnt(0)
	ds_write_b32 v20, v25
	v_add_u32_e32 v20, s9, v16
	v_add_u32_e32 v18, s10, v17
	v_ashrrev_i32_e32 v21, 31, v20
	v_ashrrev_i32_e32 v19, 31, v18
	v_lshlrev_b64 v[20:21], 12, v[20:21]
	v_lshlrev_b64 v[18:19], 12, v[18:19]
	v_lshl_add_u64 v[20:21], v[0:1], 0, v[20:21]
	v_lshl_add_u64 v[18:19], v[0:1], 0, v[18:19]
	global_load_dword v24, v[20:21], off nt
	global_load_dword v25, v[18:19], off nt
	v_mad_u64_u32 v[18:19], s[2:3], v23, s83, v[70:71]
	v_mad_u64_u32 v[20:21], s[2:3], v22, s83, v[70:71]
	s_waitcnt vmcnt(0)
	ds_write_b32 v18, v24
	s_waitcnt vmcnt(0)
	ds_write_b32 v20, v25
	s_cbranch_scc1 .LBB0_673
; #define LAS __attribute__((address_space(3)))
; __device__ __forceinline__ unsigned pk2(float lo, float hi) { unsigned r; asm("v_cvt_pk_bf16_f32 %0, %1, %2" : "=v"(r) : "v"(lo), "v"(hi)); return r; }
; template <int QPERM>
; __device__ __forceinline__ void transpose_item(const float* W, int K, int N, bf16_t* WT, LAS float* scr, int item, int lane) {
;     ...
;     asm volatile("s_waitcnt lgkmcnt(0)" ::: "memory");
;     const int c = lane & 7;
; #pragma unroll
;     for (int j = 0; j < 4; ++j) { const int n = (lane >> 3) + 8 * j; const LAS float* s = scr + (8 * c) * 33 + n;
;         u32x4 o; o.x = pk2(s[0 * 33], s[1 * 33]); o.y = pk2(s[2 * 33], s[3 * 33]); o.z = pk2(s[4 * 33], s[5 * 33]); o.w = pk2(s[6 * 33], s[7 * 33]);
;         int dn = n0 + n;
;         if (QPERM == 1) { const int h = dn / 192, d = dn % 192; if (d >= 128) { const int jj = d - 128, a = jj >> 5, p = (jj >> 4) & 1, f = jj & 15; dn = h * 192 + 128 + 2 * (a * 16 + f) + p; } }
;         if (QPERM == 2) { const int h = dn >> 8, j = dn & 255; dn = (j < 128) ? h * 128 + j : 512 + h * 128 + (j - 128); }
;         *(u32x4*)(WT + (size_t)dn * K + k0 + 8 * c) = o; }
;     asm volatile("s_waitcnt lgkmcnt(0)" ::: "memory");
	s_waitcnt lgkmcnt(0)
	ds_read2_b32 v[6:7], v113 offset0:33 offset1:41
	ds_read2_b32 v[8:9], v113 offset1:8
	s_lshl_b32 s10, s1, 1
	s_mov_b32 s1, s11
	ds_read2_b32 v[10:11], v113 offset0:66 offset1:74
	ds_read2_b32 v[12:13], v113 offset0:99 offset1:107
	ds_read2_b32 v[14:15], v113 offset0:132 offset1:140
	ds_read2_b32 v[16:17], v113 offset0:165 offset1:173
	ds_read2_b32 v[18:19], v113 offset0:198 offset1:206
	ds_read2_b32 v[20:21], v113 offset0:231 offset1:239
	v_writelane_b32 v253, s0, 32
	v_lshl_add_u64 v[4:5], v[72:73], 0, s[10:11]
	s_waitcnt lgkmcnt(6)
	v_cvt_pk_bf16_f32 v0, v8, v6
	s_waitcnt lgkmcnt(4)
	v_cvt_pk_bf16_f32 v1, v10, v12
	s_waitcnt lgkmcnt(2)
	v_cvt_pk_bf16_f32 v2, v14, v16
	s_waitcnt lgkmcnt(0)
	v_cvt_pk_bf16_f32 v3, v18, v20
	v_add_u32_e32 v22, s0, v112
	v_ashrrev_i32_e32 v23, 31, v22
	v_lshlrev_b64 v[22:23], 11, v[22:23]
	v_lshl_add_u64 v[22:23], v[4:5], 0, v[22:23]
	v_add_u32_e32 v6, s0, v114
	global_store_dwordx4 v[22:23], v[0:3], off nt
	v_add_u32_e32 v22, s0, v115
	v_ashrrev_i32_e32 v23, 31, v22
	v_cvt_pk_bf16_f32 v0, v9, v7
	v_ashrrev_i32_e32 v7, 31, v6
	v_lshlrev_b64 v[6:7], 11, v[6:7]
	v_lshl_add_u64 v[6:7], v[4:5], 0, v[6:7]
	v_cvt_pk_bf16_f32 v1, v11, v13
	v_cvt_pk_bf16_f32 v2, v15, v17
	v_cvt_pk_bf16_f32 v3, v19, v21
	global_store_dwordx4 v[6:7], v[0:3], off nt
	ds_read2_b32 v[6:7], v113 offset0:16 offset1:24
	ds_read2_b32 v[8:9], v113 offset0:49 offset1:57
	ds_read2_b32 v[10:11], v113 offset0:82 offset1:90
	ds_read2_b32 v[12:13], v113 offset0:115 offset1:123
	ds_read2_b32 v[14:15], v113 offset0:148 offset1:156
	ds_read2_b32 v[16:17], v113 offset0:181 offset1:189
	ds_read2_b32 v[18:19], v113 offset0:214 offset1:222
	ds_read2_b32 v[20:21], v113 offset0:247 offset1:255
	v_lshlrev_b64 v[22:23], 11, v[22:23]
	s_waitcnt lgkmcnt(6)
	v_cvt_pk_bf16_f32 v0, v6, v8
	v_lshl_add_u64 v[22:23], v[4:5], 0, v[22:23]
	v_add_u32_e32 v6, s0, v116
	s_waitcnt lgkmcnt(4)
	v_cvt_pk_bf16_f32 v1, v10, v12
	s_waitcnt lgkmcnt(2)
	v_cvt_pk_bf16_f32 v2, v14, v16
	s_waitcnt lgkmcnt(0)
	v_cvt_pk_bf16_f32 v3, v18, v20
	global_store_dwordx4 v[22:23], v[0:3], off nt
	v_writelane_b32 v253, s1, 33
	s_nop 0
	v_cvt_pk_bf16_f32 v0, v7, v9
	v_ashrrev_i32_e32 v7, 31, v6
	v_lshlrev_b64 v[6:7], 11, v[6:7]
	v_lshl_add_u64 v[4:5], v[4:5], 0, v[6:7]
	v_cvt_pk_bf16_f32 v1, v11, v13
	v_cvt_pk_bf16_f32 v2, v15, v17
	v_cvt_pk_bf16_f32 v3, v19, v21
	global_store_dwordx4 v[4:5], v[0:3], off nt
	s_waitcnt lgkmcnt(0)

; #define LAS __attribute__((address_space(3)))
; template <int QPERM>
; __device__ __forceinline__ void transpose_item(const float* W, int K, int N, bf16_t* WT, LAS float* scr, int item, int lane) {
;     const int nblk = N / 32, kb = item / nblk, nb = item % nblk, k0 = 64 * kb, n0 = 32 * nb;
; #pragma unroll 8
;     for (int i = 0; i < 32; ++i) { const int kk = 2 * i + (lane >> 5); scr[kk * 33 + (lane & 31)] = W[(size_t)(k0 + kk) * N + n0 + (lane & 31)]; }
.LBB0_678:
	s_lshl_b32 s9, s7, 1
	s_lshl_b32 s10, s6, 1
	v_add_u32_e32 v20, s9, v2
	v_add_u32_e32 v18, s10, v3
	v_ashrrev_i32_e32 v21, 31, v20
	v_ashrrev_i32_e32 v19, 31, v18
	v_lshlrev_b64 v[20:21], 12, v[20:21]
	v_lshlrev_b64 v[18:19], 12, v[18:19]
	v_lshl_add_u64 v[20:21], v[0:1], 0, v[20:21]
	v_lshl_add_u64 v[18:19], v[0:1], 0, v[18:19]
	global_load_dword v24, v[20:21], off nt
	global_load_dword v25, v[18:19], off nt
	v_add_u32_e32 v22, s10, v65
	v_add_u32_e32 v23, s9, v128
	v_mad_u64_u32 v[18:19], s[2:3], v23, s83, v[70:71]
	v_mad_u64_u32 v[20:21], s[2:3], v22, s83, v[70:71]
	v_add_u32_e32 v22, s10, v71
	v_add_u32_e32 v23, s9, v86
	s_add_i32 s7, s7, 16
	s_add_i32 s6, s6, 16
	s_add_i32 s8, s8, -16
	s_cmp_lg_u32 s8, 0
	s_waitcnt vmcnt(0)
	ds_write_b32 v18, v24
	ds_write_b32 v20, v25
	v_add_u32_e32 v20, s9, v4
	v_add_u32_e32 v18, s10, v5
	v_ashrrev_i32_e32 v21, 31, v20
	v_ashrrev_i32_e32 v19, 31, v18
	v_lshlrev_b64 v[20:21], 12, v[20:21]
	v_lshlrev_b64 v[18:19], 12, v[18:19]
	v_lshl_add_u64 v[20:21], v[0:1], 0, v[20:21]
	v_lshl_add_u64 v[18:19], v[0:1], 0, v[18:19]
	global_load_dword v24, v[20:21], off nt
	global_load_dword v25, v[18:19], off nt
	v_mad_u64_u32 v[18:19], s[2:3], v23, s83, v[70:71]
	v_mad_u64_u32 v[20:21], s[2:3], v22, s83, v[70:71]
	v_add_u32_e32 v22, s10, v87
	v_add_u32_e32 v23, s9, v88
	s_waitcnt vmcnt(0)
	ds_write_b32 v18, v24
	s_waitcnt vmcnt(0)
	ds_write_b32 v20, v25
	v_add_u32_e32 v20, s9, v6
	v_add_u32_e32 v18, s10, v7
	v_ashrrev_i32_e32 v21, 31, v20
	v_ashrrev_i32_e32 v19, 31, v18
	v_lshlrev_b64 v[20:21], 12, v[20:21]
	v_lshlrev_b64 v[18:19], 12, v[18:19]
	v_lshl_add_u64 v[20:21], v[0:1], 0, v[20:21]
	v_lshl_add_u64 v[18:19], v[0:1], 0, v[18:19]
	global_load_dword v24, v[20:21], off nt
	global_load_dword v25, v[18:19], off nt
	v_mad_u64_u32 v[18:19], s[2:3], v23, s83, v[70:71]
	v_mad_u64_u32 v[20:21], s[2:3], v22, s83, v[70:71]
	v_add_u32_e32 v22, s10, v89
	v_add_u32_e32 v23, s9, v90
	s_waitcnt vmcnt(0)
	ds_write_b32 v18, v24
	s_waitcnt vmcnt(0)
	ds_write_b32 v20, v25
	v_add_u32_e32 v20, s9, v8
	v_add_u32_e32 v18, s10, v9
	v_ashrrev_i32_e32 v21, 31, v20
	v_ashrrev_i32_e32 v19, 31, v18
	v_lshlrev_b64 v[20:21], 12, v[20:21]
	v_lshlrev_b64 v[18:19], 12, v[18:19]
	v_lshl_add_u64 v[20:21], v[0:1], 0, v[20:21]
	v_lshl_add_u64 v[18:19], v[0:1], 0, v[18:19]
	global_load_dword v24, v[20:21], off nt
	global_load_dword v25, v[18:19], off nt
	v_mad_u64_u32 v[18:19], s[2:3], v23, s83, v[70:71]
	v_mad_u64_u32 v[20:21], s[2:3], v22, s83, v[70:71]
	v_add_u32_e32 v22, s10, v91
	v_add_u32_e32 v23, s9, v92
	s_waitcnt vmcnt(0)
	ds_write_b32 v18, v24
	s_waitcnt vmcnt(0)
	ds_write_b32 v20, v25
	v_add_u32_e32 v20, s9, v10
	v_add_u32_e32 v18, s10, v11
	v_ashrrev_i32_e32 v21, 31, v20
	v_ashrrev_i32_e32 v19, 31, v18
	v_lshlrev_b64 v[20:21], 12, v[20:21]
	v_lshlrev_b64 v[18:19], 12, v[18:19]
	v_lshl_add_u64 v[20:21], v[0:1], 0, v[20:21]
	v_lshl_add_u64 v[18:19], v[0:1], 0, v[18:19]
	global_load_dword v24, v[20:21], off nt
	global_load_dword v25, v[18:19], off nt
	v_mad_u64_u32 v[18:19], s[2:3], v23, s83, v[70:71]
	v_mad_u64_u32 v[20:21], s[2:3], v22, s83, v[70:71]
	v_add_u32_e32 v22, s10, v93
	v_add_u32_e32 v23, s9, v94
	s_waitcnt vmcnt(0)
	ds_write_b32 v18, v24
	s_waitcnt vmcnt(0)
	ds_write_b32 v20, v25
	v_add_u32_e32 v20, s9, v12
	v_add_u32_e32 v18, s10, v13
	v_ashrrev_i32_e32 v21, 31, v20
	v_ashrrev_i32_e32 v19, 31, v18
	v_lshlrev_b64 v[20:21], 12, v[20:21]
	v_lshlrev_b64 v[18:19], 12, v[18:19]
	v_lshl_add_u64 v[20:21], v[0:1], 0, v[20:21]
	v_lshl_add_u64 v[18:19], v[0:1], 0, v[18:19]
	global_load_dword v24, v[20:21], off nt
	global_load_dword v25, v[18:19], off nt
	v_mad_u64_u32 v[18:19], s[2:3], v23, s83, v[70:71]
	v_mad_u64_u32 v[20:21], s[2:3], v22, s83, v[70:71]
	v_add_u32_e32 v22, s10, v95
	v_add_u32_e32 v23, s9, v96
	s_waitcnt vmcnt(0)
	ds_write_b32 v18, v24
	s_waitcnt vmcnt(0)
	ds_write_b32 v20, v25
	v_add_u32_e32 v20, s9, v14
	v_add_u32_e32 v18, s10, v15
	v_ashrrev_i32_e32 v21, 31, v20
	v_ashrrev_i32_e32 v19, 31, v18
	v_lshlrev_b64 v[20:21], 12, v[20:21]
	v_lshlrev_b64 v[18:19], 12, v[18:19]
	v_lshl_add_u64 v[20:21], v[0:1], 0, v[20:21]
	v_lshl_add_u64 v[18:19], v[0:1], 0, v[18:19]
	global_load_dword v24, v[20:21], off nt
	global_load_dword v25, v[18:19], off nt
	v_mad_u64_u32 v[18:19], s[2:3], v23, s83, v[70:71]
	v_mad_u64_u32 v[20:21], s[2:3], v22, s83, v[70:71]
	v_add_u32_e32 v23, s9, v98
	v_add_u32_e32 v22, s10, v97
	s_waitcnt vmcnt(0)
	ds_write_b32 v18, v24
	s_waitcnt vmcnt(0)
	ds_write_b32 v20, v25
	v_add_u32_e32 v20, s9, v16
	v_add_u32_e32 v18, s10, v17
	v_ashrrev_i32_e32 v21, 31, v20
	v_ashrrev_i32_e32 v19, 31, v18
	v_lshlrev_b64 v[20:21], 12, v[20:21]
	v_lshlrev_b64 v[18:19], 12, v[18:19]
	v_lshl_add_u64 v[20:21], v[0:1], 0, v[20:21]
	v_lshl_add_u64 v[18:19], v[0:1], 0, v[18:19]
	global_load_dword v24, v[20:21], off nt
	global_load_dword v25, v[18:19], off nt
	v_mad_u64_u32 v[18:19], s[2:3], v23, s83, v[70:71]
	v_mad_u64_u32 v[20:21], s[2:3], v22, s83, v[70:71]
	s_waitcnt vmcnt(0)
	ds_write_b32 v18, v24
	s_waitcnt vmcnt(0)
	ds_write_b32 v20, v25
	s_cbranch_scc1 .LBB0_678
; #define LAS __attribute__((address_space(3)))
; __device__ __forceinline__ unsigned pk2(float lo, float hi) { unsigned r; asm("v_cvt_pk_bf16_f32 %0, %1, %2" : "=v"(r) : "v"(lo), "v"(hi)); return r; }
; template <int QPERM>
; __device__ __forceinline__ void transpose_item(const float* W, int K, int N, bf16_t* WT, LAS float* scr, int item, int lane) {
;     ...
;     asm volatile("s_waitcnt lgkmcnt(0)" ::: "memory");
;     const int c = lane & 7;
; #pragma unroll
;     for (int j = 0; j < 4; ++j) { const int n = (lane >> 3) + 8 * j; const LAS float* s = scr + (8 * c) * 33 + n;
;         u32x4 o; o.x = pk2(s[0 * 33], s[1 * 33]); o.y = pk2(s[2 * 33], s[3 * 33]); o.z = pk2(s[4 * 33], s[5 * 33]); o.w = pk2(s[6 * 33], s[7 * 33]);
;         int dn = n0 + n;
;         if (QPERM == 1) { const int h = dn / 192, d = dn % 192; if (d >= 128) { const int jj = d - 128, a = jj >> 5, p = (jj >> 4) & 1, f = jj & 15; dn = h * 192 + 128 + 2 * (a * 16 + f) + p; } }
;         if (QPERM == 2) { const int h = dn >> 8, j = dn & 255; dn = (j < 128) ? h * 128 + j : 512 + h * 128 + (j - 128); }
;         *(u32x4*)(WT + (size_t)dn * K + k0 + 8 * c) = o; }
;     asm volatile("s_waitcnt lgkmcnt(0)" ::: "memory");
	s_waitcnt lgkmcnt(0)
	ds_read2_b32 v[6:7], v113 offset0:33 offset1:41
	ds_read2_b32 v[8:9], v113 offset1:8
	ds_read2_b32 v[10:11], v113 offset0:66 offset1:74
	ds_read2_b32 v[12:13], v113 offset0:99 offset1:107
	s_lshl_b32 s10, s1, 1
	s_mov_b32 s1, s11
	v_writelane_b32 v253, s0, 32
	s_waitcnt lgkmcnt(2)
	v_cvt_pk_bf16_f32 v0, v8, v6
	s_movk_i32 s2, 0x180
	s_waitcnt lgkmcnt(0)
	v_cvt_pk_bf16_f32 v1, v10, v12
	ds_read2_b32 v[14:15], v113 offset0:132 offset1:140
	ds_read2_b32 v[16:17], v113 offset0:165 offset1:173
	v_add_u32_e32 v6, s0, v112
	v_and_b32_e32 v8, 0xff, v6
	v_ashrrev_i32_e32 v6, 1, v6
	v_writelane_b32 v253, s1, 33
	s_movk_i32 s1, 0x80
	v_and_b32_e32 v6, 0xffffff80, v6
	ds_read2_b32 v[18:19], v113 offset0:198 offset1:206
	ds_read2_b32 v[20:21], v113 offset0:231 offset1:239
	v_cmp_gt_u32_e32 vcc, s1, v8
	v_or_b32_e32 v10, v6, v8
	v_add3_u32 v6, v8, v6, s2
	v_cndmask_b32_e32 v22, v6, v10, vcc
	v_ashrrev_i32_e32 v23, 31, v22
	v_lshl_add_u64 v[4:5], v[76:77], 0, s[10:11]
	v_lshlrev_b64 v[22:23], 9, v[22:23]
	v_lshl_add_u64 v[22:23], v[4:5], 0, v[22:23]
	v_add_u32_e32 v6, s0, v114
	s_waitcnt lgkmcnt(2)
	v_cvt_pk_bf16_f32 v2, v14, v16
	s_waitcnt lgkmcnt(0)
	v_cvt_pk_bf16_f32 v3, v18, v20
	global_store_dwordx4 v[22:23], v[0:3], off nt
	s_nop 1
	v_cvt_pk_bf16_f32 v0, v9, v7
	v_and_b32_e32 v7, 0xff, v6
	v_ashrrev_i32_e32 v6, 1, v6
	v_and_b32_e32 v6, 0xffffff80, v6
	v_cmp_gt_u32_e32 vcc, s1, v7
	v_or_b32_e32 v8, v6, v7
	v_add3_u32 v6, v7, v6, s2
	v_cndmask_b32_e32 v6, v6, v8, vcc
	v_ashrrev_i32_e32 v7, 31, v6
	v_lshlrev_b64 v[6:7], 9, v[6:7]
	v_lshl_add_u64 v[6:7], v[4:5], 0, v[6:7]
	v_cvt_pk_bf16_f32 v1, v11, v13
	v_cvt_pk_bf16_f32 v2, v15, v17
	v_cvt_pk_bf16_f32 v3, v19, v21
	global_store_dwordx4 v[6:7], v[0:3], off nt
	ds_read2_b32 v[6:7], v113 offset0:16 offset1:24
	ds_read2_b32 v[8:9], v113 offset0:49 offset1:57
	ds_read2_b32 v[10:11], v113 offset0:82 offset1:90
	ds_read2_b32 v[12:13], v113 offset0:115 offset1:123
	s_waitcnt lgkmcnt(2)
	v_cvt_pk_bf16_f32 v0, v6, v8
	v_add_u32_e32 v6, s0, v115
	v_and_b32_e32 v8, 0xff, v6
	v_ashrrev_i32_e32 v6, 1, v6
	v_and_b32_e32 v6, 0xffffff80, v6
	s_waitcnt lgkmcnt(0)
	v_cvt_pk_bf16_f32 v1, v10, v12
	ds_read2_b32 v[14:15], v113 offset0:148 offset1:156
	ds_read2_b32 v[16:17], v113 offset0:181 offset1:189
	ds_read2_b32 v[18:19], v113 offset0:214 offset1:222
	ds_read2_b32 v[20:21], v113 offset0:247 offset1:255
	v_cmp_gt_u32_e32 vcc, s1, v8
	v_or_b32_e32 v10, v6, v8
	v_add3_u32 v6, v8, v6, s2
	v_cndmask_b32_e32 v22, v6, v10, vcc
	v_ashrrev_i32_e32 v23, 31, v22
	v_lshlrev_b64 v[22:23], 9, v[22:23]
	v_lshl_add_u64 v[22:23], v[4:5], 0, v[22:23]
	v_add_u32_e32 v6, s0, v116
	s_waitcnt lgkmcnt(2)
	v_cvt_pk_bf16_f32 v2, v14, v16
	s_waitcnt lgkmcnt(0)
	v_cvt_pk_bf16_f32 v3, v18, v20
	global_store_dwordx4 v[22:23], v[0:3], off nt
	s_nop 1
	v_cvt_pk_bf16_f32 v0, v7, v9
	v_and_b32_e32 v7, 0xff, v6
	v_ashrrev_i32_e32 v6, 1, v6
	v_and_b32_e32 v6, 0xffffff80, v6
	v_cmp_gt_u32_e32 vcc, s1, v7
	v_or_b32_e32 v8, v6, v7
	v_add3_u32 v6, v7, v6, s2
	v_cndmask_b32_e32 v6, v6, v8, vcc
	v_ashrrev_i32_e32 v7, 31, v6
	v_lshlrev_b64 v[6:7], 9, v[6:7]
	v_lshl_add_u64 v[4:5], v[4:5], 0, v[6:7]
	v_cvt_pk_bf16_f32 v1, v11, v13
	v_cvt_pk_bf16_f32 v2, v15, v17
	v_cvt_pk_bf16_f32 v3, v19, v21
	global_store_dwordx4 v[4:5], v[0:3], off nt
	s_waitcnt lgkmcnt(0)

; #define LAS __attribute__((address_space(3)))
; template <int QPERM>
; __device__ __forceinline__ void transpose_item(const float* W, int K, int N, bf16_t* WT, LAS float* scr, int item, int lane) {
;     const int nblk = N / 32, kb = item / nblk, nb = item % nblk, k0 = 64 * kb, n0 = 32 * nb;
; #pragma unroll 8
;     for (int i = 0; i < 32; ++i) { const int kk = 2 * i + (lane >> 5); scr[kk * 33 + (lane & 31)] = W[(size_t)(k0 + kk) * N + n0 + (lane & 31)]; }
.LBB0_683:
	s_lshl_b32 s9, s8, 1
	s_lshl_b32 s10, s1, 1
	v_add_u32_e32 v18, s9, v2
	v_add_u32_e32 v20, s10, v3
	v_mad_i64_i32 v[18:19], s[2:3], v18, s4, v[0:1]
	v_mad_i64_i32 v[20:21], s[2:3], v20, s4, v[0:1]
	global_load_dword v24, v[18:19], off nt
	global_load_dword v25, v[20:21], off nt
	v_add_u32_e32 v23, s9, v128
	v_add_u32_e32 v22, s10, v65
	v_mad_u64_u32 v[18:19], s[2:3], v23, s83, v[70:71]
	v_mad_u64_u32 v[20:21], s[2:3], v22, s83, v[70:71]
	v_add_u32_e32 v23, s9, v86
	v_add_u32_e32 v22, s10, v71
	s_add_i32 s8, s8, 16
	s_add_i32 s1, s1, 16
	s_add_i32 s0, s0, -16
	s_cmp_lg_u32 s0, 0
	s_waitcnt vmcnt(0)
	ds_write_b32 v18, v24
	ds_write_b32 v20, v25
	v_add_u32_e32 v18, s9, v4
	v_add_u32_e32 v20, s10, v5
	v_mad_i64_i32 v[18:19], s[2:3], v18, s4, v[0:1]
	v_mad_i64_i32 v[20:21], s[2:3], v20, s4, v[0:1]
	global_load_dword v24, v[18:19], off nt
	global_load_dword v25, v[20:21], off nt
	v_mad_u64_u32 v[18:19], s[2:3], v23, s83, v[70:71]
	v_mad_u64_u32 v[20:21], s[2:3], v22, s83, v[70:71]
	v_add_u32_e32 v23, s9, v88
	v_add_u32_e32 v22, s10, v87
	s_waitcnt vmcnt(0)
	ds_write_b32 v18, v24
	s_waitcnt vmcnt(0)
	ds_write_b32 v20, v25
	v_add_u32_e32 v18, s9, v6
	v_add_u32_e32 v20, s10, v7
	v_mad_i64_i32 v[18:19], s[2:3], v18, s4, v[0:1]
	v_mad_i64_i32 v[20:21], s[2:3], v20, s4, v[0:1]
	global_load_dword v24, v[18:19], off nt
	global_load_dword v25, v[20:21], off nt
	v_mad_u64_u32 v[18:19], s[2:3], v23, s83, v[70:71]
	v_mad_u64_u32 v[20:21], s[2:3], v22, s83, v[70:71]
	v_add_u32_e32 v23, s9, v90
	v_add_u32_e32 v22, s10, v89
	s_waitcnt vmcnt(0)
	ds_write_b32 v18, v24
	s_waitcnt vmcnt(0)
	ds_write_b32 v20, v25
	v_add_u32_e32 v18, s9, v8
	v_add_u32_e32 v20, s10, v9
	v_mad_i64_i32 v[18:19], s[2:3], v18, s4, v[0:1]
	v_mad_i64_i32 v[20:21], s[2:3], v20, s4, v[0:1]
	global_load_dword v24, v[18:19], off nt
	global_load_dword v25, v[20:21], off nt
	v_mad_u64_u32 v[18:19], s[2:3], v23, s83, v[70:71]
	v_mad_u64_u32 v[20:21], s[2:3], v22, s83, v[70:71]
	v_add_u32_e32 v23, s9, v92
	v_add_u32_e32 v22, s10, v91
	s_waitcnt vmcnt(0)
	ds_write_b32 v18, v24
	s_waitcnt vmcnt(0)
	ds_write_b32 v20, v25
	v_add_u32_e32 v18, s9, v10
	v_add_u32_e32 v20, s10, v11
	v_mad_i64_i32 v[18:19], s[2:3], v18, s4, v[0:1]
	v_mad_i64_i32 v[20:21], s[2:3], v20, s4, v[0:1]
	global_load_dword v24, v[18:19], off nt
	global_load_dword v25, v[20:21], off nt
	v_mad_u64_u32 v[18:19], s[2:3], v23, s83, v[70:71]
	v_mad_u64_u32 v[20:21], s[2:3], v22, s83, v[70:71]
	v_add_u32_e32 v23, s9, v94
	v_add_u32_e32 v22, s10, v93
	s_waitcnt vmcnt(0)
	ds_write_b32 v18, v24
	s_waitcnt vmcnt(0)
	ds_write_b32 v20, v25
	v_add_u32_e32 v18, s9, v12
	v_add_u32_e32 v20, s10, v13
	v_mad_i64_i32 v[18:19], s[2:3], v18, s4, v[0:1]
	v_mad_i64_i32 v[20:21], s[2:3], v20, s4, v[0:1]
	global_load_dword v24, v[18:19], off nt
	global_load_dword v25, v[20:21], off nt
	v_mad_u64_u32 v[18:19], s[2:3], v23, s83, v[70:71]
	v_mad_u64_u32 v[20:21], s[2:3], v22, s83, v[70:71]
	v_add_u32_e32 v23, s9, v96
	v_add_u32_e32 v22, s10, v95
	s_waitcnt vmcnt(0)
	ds_write_b32 v18, v24
	s_waitcnt vmcnt(0)
	ds_write_b32 v20, v25
	v_add_u32_e32 v18, s9, v14
	v_add_u32_e32 v20, s10, v15
	v_mad_i64_i32 v[18:19], s[2:3], v18, s4, v[0:1]
	v_mad_i64_i32 v[20:21], s[2:3], v20, s4, v[0:1]
	global_load_dword v24, v[18:19], off nt
	global_load_dword v25, v[20:21], off nt
	v_mad_u64_u32 v[18:19], s[2:3], v23, s83, v[70:71]
	v_mad_u64_u32 v[20:21], s[2:3], v22, s83, v[70:71]
	v_add_u32_e32 v23, s9, v98
	v_add_u32_e32 v22, s10, v97
	s_waitcnt vmcnt(0)
	ds_write_b32 v18, v24
	s_waitcnt vmcnt(0)
	ds_write_b32 v20, v25
	v_add_u32_e32 v18, s9, v16
	v_add_u32_e32 v20, s10, v17
	v_mad_i64_i32 v[18:19], s[2:3], v18, s4, v[0:1]
	v_mad_i64_i32 v[20:21], s[2:3], v20, s4, v[0:1]
	global_load_dword v24, v[18:19], off nt
	global_load_dword v25, v[20:21], off nt
	v_mad_u64_u32 v[18:19], s[2:3], v23, s83, v[70:71]
	v_mad_u64_u32 v[20:21], s[2:3], v22, s83, v[70:71]
	s_waitcnt vmcnt(0)
	ds_write_b32 v18, v24
	s_waitcnt vmcnt(0)
	ds_write_b32 v20, v25
	s_cbranch_scc1 .LBB0_683
; #define LAS __attribute__((address_space(3)))
; __device__ __forceinline__ unsigned pk2(float lo, float hi) { unsigned r; asm("v_cvt_pk_bf16_f32 %0, %1, %2" : "=v"(r) : "v"(lo), "v"(hi)); return r; }
; template <int QPERM>
; __device__ __forceinline__ void transpose_item(const float* W, int K, int N, bf16_t* WT, LAS float* scr, int item, int lane) {
;     ...
;     asm volatile("s_waitcnt lgkmcnt(0)" ::: "memory");
;     const int c = lane & 7;
; #pragma unroll
;     for (int j = 0; j < 4; ++j) { const int n = (lane >> 3) + 8 * j; const LAS float* s = scr + (8 * c) * 33 + n;
;         u32x4 o; o.x = pk2(s[0 * 33], s[1 * 33]); o.y = pk2(s[2 * 33], s[3 * 33]); o.z = pk2(s[4 * 33], s[5 * 33]); o.w = pk2(s[6 * 33], s[7 * 33]);
;         int dn = n0 + n;
;         if (QPERM == 1) { const int h = dn / 192, d = dn % 192; if (d >= 128) { const int jj = d - 128, a = jj >> 5, p = (jj >> 4) & 1, f = jj & 15; dn = h * 192 + 128 + 2 * (a * 16 + f) + p; } }
;         if (QPERM == 2) { const int h = dn >> 8, j = dn & 255; dn = (j < 128) ? h * 128 + j : 512 + h * 128 + (j - 128); }
;         *(u32x4*)(WT + (size_t)dn * K + k0 + 8 * c) = o; }
;     asm volatile("s_waitcnt lgkmcnt(0)" ::: "memory");
	s_waitcnt lgkmcnt(0)
	ds_read2_b32 v[0:1], v113 offset1:33
	ds_read2_b32 v[2:3], v113 offset0:66 offset1:99
	s_waitcnt lgkmcnt(1)
	v_cvt_pk_bf16_f32 v0, v0, v1
	s_waitcnt lgkmcnt(0)
	v_cvt_pk_bf16_f32 v1, v2, v3
	ds_read2_b32 v[2:3], v113 offset0:132 offset1:165
	ds_read2_b32 v[4:5], v113 offset0:198 offset1:231
	v_add_u32_e32 v6, s6, v112
	s_mov_b32 s4, 0x2aaaaaab
	s_waitcnt lgkmcnt(1)
	v_cvt_pk_bf16_f32 v2, v2, v3
	s_waitcnt lgkmcnt(0)
	v_cvt_pk_bf16_f32 v3, v4, v5
	v_mul_hi_i32 v4, v6, s4
	v_lshrrev_b32_e32 v5, 31, v4
	v_lshrrev_b32_e32 v4, 5, v4
	v_add_u32_e32 v4, v4, v5
	s_movk_i32 s0, 0xc0
	v_mul_lo_u32 v4, v4, s0
	v_sub_u32_e32 v4, v6, v4
	s_movk_i32 s0, 0x7f
	v_cmp_lt_i32_e32 vcc, s0, v4
	s_and_saveexec_b64 s[0:1], vcc
	v_bfe_u32 v5, v4, 4, 1
	v_lshlrev_b32_e32 v7, 1, v4
	v_and_b32_e32 v8, 0x7fffffe0, v4
	v_sub_u32_e32 v4, v6, v4
	v_and_b32_e32 v7, 30, v7
	v_add_u32_e32 v4, v4, v8
	v_add3_u32 v6, v4, v7, v5
	s_or_b64 exec, exec, s[0:1]
	s_mov_b32 s1, s11
	s_lshl_b32 s10, s7, 1
	v_writelane_b32 v253, s0, 32
	v_lshl_add_u64 v[4:5], v[80:81], 0, s[10:11]
	s_nop 0
	v_writelane_b32 v253, s1, 33
	s_movk_i32 s0, 0x300
	v_mad_i64_i32 v[6:7], s[0:1], v6, s0, v[4:5]
	global_store_dwordx4 v[6:7], v[0:3], off nt
	ds_read2_b32 v[0:1], v113 offset0:8 offset1:41
	ds_read2_b32 v[2:3], v113 offset0:74 offset1:107
	s_waitcnt lgkmcnt(1)
	v_cvt_pk_bf16_f32 v0, v0, v1
	s_waitcnt lgkmcnt(0)
	v_cvt_pk_bf16_f32 v1, v2, v3
	ds_read2_b32 v[2:3], v113 offset0:140 offset1:173
	ds_read2_b32 v[6:7], v113 offset0:206 offset1:239
	s_waitcnt lgkmcnt(1)
	v_cvt_pk_bf16_f32 v2, v2, v3
	s_waitcnt lgkmcnt(0)
	v_cvt_pk_bf16_f32 v3, v6, v7
	v_add_u32_e32 v6, s6, v114
	v_mul_hi_i32 v7, v6, s4
	v_lshrrev_b32_e32 v8, 31, v7
	v_lshrrev_b32_e32 v7, 5, v7
	v_add_u32_e32 v7, v7, v8
	s_movk_i32 s0, 0xc0
	v_mul_lo_u32 v7, v7, s0
	v_sub_u32_e32 v7, v6, v7
	s_movk_i32 s0, 0x7f
	v_cmp_lt_i32_e32 vcc, s0, v7
	s_and_saveexec_b64 s[0:1], vcc
	v_lshlrev_b32_e32 v9, 1, v7
	v_and_b32_e32 v10, 0x7fffffe0, v7
	v_sub_u32_e32 v6, v6, v7
	v_bfe_u32 v8, v7, 4, 1
	v_and_b32_e32 v9, 30, v9
	v_add_u32_e32 v6, v6, v10
	v_add3_u32 v6, v6, v9, v8
	s_or_b64 exec, exec, s[0:1]
	s_movk_i32 s0, 0x300
	v_mad_i64_i32 v[6:7], s[0:1], v6, s0, v[4:5]
	global_store_dwordx4 v[6:7], v[0:3], off nt
	ds_read2_b32 v[0:1], v113 offset0:16 offset1:49
	ds_read2_b32 v[2:3], v113 offset0:82 offset1:115
	s_waitcnt lgkmcnt(1)
	v_cvt_pk_bf16_f32 v0, v0, v1
	s_waitcnt lgkmcnt(0)
	v_cvt_pk_bf16_f32 v1, v2, v3
	ds_read2_b32 v[2:3], v113 offset0:148 offset1:181
	ds_read2_b32 v[6:7], v113 offset0:214 offset1:247
	s_waitcnt lgkmcnt(1)
	v_cvt_pk_bf16_f32 v2, v2, v3
	s_waitcnt lgkmcnt(0)
	v_cvt_pk_bf16_f32 v3, v6, v7
	v_add_u32_e32 v6, s6, v115
	v_mul_hi_i32 v7, v6, s4
	v_lshrrev_b32_e32 v8, 31, v7
	v_lshrrev_b32_e32 v7, 5, v7
	v_add_u32_e32 v7, v7, v8
	s_movk_i32 s0, 0xc0
	v_mul_lo_u32 v7, v7, s0
	v_sub_u32_e32 v7, v6, v7
	s_movk_i32 s0, 0x7f
	v_cmp_lt_i32_e32 vcc, s0, v7
	s_and_saveexec_b64 s[0:1], vcc
	v_lshlrev_b32_e32 v9, 1, v7
	v_and_b32_e32 v10, 0x7fffffe0, v7
	v_sub_u32_e32 v6, v6, v7
	v_bfe_u32 v8, v7, 4, 1
	v_and_b32_e32 v9, 30, v9
	v_add_u32_e32 v6, v6, v10
	v_add3_u32 v6, v6, v9, v8
	s_or_b64 exec, exec, s[0:1]
	s_movk_i32 s0, 0x300
	v_mad_i64_i32 v[6:7], s[0:1], v6, s0, v[4:5]
	global_store_dwordx4 v[6:7], v[0:3], off nt
	ds_read2_b32 v[0:1], v113 offset0:24 offset1:57
	ds_read2_b32 v[2:3], v113 offset0:90 offset1:123
	s_waitcnt lgkmcnt(1)
	v_cvt_pk_bf16_f32 v0, v0, v1
	s_waitcnt lgkmcnt(0)
	v_cvt_pk_bf16_f32 v1, v2, v3
	ds_read2_b32 v[2:3], v113 offset0:156 offset1:189
	ds_read2_b32 v[6:7], v113 offset0:222 offset1:255
	s_waitcnt lgkmcnt(1)
	v_cvt_pk_bf16_f32 v2, v2, v3
	s_waitcnt lgkmcnt(0)
	v_cvt_pk_bf16_f32 v3, v6, v7
	v_add_u32_e32 v6, s6, v116
	v_mul_hi_i32 v7, v6, s4
	v_lshrrev_b32_e32 v8, 31, v7
	v_lshrrev_b32_e32 v7, 5, v7
	v_add_u32_e32 v7, v7, v8
	s_movk_i32 s0, 0xc0
	v_mul_lo_u32 v7, v7, s0
	v_sub_u32_e32 v7, v6, v7
	s_movk_i32 s0, 0x7f
	v_cmp_lt_i32_e32 vcc, s0, v7
	s_and_saveexec_b64 s[0:1], vcc
	v_lshlrev_b32_e32 v9, 1, v7
	v_and_b32_e32 v10, 0x7fffffe0, v7
	v_sub_u32_e32 v6, v6, v7
	v_bfe_u32 v8, v7, 4, 1
	v_and_b32_e32 v9, 30, v9
	v_add_u32_e32 v6, v6, v10
	v_add3_u32 v6, v6, v9, v8
	s_or_b64 exec, exec, s[0:1]
	s_movk_i32 s0, 0x300
	v_mad_i64_i32 v[4:5], s[0:1], v6, s0, v[4:5]
	global_store_dwordx4 v[4:5], v[0:3], off nt
	s_waitcnt lgkmcnt(0)

; #define LAS __attribute__((address_space(3)))
; __device__ __forceinline__ void transpose_item_fp8(const float* W, int K, int N, unsigned char* WT, float q, LAS float* scr, int item, int lane) {
;     const int nblk = N / 32, kb = item / nblk, nb = item % nblk, k0 = 64 * kb, n0 = 32 * nb;
; #pragma unroll 8
;     for (int i = 0; i < 32; ++i) { const int kk = 2 * i + (lane >> 5); scr[kk * 33 + (lane & 31)] = W[(size_t)(k0 + kk) * N + n0 + (lane & 31)]; }
.LBB0_696:
	s_lshl_b32 s9, s1, 1
	s_lshl_b32 s10, s0, 1
	v_add_u32_e32 v18, s9, v2
	v_add_u32_e32 v20, s10, v3
	v_mad_i64_i32 v[18:19], s[2:3], v18, s82, v[0:1]
	v_mad_i64_i32 v[20:21], s[2:3], v20, s82, v[0:1]
	global_load_dword v24, v[18:19], off nt
	global_load_dword v25, v[20:21], off nt
	v_add_u32_e32 v23, s9, v128
	v_add_u32_e32 v22, s10, v65
	v_mad_u64_u32 v[18:19], s[2:3], v23, s83, v[70:71]
	v_mad_u64_u32 v[20:21], s[2:3], v22, s83, v[70:71]
	v_add_u32_e32 v23, s9, v86
	v_add_u32_e32 v22, s10, v71
	s_add_i32 s1, s1, 16
	s_add_i32 s0, s0, 16
	s_add_i32 s7, s7, -16
	s_cmp_lg_u32 s7, 0
	s_waitcnt vmcnt(0)
	ds_write_b32 v18, v24
	ds_write_b32 v20, v25
	v_add_u32_e32 v18, s9, v4
	v_add_u32_e32 v20, s10, v5
	v_mad_i64_i32 v[18:19], s[2:3], v18, s82, v[0:1]
	v_mad_i64_i32 v[20:21], s[2:3], v20, s82, v[0:1]
	global_load_dword v24, v[18:19], off nt
	global_load_dword v25, v[20:21], off nt
	v_mad_u64_u32 v[18:19], s[2:3], v23, s83, v[70:71]
	v_mad_u64_u32 v[20:21], s[2:3], v22, s83, v[70:71]
	v_add_u32_e32 v23, s9, v88
	v_add_u32_e32 v22, s10, v87
	s_waitcnt vmcnt(0)
	ds_write_b32 v18, v24
	s_waitcnt vmcnt(0)
	ds_write_b32 v20, v25
	v_add_u32_e32 v18, s9, v6
	v_add_u32_e32 v20, s10, v7
	v_mad_i64_i32 v[18:19], s[2:3], v18, s82, v[0:1]
	v_mad_i64_i32 v[20:21], s[2:3], v20, s82, v[0:1]
	global_load_dword v24, v[18:19], off nt
	global_load_dword v25, v[20:21], off nt
	v_mad_u64_u32 v[18:19], s[2:3], v23, s83, v[70:71]
	v_mad_u64_u32 v[20:21], s[2:3], v22, s83, v[70:71]
	v_add_u32_e32 v23, s9, v90
	v_add_u32_e32 v22, s10, v89
	s_waitcnt vmcnt(0)
	ds_write_b32 v18, v24
	s_waitcnt vmcnt(0)
	ds_write_b32 v20, v25
	v_add_u32_e32 v18, s9, v8
	v_add_u32_e32 v20, s10, v9
	v_mad_i64_i32 v[18:19], s[2:3], v18, s82, v[0:1]
	v_mad_i64_i32 v[20:21], s[2:3], v20, s82, v[0:1]
	global_load_dword v24, v[18:19], off nt
	global_load_dword v25, v[20:21], off nt
	v_mad_u64_u32 v[18:19], s[2:3], v23, s83, v[70:71]
	v_mad_u64_u32 v[20:21], s[2:3], v22, s83, v[70:71]
	v_add_u32_e32 v23, s9, v92
	v_add_u32_e32 v22, s10, v91
	s_waitcnt vmcnt(0)
	ds_write_b32 v18, v24
	s_waitcnt vmcnt(0)
	ds_write_b32 v20, v25
	v_add_u32_e32 v18, s9, v10
	v_add_u32_e32 v20, s10, v11
	v_mad_i64_i32 v[18:19], s[2:3], v18, s82, v[0:1]
	v_mad_i64_i32 v[20:21], s[2:3], v20, s82, v[0:1]
	global_load_dword v24, v[18:19], off nt
	global_load_dword v25, v[20:21], off nt
	v_mad_u64_u32 v[18:19], s[2:3], v23, s83, v[70:71]
	v_mad_u64_u32 v[20:21], s[2:3], v22, s83, v[70:71]
	v_add_u32_e32 v23, s9, v94
	v_add_u32_e32 v22, s10, v93
	s_waitcnt vmcnt(0)
	ds_write_b32 v18, v24
	s_waitcnt vmcnt(0)
	ds_write_b32 v20, v25
	v_add_u32_e32 v18, s9, v12
	v_add_u32_e32 v20, s10, v13
	v_mad_i64_i32 v[18:19], s[2:3], v18, s82, v[0:1]
	v_mad_i64_i32 v[20:21], s[2:3], v20, s82, v[0:1]
	global_load_dword v24, v[18:19], off nt
	global_load_dword v25, v[20:21], off nt
	v_mad_u64_u32 v[18:19], s[2:3], v23, s83, v[70:71]
	v_mad_u64_u32 v[20:21], s[2:3], v22, s83, v[70:71]
	v_add_u32_e32 v23, s9, v96
	v_add_u32_e32 v22, s10, v95
	s_waitcnt vmcnt(0)
	ds_write_b32 v18, v24
	s_waitcnt vmcnt(0)
	ds_write_b32 v20, v25
	v_add_u32_e32 v18, s9, v14
	v_add_u32_e32 v20, s10, v15
	v_mad_i64_i32 v[18:19], s[2:3], v18, s82, v[0:1]
	v_mad_i64_i32 v[20:21], s[2:3], v20, s82, v[0:1]
	global_load_dword v24, v[18:19], off nt
	global_load_dword v25, v[20:21], off nt
	v_mad_u64_u32 v[18:19], s[2:3], v23, s83, v[70:71]
	v_mad_u64_u32 v[20:21], s[2:3], v22, s83, v[70:71]
	v_add_u32_e32 v23, s9, v98
	v_add_u32_e32 v22, s10, v97
	s_waitcnt vmcnt(0)
	ds_write_b32 v18, v24
	s_waitcnt vmcnt(0)
	ds_write_b32 v20, v25
	v_add_u32_e32 v18, s9, v16
	v_add_u32_e32 v20, s10, v17
	v_mad_i64_i32 v[18:19], s[2:3], v18, s82, v[0:1]
	v_mad_i64_i32 v[20:21], s[2:3], v20, s82, v[0:1]
	global_load_dword v24, v[18:19], off nt
	global_load_dword v25, v[20:21], off nt
	v_mad_u64_u32 v[18:19], s[2:3], v23, s83, v[70:71]
	v_mad_u64_u32 v[20:21], s[2:3], v22, s83, v[70:71]
	s_waitcnt vmcnt(0)
	ds_write_b32 v18, v24
	s_waitcnt vmcnt(0)
	ds_write_b32 v20, v25
	s_cbranch_scc1 .LBB0_696
; #define LAS __attribute__((address_space(3)))
; __device__ __forceinline__ unsigned pk4_fp8(float x0, float x1, float x2, float x3) { int w = 0; w = __builtin_amdgcn_cvt_pk_fp8_f32(x0, x1, w, false); w = __builtin_amdgcn_cvt_pk_fp8_f32(x2, x3, w, true); return (unsigned)w; }
; __device__ __forceinline__ void transpose_item_fp8(const float* W, int K, int N, unsigned char* WT, float q, LAS float* scr, int item, int lane) {
;     ...
;     asm volatile("s_waitcnt lgkmcnt(0)" ::: "memory");
;     const int c = lane & 7;
; #pragma unroll
;     for (int j = 0; j < 4; ++j) { const int n = (lane >> 3) + 8 * j; const LAS float* s = scr + (8 * c) * 33 + n;
;         u32x2 o; o.x = pk4_fp8(s[0 * 33] * q, s[1 * 33] * q, s[2 * 33] * q, s[3 * 33] * q); o.y = pk4_fp8(s[4 * 33] * q, s[5 * 33] * q, s[6 * 33] * q, s[7 * 33] * q);
;         *(u32x2*)(WT + (size_t)(n0 + n) * K + k0 + 8 * c) = o; }
;     asm volatile("s_waitcnt lgkmcnt(0)" ::: "memory");
	s_waitcnt lgkmcnt(0)
	ds_read2_b32 v[2:3], v113 offset1:8
	ds_read2_b32 v[4:5], v113 offset0:33 offset1:41
	ds_read2_b32 v[12:13], v113 offset0:132 offset1:140
	ds_read2_b32 v[14:15], v113 offset0:165 offset1:173
	ds_read2_b32 v[6:7], v113 offset0:66 offset1:74
	ds_read2_b32 v[8:9], v113 offset0:99 offset1:107
	s_waitcnt lgkmcnt(5)
	v_mul_f32_e32 v2, 0x43000000, v2
	s_waitcnt lgkmcnt(4)
	v_mul_f32_e32 v4, 0x43000000, v4
	v_mov_b32_e32 v10, v153
	ds_read2_b32 v[16:17], v113 offset0:198 offset1:206
	ds_read2_b32 v[18:19], v113 offset0:231 offset1:239
	v_cvt_pk_fp8_f32 v10, v2, v4
	s_waitcnt lgkmcnt(5)
	v_mul_f32_e32 v2, 0x43000000, v12
	s_waitcnt lgkmcnt(4)
	v_mul_f32_e32 v4, 0x43000000, v14
	v_mov_b32_e32 v11, v153
	v_cvt_pk_fp8_f32 v11, v2, v4
	v_mul_f32_e32 v3, 0x43000000, v3
	v_mul_f32_e32 v4, 0x43000000, v5
	v_mov_b32_e32 v2, v153
	v_cvt_pk_fp8_f32 v2, v3, v4
	s_waitcnt lgkmcnt(3)
	v_mul_f32_e32 v6, 0x43000000, v6
	s_waitcnt lgkmcnt(2)
	v_mul_f32_e32 v8, 0x43000000, v8
	v_cvt_pk_fp8_f32 v10, v6, v8 op_sel:[0,0,1]
	s_waitcnt lgkmcnt(1)
	v_mul_f32_e32 v6, 0x43000000, v16
	s_waitcnt lgkmcnt(0)
	v_mul_f32_e32 v8, 0x43000000, v18
	v_cvt_pk_fp8_f32 v11, v6, v8 op_sel:[0,0,1]
	v_mul_f32_e32 v5, 0x43000000, v7
	v_mul_f32_e32 v6, 0x43000000, v9
	v_cvt_pk_fp8_f32 v2, v5, v6 op_sel:[0,0,1]
	v_mul_f32_e32 v4, 0x43000000, v13
	v_mul_f32_e32 v5, 0x43000000, v15
	v_mov_b32_e32 v3, v153
	v_cvt_pk_fp8_f32 v3, v4, v5
	v_mul_f32_e32 v6, 0x43000000, v17
	v_mul_f32_e32 v7, 0x43000000, v19
	v_add_u32_e32 v4, s6, v114
	v_cvt_pk_fp8_f32 v3, v6, v7 op_sel:[0,0,1]
	s_ashr_i32 s9, s8, 31
	v_ashrrev_i32_e32 v5, 31, v4
	v_lshl_add_u64 v[0:1], v[84:85], 0, s[8:9]
	v_lshlrev_b64 v[4:5], 10, v[4:5]
	v_lshl_add_u64 v[4:5], v[0:1], 0, v[4:5]
	global_store_dwordx2 v[4:5], v[2:3], off nt
	ds_read2_b32 v[2:3], v113 offset0:16 offset1:24
	ds_read2_b32 v[4:5], v113 offset0:49 offset1:57
	v_add_u32_e32 v20, s6, v112
	ds_read2_b32 v[12:13], v113 offset0:148 offset1:156
	ds_read2_b32 v[14:15], v113 offset0:181 offset1:189
	v_ashrrev_i32_e32 v21, 31, v20
	v_lshlrev_b64 v[20:21], 10, v[20:21]
	v_lshl_add_u64 v[20:21], v[0:1], 0, v[20:21]
	ds_read2_b32 v[6:7], v113 offset0:82 offset1:90
	ds_read2_b32 v[8:9], v113 offset0:115 offset1:123
	global_store_dwordx2 v[20:21], v[10:11], off nt
	s_waitcnt lgkmcnt(5)
	v_mul_f32_e32 v2, 0x43000000, v2
	s_waitcnt lgkmcnt(4)
	v_mul_f32_e32 v4, 0x43000000, v4
	v_mov_b32_e32 v10, v153
	ds_read2_b32 v[16:17], v113 offset0:214 offset1:222
	ds_read2_b32 v[18:19], v113 offset0:247 offset1:255
	v_cvt_pk_fp8_f32 v10, v2, v4
	s_waitcnt lgkmcnt(5)
	v_mul_f32_e32 v2, 0x43000000, v12
	s_waitcnt lgkmcnt(4)
	v_mul_f32_e32 v4, 0x43000000, v14
	v_mov_b32_e32 v11, v153
	v_cvt_pk_fp8_f32 v11, v2, v4
	v_mul_f32_e32 v3, 0x43000000, v3
	v_mul_f32_e32 v4, 0x43000000, v5
	v_mov_b32_e32 v2, v153
	v_cvt_pk_fp8_f32 v2, v3, v4
	s_waitcnt lgkmcnt(3)
	v_mul_f32_e32 v6, 0x43000000, v6
	s_waitcnt lgkmcnt(2)
	v_mul_f32_e32 v8, 0x43000000, v8
	v_cvt_pk_fp8_f32 v10, v6, v8 op_sel:[0,0,1]
	s_waitcnt lgkmcnt(1)
	v_mul_f32_e32 v6, 0x43000000, v16
	s_waitcnt lgkmcnt(0)
	v_mul_f32_e32 v8, 0x43000000, v18
	v_cvt_pk_fp8_f32 v11, v6, v8 op_sel:[0,0,1]
	v_mul_f32_e32 v5, 0x43000000, v7
	v_mul_f32_e32 v6, 0x43000000, v9
	v_cvt_pk_fp8_f32 v2, v5, v6 op_sel:[0,0,1]
	v_mul_f32_e32 v4, 0x43000000, v13
	v_mul_f32_e32 v5, 0x43000000, v15
	v_mov_b32_e32 v3, v153
	v_cvt_pk_fp8_f32 v3, v4, v5
	v_mul_f32_e32 v6, 0x43000000, v17
	v_mul_f32_e32 v7, 0x43000000, v19
	v_add_u32_e32 v20, s6, v115
	v_cvt_pk_fp8_f32 v3, v6, v7 op_sel:[0,0,1]
	v_add_u32_e32 v4, s6, v116
	v_ashrrev_i32_e32 v21, 31, v20
	v_ashrrev_i32_e32 v5, 31, v4
	v_lshlrev_b64 v[20:21], 10, v[20:21]
	v_lshlrev_b64 v[4:5], 10, v[4:5]
	v_lshl_add_u64 v[20:21], v[0:1], 0, v[20:21]
	v_lshl_add_u64 v[0:1], v[0:1], 0, v[4:5]
	global_store_dwordx2 v[20:21], v[10:11], off nt
	global_store_dwordx2 v[0:1], v[2:3], off nt
	s_waitcnt lgkmcnt(0)
	s_branch .LBB0_661
